# weight conversion items: sink early vmcnt waits and their consumers below the last of the 16 streaming loads (all loads in flight together) in hook/naw/late copies
# speedup vs baseline: 1.2463x; 1.0060x over previous
; #define LAS __attribute__((address_space(3)))
; __device__ __forceinline__ unsigned pk4_fp8(float a, float b, float c, float d) { unsigned w = 0u; w = __builtin_amdgcn_cvt_pk_fp8_f32(a, b, w, false); w = __builtin_amdgcn_cvt_pk_fp8_f32(c, d, w, true); return w; }
; __device__ __forceinline__ void conv_item8(const float* W, int K, int N, unsigned char* WT, int k0, int n0, int drow0, LAS unsigned* scr, int lane, float sc, bool rperm = false) {
;     const int q = lane >> 4, n4 = lane & 15;
;     f32x4 v[4][4];
; #pragma unroll
;     for (int i = 0; i < 4; ++i)
; #pragma unroll
;         for (int t = 0; t < 4; ++t) v[i][t] = __builtin_nontemporal_load((const f32x4*)(W + (size_t)(k0 + 4 * (4 * i + q) + t) * N + n0 + 4 * n4));
; #pragma unroll
;     for (int i = 0; i < 4; ++i) { const int rp = 4 * i + q; LAS unsigned* sp = scr + (4 * n4) * 17 + rp;
;         sp[0]  = pk4_fp8(v[i][0].x * sc, v[i][1].x * sc, v[i][2].x * sc, v[i][3].x * sc);
;         sp[17] = pk4_fp8(v[i][0].y * sc, v[i][1].y * sc, v[i][2].y * sc, v[i][3].y * sc);
;         sp[34] = pk4_fp8(v[i][0].z * sc, v[i][1].z * sc, v[i][2].z * sc, v[i][3].z * sc);
;         sp[51] = pk4_fp8(v[i][0].w * sc, v[i][1].w * sc, v[i][2].w * sc, v[i][3].w * sc); }
; __device__ __forceinline__ void conv_dispatch(const Params& p, int it, LAS unsigned* scr, int lane) {
;     ...
;     { const int e = r / 512, rr = r % 512, kb = rr / 32, nb = rr % 32;
;         conv_item8(p.in[l ? 23 : 12] + (size_t)e * DFF * D, DFF, D, (l ? p.wp[IX_WD1] : p.wp[IX_WD0]) + (size_t)e * D * DFF, kb * 64, nb * 64, nb * 64, scr, lane, F8_SWD); }
.LBB0_157:
	s_movk_i32 s6, 0x4800
	v_cmp_gt_i32_e32 vcc, s6, v67
	s_movk_i32 s6, 0x73ff
	s_nop 0
	v_cndmask_b32_e32 v0, v177, v178, vcc
	v_add_u32_e32 v0, v0, v67
	v_add_u32_e32 v3, 0xffff8c00, v0
	v_cmp_lt_i32_e32 vcc, s6, v0
	s_nop 1
	v_cndmask_b32_e32 v2, v179, v180, vcc
	v_cndmask_b32_e32 v4, v0, v3, vcc
	v_cmp_ge_i32_e64 s[6:7], v4, v2
	s_and_saveexec_b64 s[8:9], s[6:7]
	s_xor_b64 s[8:9], exec, s[8:9]
	s_cbranch_execz .LBB0_167
	v_sub_u32_e32 v5, v4, v2
	s_movk_i32 s6, 0x3ff
	v_cmp_lt_i32_e64 s[6:7], s6, v5
	s_and_saveexec_b64 s[48:49], s[6:7]
	s_xor_b64 s[48:49], exec, s[48:49]
	s_cbranch_execz .LBB0_164
	s_movk_i32 s6, 0x43ff
	v_cmp_lt_u32_e64 s[6:7], s6, v5
	s_and_saveexec_b64 s[50:51], s[6:7]
	s_xor_b64 s[50:51], exec, s[50:51]
	s_cbranch_execz .LBB0_161
	v_cndmask_b32_e32 v162, v181, v182, vcc
	v_lshl_add_u64 v[6:7], s[0:1], 0, v[162:163]
	global_load_dwordx2 v[6:7], v[6:7], off
	v_add_u32_e32 v0, 0xffffbc00, v5
	v_lshrrev_b32_e32 v2, 9, v0
	v_mov_b32_e32 v3, v163
	v_lshlrev_b64 v[8:9], 23, v[2:3]
	v_cndmask_b32_e32 v162, v183, v184, vcc
	v_lshlrev_b32_e32 v0, 1, v4
	v_and_b32_e32 v72, 0x3c0, v0
	v_lshlrev_b32_e32 v0, 6, v4
	v_and_b32_e32 v74, 0x7c0, v0
	v_lshlrev_b64 v[2:3], 21, v[2:3]
	v_mov_b32_e32 v73, v163
	s_waitcnt vmcnt(0)
	v_lshl_add_u64 v[6:7], v[6:7], 0, v[8:9]
	v_lshl_add_u64 v[8:9], s[0:1], 0, v[162:163]
	global_load_dwordx2 v[8:9], v[8:9], off
	v_lshlrev_b32_e32 v162, 2, v74
	s_waitcnt vmcnt(0)
	v_lshl_add_u64 v[70:71], v[8:9], 0, v[2:3]
	v_lshl_add_u64 v[2:3], v[6:7], 0, v[162:163]
	v_lshlrev_b32_e32 v162, 2, v66
	v_lshl_add_u64 v[2:3], v[2:3], 0, v[162:163]
	v_lshl_or_b32 v162, v72, 13, v86
	v_lshl_add_u64 v[18:19], v[2:3], 0, v[162:163]
	v_add_co_u32_e64 v2, s[6:7], s57, v18
	global_load_dwordx4 v[50:53], v[18:19], off nt
	s_nop 0
	v_addc_co_u32_e64 v3, s[6:7], 0, v19, s[6:7]
	s_movk_i32 s6, 0x4000
	global_load_dwordx4 v[54:57], v[2:3], off nt
	v_add_co_u32_e64 v2, s[6:7], s6, v18
	s_nop 1
	v_addc_co_u32_e64 v3, s[6:7], 0, v19, s[6:7]
	s_movk_i32 s6, 0x6000
	global_load_dwordx4 v[58:61], v[2:3], off nt
	v_add_co_u32_e64 v2, s[6:7], s6, v18
	s_nop 1
	v_addc_co_u32_e64 v3, s[6:7], 0, v19, s[6:7]
	s_mov_b32 s6, 0x20000
	global_load_dwordx4 v[62:65], v[2:3], off nt
	v_add_co_u32_e64 v2, s[6:7], s6, v18
	s_nop 1
	v_addc_co_u32_e64 v3, s[6:7], 0, v19, s[6:7]
	s_mov_b32 s6, 0x22000
	global_load_dwordx4 v[34:37], v[2:3], off nt
	v_add_co_u32_e64 v2, s[6:7], s6, v18
	s_nop 1
	v_addc_co_u32_e64 v3, s[6:7], 0, v19, s[6:7]
	s_mov_b32 s6, 0x24000
	global_load_dwordx4 v[38:41], v[2:3], off nt
	v_add_co_u32_e64 v2, s[6:7], s6, v18
	s_nop 0
	s_nop 0
	v_addc_co_u32_e64 v3, s[6:7], 0, v19, s[6:7]
	s_mov_b32 s6, 0x26000
	global_load_dwordx4 v[42:45], v[2:3], off nt
	v_add_co_u32_e64 v2, s[6:7], s6, v18
	s_nop 0
	s_nop 0
	v_addc_co_u32_e64 v3, s[6:7], 0, v19, s[6:7]
	s_mov_b32 s6, 0x40000
	global_load_dwordx4 v[46:49], v[2:3], off nt
	v_add_co_u32_e64 v2, s[6:7], s6, v18
	s_nop 0
	s_nop 0
	v_addc_co_u32_e64 v3, s[6:7], 0, v19, s[6:7]
	s_mov_b32 s6, 0x42000
	s_nop 0
	v_add_co_u32_e64 v6, s[6:7], s6, v18
	global_load_dwordx4 v[2:5], v[2:3], off nt
	s_nop 0
	v_addc_co_u32_e64 v7, s[6:7], 0, v19, s[6:7]
	global_load_dwordx4 v[22:25], v[6:7], off nt
	v_add_co_u32_e64 v6, s[6:7], s72, v18
	s_nop 0
	s_nop 0
	v_addc_co_u32_e64 v7, s[6:7], 0, v19, s[6:7]
	global_load_dwordx4 v[26:29], v[6:7], off nt
	v_add_co_u32_e64 v6, s[6:7], s73, v18
	s_nop 0
	s_nop 0
	v_addc_co_u32_e64 v7, s[6:7], 0, v19, s[6:7]
	global_load_dwordx4 v[30:33], v[6:7], off nt
	v_add_co_u32_e64 v6, s[6:7], s74, v18
	s_nop 0
	s_nop 0
	v_addc_co_u32_e64 v7, s[6:7], 0, v19, s[6:7]
	v_add_co_u32_e64 v10, s[6:7], s75, v18
	global_load_dwordx4 v[6:9], v[6:7], off nt
	s_nop 0
	v_addc_co_u32_e64 v11, s[6:7], 0, v19, s[6:7]
	global_load_dwordx4 v[10:13], v[10:11], off nt
	v_add_co_u32_e64 v14, s[6:7], s76, v18
	s_nop 0
	s_nop 0
	v_addc_co_u32_e64 v15, s[6:7], 0, v19, s[6:7]
	v_add_co_u32_e64 v18, s[6:7], s77, v18
	global_load_dwordx4 v[14:17], v[14:15], off nt
	s_nop 0
	v_addc_co_u32_e64 v19, s[6:7], 0, v19, s[6:7]
	global_load_dwordx4 v[18:21], v[18:19], off nt
	s_waitcnt vmcnt(15)
	v_mul_f32_e32 v0, 0x43800000, v50
	s_waitcnt vmcnt(14)
	v_mul_f32_e32 v50, 0x43800000, v54
	s_waitcnt vmcnt(13)
	v_mul_f32_e32 v54, 0x43800000, v58
	s_waitcnt vmcnt(12)
	v_mul_f32_e32 v58, 0x43800000, v62
	v_mov_b32_e32 v62, v163
	v_cvt_pk_fp8_f32 v62, v0, v50
	v_mul_f32_e32 v0, 0x43800000, v51
	v_mul_f32_e32 v50, 0x43800000, v55
	v_mov_b32_e32 v55, v163
	v_cvt_pk_fp8_f32 v55, v0, v50
	v_cvt_pk_fp8_f32 v62, v54, v58 op_sel:[0,0,1]
	v_mul_f32_e32 v51, 0x43800000, v59
	v_mul_f32_e32 v54, 0x43800000, v63
	v_cvt_pk_fp8_f32 v55, v51, v54 op_sel:[0,0,1]
	v_mul_f32_e32 v0, 0x43800000, v52
	v_mul_f32_e32 v50, 0x43800000, v56
	v_mov_b32_e32 v54, v163
	v_cvt_pk_fp8_f32 v54, v0, v50
	v_mul_f32_e32 v0, 0x43800000, v53
	v_mul_f32_e32 v50, 0x43800000, v57
	v_mov_b32_e32 v53, v163
	v_cvt_pk_fp8_f32 v53, v0, v50
	v_mul_f32_e32 v51, 0x43800000, v60
	s_waitcnt vmcnt(11)
	v_mul_f32_e32 v0, 0x43800000, v34
	v_mul_f32_e32 v52, 0x43800000, v64
	v_cvt_pk_fp8_f32 v54, v51, v52 op_sel:[0,0,1]
	v_mul_f32_e32 v51, 0x43800000, v61
	v_mul_f32_e32 v52, 0x43800000, v65
	v_cvt_pk_fp8_f32 v53, v51, v52 op_sel:[0,0,1]
	s_waitcnt vmcnt(10)
	v_mul_f32_e32 v34, 0x43800000, v38
	s_waitcnt vmcnt(9)
	v_mul_f32_e32 v38, 0x43800000, v42
	s_waitcnt vmcnt(8)
; #define LAS __attribute__((address_space(3)))
; __device__ __forceinline__ unsigned pk4_fp8(float a, float b, float c, float d) { unsigned w = 0u; w = __builtin_amdgcn_cvt_pk_fp8_f32(a, b, w, false); w = __builtin_amdgcn_cvt_pk_fp8_f32(c, d, w, true); return w; }
; __device__ __forceinline__ void conv_item8(const float* W, int K, int N, unsigned char* WT, int k0, int n0, int drow0, LAS unsigned* scr, int lane, float sc, bool rperm = false) {
;     ...
;         for (int t = 0; t < 4; ++t) v[i][t] = __builtin_nontemporal_load((const f32x4*)(W + (size_t)(k0 + 4 * (4 * i + q) + t) * N + n0 + 4 * n4));
; #pragma unroll
;     for (int i = 0; i < 4; ++i) { const int rp = 4 * i + q; LAS unsigned* sp = scr + (4 * n4) * 17 + rp;
;         sp[0]  = pk4_fp8(v[i][0].x * sc, v[i][1].x * sc, v[i][2].x * sc, v[i][3].x * sc);
;         sp[17] = pk4_fp8(v[i][0].y * sc, v[i][1].y * sc, v[i][2].y * sc, v[i][3].y * sc);
;         sp[34] = pk4_fp8(v[i][0].z * sc, v[i][1].z * sc, v[i][2].z * sc, v[i][3].z * sc);
;         sp[51] = pk4_fp8(v[i][0].w * sc, v[i][1].w * sc, v[i][2].w * sc, v[i][3].w * sc); }
;     asm volatile("s_waitcnt lgkmcnt(0)" ::: "memory");
;     const int c = lane & 3;
; #pragma unroll
;     for (int j = 0; j < 4; ++j) {
;         const int n = (lane >> 2) + 16 * j; const LAS unsigned* sp = scr + n * 17 + 4 * c;
;         u32x4 o; o.x = sp[0]; o.y = sp[1]; o.z = sp[2]; o.w = sp[3];
;         const int nr = (rperm && n < 32) ? ((n < 16) ? 2 * n : 2 * (n - 16) + 1) : n;
;         *(u32x4*)(WT + (size_t)(drow0 + nr) * K + k0 + 16 * c) = o;
;     }
;     asm volatile("s_waitcnt lgkmcnt(0)" ::: "memory");
	v_mul_f32_e32 v42, 0x43800000, v46
	v_mov_b32_e32 v46, v163
	v_cvt_pk_fp8_f32 v46, v0, v34
	v_mul_f32_e32 v0, 0x43800000, v35
	v_mul_f32_e32 v34, 0x43800000, v39
	v_mov_b32_e32 v39, v163
	v_cvt_pk_fp8_f32 v39, v0, v34
	v_cvt_pk_fp8_f32 v46, v38, v42 op_sel:[0,0,1]
	v_mul_f32_e32 v35, 0x43800000, v43
	v_mul_f32_e32 v38, 0x43800000, v47
	v_cvt_pk_fp8_f32 v39, v35, v38 op_sel:[0,0,1]
	v_mul_f32_e32 v0, 0x43800000, v36
	v_mul_f32_e32 v34, 0x43800000, v40
	v_mov_b32_e32 v38, v163
	v_cvt_pk_fp8_f32 v38, v0, v34
	v_mul_f32_e32 v0, 0x43800000, v37
	v_mul_f32_e32 v34, 0x43800000, v41
	v_mov_b32_e32 v37, v163
	v_cvt_pk_fp8_f32 v37, v0, v34
	s_waitcnt vmcnt(7)
	v_mul_f32_e32 v0, 0x43800000, v2
	s_waitcnt vmcnt(6)
	v_mul_f32_e32 v2, 0x43800000, v22
	s_waitcnt vmcnt(5)
	v_mul_f32_e32 v22, 0x43800000, v26
	v_mul_f32_e32 v35, 0x43800000, v44
	v_mul_f32_e32 v36, 0x43800000, v48
	s_waitcnt vmcnt(4)
	v_mul_f32_e32 v26, 0x43800000, v30
	v_mov_b32_e32 v30, v163
	v_cvt_pk_fp8_f32 v30, v0, v2
	v_mul_f32_e32 v0, 0x43800000, v3
	v_mul_f32_e32 v2, 0x43800000, v23
	v_mov_b32_e32 v23, v163
	v_cvt_pk_fp8_f32 v23, v0, v2
	v_cvt_pk_fp8_f32 v30, v22, v26 op_sel:[0,0,1]
	v_mul_f32_e32 v3, 0x43800000, v27
	v_mul_f32_e32 v22, 0x43800000, v31
	v_cvt_pk_fp8_f32 v23, v3, v22 op_sel:[0,0,1]
	v_mul_f32_e32 v0, 0x43800000, v4
	v_mul_f32_e32 v2, 0x43800000, v24
	v_mov_b32_e32 v22, v163
	v_cvt_pk_fp8_f32 v22, v0, v2
	v_mul_f32_e32 v0, 0x43800000, v5
	v_mul_f32_e32 v2, 0x43800000, v25
	v_mov_b32_e32 v5, v163
	v_cvt_pk_fp8_f32 v5, v0, v2
	s_waitcnt vmcnt(3)
	v_mul_f32_e32 v0, 0x43800000, v6
	s_waitcnt vmcnt(2)
	v_mul_f32_e32 v2, 0x43800000, v10
	v_mov_b32_e32 v6, v163
	v_cvt_pk_fp8_f32 v6, v0, v2
	v_mul_f32_e32 v3, 0x43800000, v28
	v_mul_f32_e32 v4, 0x43800000, v32
	v_cvt_pk_fp8_f32 v22, v3, v4 op_sel:[0,0,1]
	v_mul_f32_e32 v3, 0x43800000, v29
	v_mul_f32_e32 v4, 0x43800000, v33
	v_cvt_pk_fp8_f32 v5, v3, v4 op_sel:[0,0,1]
	s_waitcnt vmcnt(1)
	v_mul_f32_e32 v3, 0x43800000, v14
	s_waitcnt vmcnt(0)
	v_mul_f32_e32 v4, 0x43800000, v18
	v_cvt_pk_fp8_f32 v6, v3, v4 op_sel:[0,0,1]
	v_mul_f32_e32 v0, 0x43800000, v7
	v_mul_f32_e32 v2, 0x43800000, v11
	v_mul_f32_e32 v3, 0x43800000, v15
	ds_write2_b32 v78, v30, v6 offset0:8 offset1:12
	v_mov_b32_e32 v6, v163
	v_cvt_pk_fp8_f32 v6, v0, v2
	v_mul_f32_e32 v4, 0x43800000, v19
	v_mul_f32_e32 v0, 0x43800000, v8
	v_mul_f32_e32 v2, 0x43800000, v12
	v_cvt_pk_fp8_f32 v6, v3, v4 op_sel:[0,0,1]
	v_mul_f32_e32 v3, 0x43800000, v16
	v_mul_f32_e32 v4, 0x43800000, v20
	v_cvt_pk_fp8_f32 v38, v35, v36 op_sel:[0,0,1]
	ds_write2_b32 v78, v23, v6 offset0:25 offset1:29
	v_mov_b32_e32 v6, v163
	v_cvt_pk_fp8_f32 v6, v0, v2
	v_mul_f32_e32 v0, 0x43800000, v9
	v_mul_f32_e32 v2, 0x43800000, v13
	v_mul_f32_e32 v35, 0x43800000, v45
	v_cvt_pk_fp8_f32 v6, v3, v4 op_sel:[0,0,1]
	v_mul_f32_e32 v36, 0x43800000, v49
	v_mul_f32_e32 v3, 0x43800000, v17
	v_mul_f32_e32 v4, 0x43800000, v21
	ds_write2_b32 v78, v22, v6 offset0:42 offset1:46
	v_mov_b32_e32 v6, v163
	v_cvt_pk_fp8_f32 v6, v0, v2
	v_cvt_pk_fp8_f32 v37, v35, v36 op_sel:[0,0,1]
	ds_write2_b32 v78, v62, v46 offset1:4
	ds_write2_b32 v78, v55, v39 offset0:17 offset1:21
	v_cvt_pk_fp8_f32 v6, v3, v4 op_sel:[0,0,1]
	ds_write2_b32 v78, v54, v38 offset0:34 offset1:38
	ds_write2_b32 v78, v53, v37 offset0:51 offset1:55
	v_lshl_add_u64 v[2:3], v[70:71], 0, v[72:73]
	ds_write2_b32 v78, v5, v6 offset0:59 offset1:63
	s_waitcnt lgkmcnt(0)
	v_add_u32_e32 v0, v80, v81
	v_lshl_add_u64 v[6:7], v[2:3], 0, v[68:69]
	ds_read2_b32 v[2:3], v0 offset1:1
	ds_read2_b32 v[4:5], v0 offset0:2 offset1:3
	v_or_b32_e32 v8, v74, v79
	v_lshlrev_b32_e32 v162, 10, v8
	v_lshl_add_u64 v[8:9], v[6:7], 0, v[162:163]
	s_waitcnt lgkmcnt(0)
	global_store_dwordx4 v[8:9], v[2:5], off
	v_or_b32_e32 v8, v74, v82
	s_nop 0
	v_add_u32_e32 v2, 0x440, v0
	v_add_u32_e32 v4, 0x448, v0
	ds_read2_b32 v[2:3], v2 offset1:1
	ds_read2_b32 v[4:5], v4 offset1:1
	v_lshlrev_b32_e32 v162, 10, v8
	v_lshl_add_u64 v[8:9], v[6:7], 0, v[162:163]
	s_waitcnt lgkmcnt(0)
	global_store_dwordx4 v[8:9], v[2:5], off
	s_nop 1
	v_add_u32_e32 v2, 0x880, v0
	v_add_u32_e32 v4, 0x888, v0
	ds_read2_b32 v[2:3], v2 offset1:1
	ds_read2_b32 v[4:5], v4 offset1:1
	v_or_b32_e32 v8, v74, v83
	v_lshlrev_b32_e32 v162, 10, v8
	v_lshl_add_u64 v[8:9], v[6:7], 0, v[162:163]
	s_waitcnt lgkmcnt(0)
	global_store_dwordx4 v[8:9], v[2:5], off
	s_nop 1
	v_add_u32_e32 v2, 0xcc0, v0
	v_add_u32_e32 v0, 0xcc8, v0
	ds_read2_b32 v[2:3], v2 offset1:1
	ds_read2_b32 v[4:5], v0 offset1:1
	v_or_b32_e32 v0, v74, v84
	v_lshlrev_b32_e32 v162, 10, v0
	v_lshl_add_u64 v[6:7], v[6:7], 0, v[162:163]
	s_waitcnt lgkmcnt(0)
	global_store_dwordx4 v[6:7], v[2:5], off
	s_waitcnt lgkmcnt(0)
; #define LAS __attribute__((address_space(3)))
; __device__ __forceinline__ unsigned pk4_fp8(float a, float b, float c, float d) { unsigned w = 0u; w = __builtin_amdgcn_cvt_pk_fp8_f32(a, b, w, false); w = __builtin_amdgcn_cvt_pk_fp8_f32(c, d, w, true); return w; }
; __device__ __forceinline__ void conv_item8(const float* W, int K, int N, unsigned char* WT, int k0, int n0, int drow0, LAS unsigned* scr, int lane, float sc, bool rperm = false) {
;     const int q = lane >> 4, n4 = lane & 15;
;     f32x4 v[4][4];
; #pragma unroll
;     for (int i = 0; i < 4; ++i)
; #pragma unroll
;         for (int t = 0; t < 4; ++t) v[i][t] = __builtin_nontemporal_load((const f32x4*)(W + (size_t)(k0 + 4 * (4 * i + q) + t) * N + n0 + 4 * n4));
; #pragma unroll
;     for (int i = 0; i < 4; ++i) { const int rp = 4 * i + q; LAS unsigned* sp = scr + (4 * n4) * 17 + rp;
;         sp[0]  = pk4_fp8(v[i][0].x * sc, v[i][1].x * sc, v[i][2].x * sc, v[i][3].x * sc);
;         sp[17] = pk4_fp8(v[i][0].y * sc, v[i][1].y * sc, v[i][2].y * sc, v[i][3].y * sc);
;         sp[34] = pk4_fp8(v[i][0].z * sc, v[i][1].z * sc, v[i][2].z * sc, v[i][3].z * sc);
;         sp[51] = pk4_fp8(v[i][0].w * sc, v[i][1].w * sc, v[i][2].w * sc, v[i][3].w * sc); }
; __device__ __forceinline__ void conv_dispatch(const Params& p, int it, LAS unsigned* scr, int lane) {
;     ...
;     if (r < 2 * I_G) { const int up = r >= I_G; if (up) r -= I_G; const int e = r / 512, rr = r % 512, kb = rr / 16, nb = rr % 16, n0 = nb * 64;
;         conv_item8(p.in[(l ? 21 : 10) + up] + (size_t)e * D * DFF, D, DFF, (l ? p.wp[IX_WGU1] : p.wp[IX_WGU0]) + (size_t)e * 2048 * D, kb * 64, n0, (n0 >> 7) * 256 + (n0 & 127) + up * 128, scr, lane, F8_SW);
;         return; } r -= 2 * I_G;
.LBB0_161:
	s_andn2_saveexec_b64 s[50:51], s[50:51]
	s_cbranch_execz .LBB0_163
	v_cmp_lt_u32_e64 s[6:7], s78, v5
	v_cndmask_b32_e32 v162, v187, v188, vcc
	v_lshl_add_u64 v[6:7], s[0:1], 0, v[162:163]
	v_cndmask_b32_e64 v3, 0, 1, s[6:7]
	v_lshlrev_b32_e32 v162, 3, v3
	v_lshl_add_u64 v[6:7], v[6:7], 0, v[162:163]
	global_load_dwordx2 v[6:7], v[6:7], off
	v_cndmask_b32_e64 v0, v185, v186, s[6:7]
	v_add_u32_e32 v0, v0, v5
	v_lshrrev_b32_e32 v2, 9, v0
	v_mov_b32_e32 v3, v163
	v_lshlrev_b64 v[8:9], 23, v[2:3]
	v_cndmask_b32_e32 v162, v189, v190, vcc
	v_lshlrev_b64 v[2:3], 22, v[2:3]
	v_lshlrev_b32_e32 v5, 6, v0
	v_and_or_b32 v4, v4, s79, v76
	v_mov_b32_e32 v65, v163
	s_waitcnt vmcnt(0)
	v_lshl_add_u64 v[6:7], v[6:7], 0, v[8:9]
	v_lshl_add_u64 v[8:9], s[0:1], 0, v[162:163]
	global_load_dwordx2 v[8:9], v[8:9], off
	s_waitcnt vmcnt(0)
	v_lshl_add_u64 v[62:63], v[8:9], 0, v[2:3]
	v_lshlrev_b32_e32 v2, 2, v0
	v_and_b32_e32 v64, 0x7c0, v2
	v_lshlrev_b32_e32 v2, 7, v0
	v_lshlrev_b32_e32 v0, 8, v0
	v_and_b32_e32 v2, 0x700, v2
	v_and_b32_e32 v3, 64, v5
	v_cndmask_b32_e64 v5, 0, v191, s[6:7]
	v_and_b32_e32 v162, 0xf00, v0
	v_or3_b32 v70, v3, v5, v2
	v_lshl_add_u64 v[2:3], v[6:7], 0, v[162:163]
	v_lshlrev_b32_e32 v162, 2, v66
	v_lshl_add_u64 v[2:3], v[2:3], 0, v[162:163]
	v_lshlrev_b32_e32 v162, 14, v4
	v_lshl_add_u64 v[10:11], v[2:3], 0, v[162:163]
	v_add_co_u32_e64 v2, s[6:7], s57, v10
	global_load_dwordx4 v[50:53], v[10:11], off nt
	s_nop 0
	v_addc_co_u32_e64 v3, s[6:7], 0, v11, s[6:7]
	global_load_dwordx4 v[54:57], v[2:3], off offset:-4096 nt
	global_load_dwordx4 v[58:61], v[2:3], off nt
	s_movk_i32 s6, 0x3000
	v_add_co_u32_e64 v2, s[6:7], s6, v10
	s_nop 1
	v_addc_co_u32_e64 v3, s[6:7], 0, v11, s[6:7]
	global_load_dwordx4 v[72:75], v[2:3], off nt
	v_add_co_u32_e64 v2, s[6:7], s80, v10
	s_nop 1
	v_addc_co_u32_e64 v3, s[6:7], 0, v11, s[6:7]
	global_load_dwordx4 v[34:37], v[2:3], off offset:-4096 nt
	global_load_dwordx4 v[38:41], v[2:3], off nt
	v_add_co_u32_e64 v2, s[6:7], s81, v10
	s_nop 0
	s_nop 0
	v_addc_co_u32_e64 v3, s[6:7], 0, v11, s[6:7]
	global_load_dwordx4 v[42:45], v[2:3], off offset:-4096 nt
	global_load_dwordx4 v[46:49], v[2:3], off nt
	v_add_co_u32_e64 v2, s[6:7], s82, v10
	s_nop 0
	s_nop 0
	v_addc_co_u32_e64 v3, s[6:7], 0, v11, s[6:7]
	global_load_dwordx4 v[18:21], v[2:3], off offset:-4096 nt
	global_load_dwordx4 v[22:25], v[2:3], off nt
	v_add_co_u32_e64 v2, s[6:7], s83, v10
	s_nop 0
	s_nop 0
	v_addc_co_u32_e64 v3, s[6:7], 0, v11, s[6:7]
	global_load_dwordx4 v[26:29], v[2:3], off offset:-4096 nt
	global_load_dwordx4 v[30:33], v[2:3], off nt
	v_add_co_u32_e64 v6, s[6:7], s84, v10
	s_nop 0
	s_nop 0
	v_addc_co_u32_e64 v7, s[6:7], 0, v11, s[6:7]
	v_add_co_u32_e64 v14, s[6:7], s85, v10
	global_load_dwordx4 v[2:5], v[6:7], off offset:-4096 nt
	s_nop 0
	global_load_dwordx4 v[6:9], v[6:7], off nt
	v_addc_co_u32_e64 v15, s[6:7], 0, v11, s[6:7]
	global_load_dwordx4 v[10:13], v[14:15], off offset:-4096 nt
	s_nop 0
	global_load_dwordx4 v[14:17], v[14:15], off nt
	s_waitcnt vmcnt(15)
	v_mul_f32_e32 v0, 0x43800000, v50
	s_waitcnt vmcnt(14)
	v_mul_f32_e32 v50, 0x43800000, v54
	v_cvt_pk_fp8_f32 v65, v0, v50
	v_mul_f32_e32 v0, 0x43800000, v51
	v_mul_f32_e32 v50, 0x43800000, v55
	v_mov_b32_e32 v55, v163
	v_cvt_pk_fp8_f32 v55, v0, v50
	s_waitcnt vmcnt(13)
	v_mul_f32_e32 v54, 0x43800000, v58
	v_mul_f32_e32 v51, 0x43800000, v59
	v_mul_f32_e32 v0, 0x43800000, v52
	v_mul_f32_e32 v50, 0x43800000, v56
	s_waitcnt vmcnt(12)
	v_mul_f32_e32 v58, 0x43800000, v72
	v_cvt_pk_fp8_f32 v65, v54, v58 op_sel:[0,0,1]
	v_mul_f32_e32 v54, 0x43800000, v73
	v_cvt_pk_fp8_f32 v55, v51, v54 op_sel:[0,0,1]
	v_mov_b32_e32 v54, v163
	v_cvt_pk_fp8_f32 v54, v0, v50
	v_mul_f32_e32 v0, 0x43800000, v53
	v_mul_f32_e32 v50, 0x43800000, v57
	v_mov_b32_e32 v53, v163
	v_cvt_pk_fp8_f32 v53, v0, v50
	s_waitcnt vmcnt(11)
	v_mul_f32_e32 v0, 0x43800000, v34
	s_waitcnt vmcnt(10)
	v_mul_f32_e32 v34, 0x43800000, v38
	s_waitcnt vmcnt(9)
	v_mul_f32_e32 v38, 0x43800000, v42
	s_waitcnt vmcnt(8)
	v_mul_f32_e32 v42, 0x43800000, v46
	v_mov_b32_e32 v46, v163
	v_cvt_pk_fp8_f32 v46, v0, v34
	v_mul_f32_e32 v0, 0x43800000, v35
	v_mul_f32_e32 v34, 0x43800000, v39
	v_mov_b32_e32 v39, v163
	v_cvt_pk_fp8_f32 v39, v0, v34
	v_cvt_pk_fp8_f32 v46, v38, v42 op_sel:[0,0,1]
	v_mul_f32_e32 v35, 0x43800000, v43
	v_mul_f32_e32 v38, 0x43800000, v47
	v_cvt_pk_fp8_f32 v39, v35, v38 op_sel:[0,0,1]
	v_mul_f32_e32 v0, 0x43800000, v36
	v_mul_f32_e32 v34, 0x43800000, v40
	v_mov_b32_e32 v38, v163
	v_cvt_pk_fp8_f32 v38, v0, v34
	v_mul_f32_e32 v0, 0x43800000, v37
	v_mul_f32_e32 v34, 0x43800000, v41
	v_mov_b32_e32 v37, v163
	v_cvt_pk_fp8_f32 v37, v0, v34
	s_waitcnt vmcnt(7)
; #define LAS __attribute__((address_space(3)))
; __device__ __forceinline__ unsigned pk4_fp8(float a, float b, float c, float d) { unsigned w = 0u; w = __builtin_amdgcn_cvt_pk_fp8_f32(a, b, w, false); w = __builtin_amdgcn_cvt_pk_fp8_f32(c, d, w, true); return w; }
; __device__ __forceinline__ void conv_item8(const float* W, int K, int N, unsigned char* WT, int k0, int n0, int drow0, LAS unsigned* scr, int lane, float sc, bool rperm = false) {
;     ...
;         for (int t = 0; t < 4; ++t) v[i][t] = __builtin_nontemporal_load((const f32x4*)(W + (size_t)(k0 + 4 * (4 * i + q) + t) * N + n0 + 4 * n4));
; #pragma unroll
;     for (int i = 0; i < 4; ++i) { const int rp = 4 * i + q; LAS unsigned* sp = scr + (4 * n4) * 17 + rp;
;         sp[0]  = pk4_fp8(v[i][0].x * sc, v[i][1].x * sc, v[i][2].x * sc, v[i][3].x * sc);
;         sp[17] = pk4_fp8(v[i][0].y * sc, v[i][1].y * sc, v[i][2].y * sc, v[i][3].y * sc);
;         sp[34] = pk4_fp8(v[i][0].z * sc, v[i][1].z * sc, v[i][2].z * sc, v[i][3].z * sc);
;         sp[51] = pk4_fp8(v[i][0].w * sc, v[i][1].w * sc, v[i][2].w * sc, v[i][3].w * sc); }
;     asm volatile("s_waitcnt lgkmcnt(0)" ::: "memory");
;     const int c = lane & 3;
; #pragma unroll
;     for (int j = 0; j < 4; ++j) {
;         const int n = (lane >> 2) + 16 * j; const LAS unsigned* sp = scr + n * 17 + 4 * c;
;         u32x4 o; o.x = sp[0]; o.y = sp[1]; o.z = sp[2]; o.w = sp[3];
;         const int nr = (rperm && n < 32) ? ((n < 16) ? 2 * n : 2 * (n - 16) + 1) : n;
;         *(u32x4*)(WT + (size_t)(drow0 + nr) * K + k0 + 16 * c) = o;
;     }
;     asm volatile("s_waitcnt lgkmcnt(0)" ::: "memory");
	v_mul_f32_e32 v0, 0x43800000, v18
	s_waitcnt vmcnt(6)
	v_mul_f32_e32 v18, 0x43800000, v22
	s_waitcnt vmcnt(5)
	v_mul_f32_e32 v22, 0x43800000, v26
	s_waitcnt vmcnt(4)
	v_mul_f32_e32 v26, 0x43800000, v30
	v_mov_b32_e32 v30, v163
	v_cvt_pk_fp8_f32 v30, v0, v18
	v_mul_f32_e32 v0, 0x43800000, v19
	v_mul_f32_e32 v19, 0x43800000, v23
	v_mov_b32_e32 v18, v163
	v_cvt_pk_fp8_f32 v18, v0, v19
	v_cvt_pk_fp8_f32 v30, v22, v26 op_sel:[0,0,1]
	v_mul_f32_e32 v22, 0x43800000, v27
	v_mul_f32_e32 v23, 0x43800000, v31
	v_cvt_pk_fp8_f32 v18, v22, v23 op_sel:[0,0,1]
	v_mul_f32_e32 v0, 0x43800000, v20
	v_mul_f32_e32 v19, 0x43800000, v24
	v_mov_b32_e32 v23, v163
	v_cvt_pk_fp8_f32 v23, v0, v19
	v_mul_f32_e32 v20, 0x43800000, v28
	v_mul_f32_e32 v22, 0x43800000, v32
	v_mul_f32_e32 v0, 0x43800000, v21
	v_cvt_pk_fp8_f32 v23, v20, v22 op_sel:[0,0,1]
	v_mul_f32_e32 v20, 0x43800000, v25
	v_mov_b32_e32 v19, v163
	v_cvt_pk_fp8_f32 v19, v0, v20
	s_waitcnt vmcnt(3)
	v_mul_f32_e32 v0, 0x43800000, v2
	s_waitcnt vmcnt(2)
	v_mul_f32_e32 v2, 0x43800000, v6
	s_waitcnt vmcnt(1)
	v_mul_f32_e32 v6, 0x43800000, v10
	s_waitcnt vmcnt(0)
	v_mul_f32_e32 v10, 0x43800000, v14
	v_mov_b32_e32 v14, v163
	v_cvt_pk_fp8_f32 v14, v0, v2
	v_mul_f32_e32 v0, 0x43800000, v3
	v_mul_f32_e32 v2, 0x43800000, v7
	v_mov_b32_e32 v7, v163
	v_cvt_pk_fp8_f32 v7, v0, v2
	v_cvt_pk_fp8_f32 v14, v6, v10 op_sel:[0,0,1]
	v_mul_f32_e32 v3, 0x43800000, v11
	v_mul_f32_e32 v6, 0x43800000, v15
	v_cvt_pk_fp8_f32 v7, v3, v6 op_sel:[0,0,1]
	v_mul_f32_e32 v0, 0x43800000, v4
	v_mul_f32_e32 v2, 0x43800000, v8
	v_mov_b32_e32 v6, v163
	v_cvt_pk_fp8_f32 v6, v0, v2
	v_mul_f32_e32 v0, 0x43800000, v5
	v_mul_f32_e32 v2, 0x43800000, v9
	v_mov_b32_e32 v5, v163
	v_cvt_pk_fp8_f32 v5, v0, v2
	v_mul_f32_e32 v51, 0x43800000, v60
	v_mul_f32_e32 v52, 0x43800000, v74
	v_mul_f32_e32 v35, 0x43800000, v44
	v_mul_f32_e32 v36, 0x43800000, v48
	v_mul_f32_e32 v3, 0x43800000, v12
	v_mul_f32_e32 v4, 0x43800000, v16
	v_cvt_pk_fp8_f32 v54, v51, v52 op_sel:[0,0,1]
	v_mul_f32_e32 v51, 0x43800000, v61
	v_mul_f32_e32 v52, 0x43800000, v75
	v_cvt_pk_fp8_f32 v38, v35, v36 op_sel:[0,0,1]
	v_mul_f32_e32 v35, 0x43800000, v45
	v_mul_f32_e32 v36, 0x43800000, v49
	v_mul_f32_e32 v21, 0x43800000, v29
	v_mul_f32_e32 v22, 0x43800000, v33
	v_cvt_pk_fp8_f32 v6, v3, v4 op_sel:[0,0,1]
	v_mul_f32_e32 v3, 0x43800000, v13
	v_mul_f32_e32 v4, 0x43800000, v17
	v_cvt_pk_fp8_f32 v53, v51, v52 op_sel:[0,0,1]
	v_cvt_pk_fp8_f32 v37, v35, v36 op_sel:[0,0,1]
	v_cvt_pk_fp8_f32 v19, v21, v22 op_sel:[0,0,1]
	v_cvt_pk_fp8_f32 v5, v3, v4 op_sel:[0,0,1]
	ds_write2_b32 v78, v65, v46 offset1:4
	ds_write2_b32 v78, v55, v39 offset0:17 offset1:21
	ds_write2_b32 v78, v54, v38 offset0:34 offset1:38
	ds_write2_b32 v78, v53, v37 offset0:51 offset1:55
	ds_write2_b32 v78, v30, v14 offset0:8 offset1:12
	ds_write2_b32 v78, v18, v7 offset0:25 offset1:29
	ds_write2_b32 v78, v23, v6 offset0:42 offset1:46
	ds_write2_b32 v78, v19, v5 offset0:59 offset1:63
	v_mov_b32_e32 v65, v163
	s_waitcnt lgkmcnt(0)
	v_lshl_add_u64 v[2:3], v[62:63], 0, v[64:65]
	v_add_u32_e32 v0, v80, v81
	v_lshl_add_u64 v[6:7], v[2:3], 0, v[68:69]
	ds_read2_b32 v[2:3], v0 offset1:1
	ds_read2_b32 v[4:5], v0 offset0:2 offset1:3
	v_or_b32_e32 v8, v70, v79
	v_lshlrev_b32_e32 v162, 11, v8
	v_lshl_add_u64 v[8:9], v[6:7], 0, v[162:163]
	s_waitcnt lgkmcnt(0)
	global_store_dwordx4 v[8:9], v[2:5], off
	v_or_b32_e32 v8, v70, v82
	s_nop 0
	v_add_u32_e32 v2, 0x440, v0
	v_add_u32_e32 v4, 0x448, v0
	ds_read2_b32 v[2:3], v2 offset1:1
	ds_read2_b32 v[4:5], v4 offset1:1
	v_lshlrev_b32_e32 v162, 11, v8
	v_lshl_add_u64 v[8:9], v[6:7], 0, v[162:163]
	s_waitcnt lgkmcnt(0)
	global_store_dwordx4 v[8:9], v[2:5], off
	s_nop 1
	v_add_u32_e32 v2, 0x880, v0
	v_add_u32_e32 v4, 0x888, v0
	ds_read2_b32 v[2:3], v2 offset1:1
	ds_read2_b32 v[4:5], v4 offset1:1
	v_or_b32_e32 v8, v70, v83
	v_lshlrev_b32_e32 v162, 11, v8
	v_lshl_add_u64 v[8:9], v[6:7], 0, v[162:163]
	s_waitcnt lgkmcnt(0)
	global_store_dwordx4 v[8:9], v[2:5], off
	s_nop 1
	v_add_u32_e32 v2, 0xcc0, v0
	v_add_u32_e32 v0, 0xcc8, v0
	ds_read2_b32 v[2:3], v2 offset1:1
	ds_read2_b32 v[4:5], v0 offset1:1
	v_or_b32_e32 v0, v70, v84
	v_lshlrev_b32_e32 v162, 11, v0
	v_lshl_add_u64 v[6:7], v[6:7], 0, v[162:163]
	s_waitcnt lgkmcnt(0)
	global_store_dwordx4 v[6:7], v[2:5], off
	s_waitcnt lgkmcnt(0)

; #define LAS __attribute__((address_space(3)))
; __device__ __forceinline__ unsigned pk4_fp8(float a, float b, float c, float d) { unsigned w = 0u; w = __builtin_amdgcn_cvt_pk_fp8_f32(a, b, w, false); w = __builtin_amdgcn_cvt_pk_fp8_f32(c, d, w, true); return w; }
; __device__ __forceinline__ void conv_item8(const float* W, int K, int N, unsigned char* WT, int k0, int n0, int drow0, LAS unsigned* scr, int lane, float sc, bool rperm = false) {
;     const int q = lane >> 4, n4 = lane & 15;
;     f32x4 v[4][4];
; #pragma unroll
;     for (int i = 0; i < 4; ++i)
; #pragma unroll
;         for (int t = 0; t < 4; ++t) v[i][t] = __builtin_nontemporal_load((const f32x4*)(W + (size_t)(k0 + 4 * (4 * i + q) + t) * N + n0 + 4 * n4));
; #pragma unroll
;     for (int i = 0; i < 4; ++i) { const int rp = 4 * i + q; LAS unsigned* sp = scr + (4 * n4) * 17 + rp;
;         sp[0]  = pk4_fp8(v[i][0].x * sc, v[i][1].x * sc, v[i][2].x * sc, v[i][3].x * sc);
;         sp[17] = pk4_fp8(v[i][0].y * sc, v[i][1].y * sc, v[i][2].y * sc, v[i][3].y * sc);
;         sp[34] = pk4_fp8(v[i][0].z * sc, v[i][1].z * sc, v[i][2].z * sc, v[i][3].z * sc);
;         sp[51] = pk4_fp8(v[i][0].w * sc, v[i][1].w * sc, v[i][2].w * sc, v[i][3].w * sc); }
; __device__ __forceinline__ void conv_dispatch(const Params& p, int it, LAS unsigned* scr, int lane) {
;     ...
;     { const int e = r / 512, rr = r % 512, kb = rr / 32, nb = rr % 32;
;         conv_item8(p.in[l ? 23 : 12] + (size_t)e * DFF * D, DFF, D, (l ? p.wp[IX_WD1] : p.wp[IX_WD0]) + (size_t)e * D * DFF, kb * 64, nb * 64, nb * 64, scr, lane, F8_SWD); }
.LBB0_182:
	v_cmp_gt_i32_e32 vcc, s19, v2
	s_nop 1
	v_cndmask_b32_e32 v0, v22, v23, vcc
	v_add_u32_e32 v0, v0, v2
	v_add_u32_e32 v9, 0xffff8c00, v0
	v_cmp_lt_i32_e32 vcc, s36, v0
	s_nop 1
	v_cndmask_b32_e32 v4, v24, v25, vcc
	v_cndmask_b32_e32 v10, v0, v9, vcc
	v_cmp_ge_i32_e64 s[4:5], v10, v4
	s_and_saveexec_b64 s[6:7], s[4:5]
	s_xor_b64 s[12:13], exec, s[6:7]
	s_cbranch_execz .LBB0_192
	v_sub_u32_e32 v11, v10, v4
	v_cmp_lt_i32_e64 s[4:5], s37, v11
	s_and_saveexec_b64 s[6:7], s[4:5]
	s_xor_b64 s[14:15], exec, s[6:7]
	s_cbranch_execz .LBB0_189
	v_cmp_lt_u32_e64 s[4:5], s38, v11
	s_and_saveexec_b64 s[6:7], s[4:5]
	s_xor_b64 s[6:7], exec, s[6:7]
	s_cbranch_execz .LBB0_186
	v_cndmask_b32_e32 v4, v34, v35, vcc
	v_lshl_add_u64 v[12:13], s[0:1], 0, v[4:5]
	global_load_dwordx2 v[12:13], v[12:13], off
	v_cndmask_b32_e32 v4, v36, v37, vcc
	v_lshl_add_u64 v[54:55], s[0:1], 0, v[4:5]
	global_load_dwordx2 v[100:101], v[54:55], off
	v_add_u32_e32 v0, 0xffffbc00, v11
	v_mov_b32_e32 v99, v5
	v_lshlrev_b32_e32 v14, 6, v10
	v_lshrrev_b32_e32 v98, 9, v0
	v_and_b32_e32 v0, 0x7c0, v14
	v_lshlrev_b64 v[14:15], 23, v[98:99]
	v_lshlrev_b32_e32 v11, 1, v10
	v_lshlrev_b32_e32 v4, 2, v0
	v_mov_b32_e32 v9, v5
	v_and_b32_e32 v10, 0x3c0, v11
	v_lshlrev_b64 v[98:99], 21, v[98:99]
	v_mov_b32_e32 v116, v5
	v_mov_b32_e32 v117, v5
	v_mov_b32_e32 v11, v5
	v_mov_b32_e32 v118, v5
	v_mov_b32_e32 v53, v5
	v_mov_b32_e32 v119, v5
	v_mov_b32_e32 v120, v5
	v_mov_b32_e32 v121, v5
	s_waitcnt vmcnt(0)
	v_lshl_add_u64 v[12:13], v[12:13], 0, v[14:15]
	v_lshl_add_u64 v[12:13], v[12:13], 0, v[4:5]
	v_lshl_or_b32 v4, v10, 13, v26
	v_lshl_add_u64 v[12:13], v[12:13], 0, v[8:9]
	v_lshl_add_u64 v[102:103], v[12:13], 0, v[4:5]
	v_add_co_u32_e64 v54, s[4:5], s39, v102
	v_lshl_add_u64 v[114:115], v[100:101], 0, v[98:99]
	s_nop 0
	v_addc_co_u32_e64 v55, s[4:5], 0, v103, s[4:5]
	v_add_co_u32_e64 v58, s[4:5], s40, v102
	v_mov_b32_e32 v4, v5
	s_nop 0
	v_addc_co_u32_e64 v59, s[4:5], 0, v103, s[4:5]
	v_add_co_u32_e64 v62, s[4:5], s41, v102
	s_nop 1
	v_addc_co_u32_e64 v63, s[4:5], 0, v103, s[4:5]
	v_add_co_u32_e64 v66, s[4:5], s3, v102
	global_load_dwordx4 v[12:15], v[102:103], off nt
	s_nop 0
	global_load_dwordx4 v[54:57], v[54:55], off nt
	s_nop 0
	global_load_dwordx4 v[58:61], v[58:59], off nt
	s_nop 0
	global_load_dwordx4 v[62:65], v[62:63], off nt
	v_addc_co_u32_e64 v67, s[4:5], 0, v103, s[4:5]
	v_add_co_u32_e64 v70, s[4:5], s42, v102
	s_nop 1
	v_addc_co_u32_e64 v71, s[4:5], 0, v103, s[4:5]
	v_add_co_u32_e64 v74, s[4:5], s43, v102
	s_nop 1
	v_addc_co_u32_e64 v75, s[4:5], 0, v103, s[4:5]
	v_add_co_u32_e64 v78, s[4:5], s44, v102
	s_nop 0
	s_nop 0
	v_addc_co_u32_e64 v79, s[4:5], 0, v103, s[4:5]
	v_add_co_u32_e64 v82, s[4:5], s45, v102
	global_load_dwordx4 v[66:69], v[66:67], off nt
	s_nop 0
	global_load_dwordx4 v[70:73], v[70:71], off nt
	s_nop 0
	global_load_dwordx4 v[74:77], v[74:75], off nt
	s_nop 0
	global_load_dwordx4 v[78:81], v[78:79], off nt
	v_addc_co_u32_e64 v83, s[4:5], 0, v103, s[4:5]
	v_add_co_u32_e64 v86, s[4:5], s46, v102
	s_nop 0
	s_nop 0
	v_addc_co_u32_e64 v87, s[4:5], 0, v103, s[4:5]
	v_add_co_u32_e64 v90, s[4:5], s47, v102
	s_nop 0
	s_nop 0
	v_addc_co_u32_e64 v91, s[4:5], 0, v103, s[4:5]
	v_add_co_u32_e64 v94, s[4:5], s48, v102
	s_nop 0
	s_nop 0
	v_addc_co_u32_e64 v95, s[4:5], 0, v103, s[4:5]
	v_add_co_u32_e64 v98, s[4:5], s49, v102
	global_load_dwordx4 v[82:85], v[82:83], off nt
	s_nop 0
	global_load_dwordx4 v[86:89], v[86:87], off nt
	s_nop 0
	global_load_dwordx4 v[90:93], v[90:91], off nt
	s_nop 0
	global_load_dwordx4 v[94:97], v[94:95], off nt
	v_addc_co_u32_e64 v99, s[4:5], 0, v103, s[4:5]
	v_add_co_u32_e64 v104, s[4:5], s50, v102
	s_nop 0
	s_nop 0
	v_addc_co_u32_e64 v105, s[4:5], 0, v103, s[4:5]
	v_add_co_u32_e64 v106, s[4:5], s51, v102
	s_nop 0
	s_nop 0
	v_addc_co_u32_e64 v107, s[4:5], 0, v103, s[4:5]
	v_add_co_u32_e64 v110, s[4:5], s52, v102
	s_nop 0
	s_nop 0
	v_addc_co_u32_e64 v111, s[4:5], 0, v103, s[4:5]
	global_load_dwordx4 v[98:101], v[98:99], off nt
	s_nop 0
	global_load_dwordx4 v[102:105], v[104:105], off nt
	s_nop 0
	global_load_dwordx4 v[106:109], v[106:107], off nt
	s_nop 0
	global_load_dwordx4 v[110:113], v[110:111], off nt
	s_waitcnt vmcnt(15)
	v_mul_f32_e32 v12, 0x43800000, v12
	s_waitcnt vmcnt(14)
	v_mul_f32_e32 v54, 0x43800000, v54
	v_mul_f32_e32 v13, 0x43800000, v13
	v_mul_f32_e32 v55, 0x43800000, v55
	v_cvt_pk_fp8_f32 v4, v12, v54
	v_mul_f32_e32 v14, 0x43800000, v14
	v_mul_f32_e32 v56, 0x43800000, v56
	v_cvt_pk_fp8_f32 v9, v13, v55
	v_mul_f32_e32 v15, 0x43800000, v15
	v_mul_f32_e32 v57, 0x43800000, v57
	v_cvt_pk_fp8_f32 v11, v14, v56
	s_waitcnt vmcnt(13)
	v_mul_f32_e32 v58, 0x43800000, v58
	s_waitcnt vmcnt(12)
	v_mul_f32_e32 v62, 0x43800000, v62
	v_cvt_pk_fp8_f32 v53, v15, v57
	v_mul_f32_e32 v59, 0x43800000, v59
	v_mul_f32_e32 v63, 0x43800000, v63
	v_cvt_pk_fp8_f32 v4, v58, v62 op_sel:[0,0,1]
	v_mul_f32_e32 v60, 0x43800000, v60
	v_mul_f32_e32 v64, 0x43800000, v64
	v_cvt_pk_fp8_f32 v9, v59, v63 op_sel:[0,0,1]
	v_mul_f32_e32 v61, 0x43800000, v61
	v_mul_f32_e32 v65, 0x43800000, v65
	v_cvt_pk_fp8_f32 v11, v60, v64 op_sel:[0,0,1]
	v_cvt_pk_fp8_f32 v53, v61, v65 op_sel:[0,0,1]
	v_mov_b32_e32 v12, v5
	v_mov_b32_e32 v15, v5
	v_mov_b32_e32 v54, v5
	v_mov_b32_e32 v55, v5
	s_waitcnt vmcnt(11)
	v_mul_f32_e32 v66, 0x43800000, v66
	s_waitcnt vmcnt(10)
	v_mul_f32_e32 v70, 0x43800000, v70
	v_mul_f32_e32 v67, 0x43800000, v67
	v_mul_f32_e32 v71, 0x43800000, v71
	v_cvt_pk_fp8_f32 v116, v66, v70
	v_mul_f32_e32 v68, 0x43800000, v68
	v_mul_f32_e32 v72, 0x43800000, v72
	v_cvt_pk_fp8_f32 v117, v67, v71
	v_mul_f32_e32 v69, 0x43800000, v69
	v_mul_f32_e32 v73, 0x43800000, v73
	v_cvt_pk_fp8_f32 v118, v68, v72
	s_waitcnt vmcnt(9)
; #define LAS __attribute__((address_space(3)))
; __device__ __forceinline__ unsigned pk4_fp8(float a, float b, float c, float d) { unsigned w = 0u; w = __builtin_amdgcn_cvt_pk_fp8_f32(a, b, w, false); w = __builtin_amdgcn_cvt_pk_fp8_f32(c, d, w, true); return w; }
; __device__ __forceinline__ void conv_item8(const float* W, int K, int N, unsigned char* WT, int k0, int n0, int drow0, LAS unsigned* scr, int lane, float sc, bool rperm = false) {
;     ...
;         for (int t = 0; t < 4; ++t) v[i][t] = __builtin_nontemporal_load((const f32x4*)(W + (size_t)(k0 + 4 * (4 * i + q) + t) * N + n0 + 4 * n4));
; #pragma unroll
;     for (int i = 0; i < 4; ++i) { const int rp = 4 * i + q; LAS unsigned* sp = scr + (4 * n4) * 17 + rp;
;         sp[0]  = pk4_fp8(v[i][0].x * sc, v[i][1].x * sc, v[i][2].x * sc, v[i][3].x * sc);
;         sp[17] = pk4_fp8(v[i][0].y * sc, v[i][1].y * sc, v[i][2].y * sc, v[i][3].y * sc);
;         sp[34] = pk4_fp8(v[i][0].z * sc, v[i][1].z * sc, v[i][2].z * sc, v[i][3].z * sc);
;         sp[51] = pk4_fp8(v[i][0].w * sc, v[i][1].w * sc, v[i][2].w * sc, v[i][3].w * sc); }
;     asm volatile("s_waitcnt lgkmcnt(0)" ::: "memory");
;     const int c = lane & 3;
; #pragma unroll
;     for (int j = 0; j < 4; ++j) {
;         const int n = (lane >> 2) + 16 * j; const LAS unsigned* sp = scr + n * 17 + 4 * c;
;         u32x4 o; o.x = sp[0]; o.y = sp[1]; o.z = sp[2]; o.w = sp[3];
;         const int nr = (rperm && n < 32) ? ((n < 16) ? 2 * n : 2 * (n - 16) + 1) : n;
;         *(u32x4*)(WT + (size_t)(drow0 + nr) * K + k0 + 16 * c) = o;
;     }
;     asm volatile("s_waitcnt lgkmcnt(0)" ::: "memory");
; __device__ __forceinline__ void conv_dispatch(const Params& p, int it, LAS unsigned* scr, int lane) {
;     ...
;     if (r < 2 * I_G) { const int up = r >= I_G; if (up) r -= I_G; const int e = r / 512, rr = r % 512, kb = rr / 16, nb = rr % 16, n0 = nb * 64;
;         conv_item8(p.in[(l ? 21 : 10) + up] + (size_t)e * D * DFF, D, DFF, (l ? p.wp[IX_WGU1] : p.wp[IX_WGU0]) + (size_t)e * 2048 * D, kb * 64, n0, (n0 >> 7) * 256 + (n0 & 127) + up * 128, scr, lane, F8_SW);
	v_mul_f32_e32 v74, 0x43800000, v74
	s_waitcnt vmcnt(8)
	v_mul_f32_e32 v78, 0x43800000, v78
	v_cvt_pk_fp8_f32 v119, v69, v73
	v_mul_f32_e32 v75, 0x43800000, v75
	v_mul_f32_e32 v79, 0x43800000, v79
	v_cvt_pk_fp8_f32 v116, v74, v78 op_sel:[0,0,1]
	v_mul_f32_e32 v76, 0x43800000, v76
	v_mul_f32_e32 v80, 0x43800000, v80
	v_cvt_pk_fp8_f32 v117, v75, v79 op_sel:[0,0,1]
	v_mul_f32_e32 v77, 0x43800000, v77
	v_mul_f32_e32 v81, 0x43800000, v81
	v_cvt_pk_fp8_f32 v118, v76, v80 op_sel:[0,0,1]
	v_cvt_pk_fp8_f32 v119, v77, v81 op_sel:[0,0,1]
	ds_write2_b32 v16, v4, v116 offset1:4
	ds_write2_b32 v16, v9, v117 offset0:17 offset1:21
	ds_write2_b32 v16, v11, v118 offset0:34 offset1:38
	ds_write2_b32 v16, v53, v119 offset0:51 offset1:55
	s_waitcnt vmcnt(7)
	v_mul_f32_e32 v9, 0x43800000, v85
	s_waitcnt vmcnt(6)
	v_mul_f32_e32 v11, 0x43800000, v89
	v_cvt_pk_fp8_f32 v12, v9, v11
	s_waitcnt vmcnt(5)
	v_mul_f32_e32 v9, 0x43800000, v93
	s_waitcnt vmcnt(4)
	v_mul_f32_e32 v11, 0x43800000, v97
	v_mov_b32_e32 v53, v5
	v_cvt_pk_fp8_f32 v12, v9, v11 op_sel:[0,0,1]
	v_mul_f32_e32 v82, 0x43800000, v82
	v_mul_f32_e32 v86, 0x43800000, v86
	v_mul_f32_e32 v83, 0x43800000, v83
	v_mul_f32_e32 v87, 0x43800000, v87
	v_cvt_pk_fp8_f32 v120, v82, v86
	v_mul_f32_e32 v84, 0x43800000, v84
	s_waitcnt vmcnt(3)
	v_mul_f32_e32 v9, 0x43800000, v98
	s_waitcnt vmcnt(2)
	v_mul_f32_e32 v11, 0x43800000, v102
	v_cvt_pk_fp8_f32 v15, v9, v11
	v_mul_f32_e32 v9, 0x43800000, v99
	v_mul_f32_e32 v11, 0x43800000, v103
	v_cvt_pk_fp8_f32 v53, v9, v11
	s_waitcnt vmcnt(1)
	v_mul_f32_e32 v9, 0x43800000, v107
	s_waitcnt vmcnt(0)
	v_mul_f32_e32 v11, 0x43800000, v111
	v_mul_f32_e32 v88, 0x43800000, v88
	v_cvt_pk_fp8_f32 v121, v83, v87
	v_mov_b32_e32 v4, v5
	v_cvt_pk_fp8_f32 v53, v9, v11 op_sel:[0,0,1]
	v_mul_f32_e32 v9, 0x43800000, v100
	v_mul_f32_e32 v11, 0x43800000, v104
	v_cvt_pk_fp8_f32 v4, v84, v88
	v_cvt_pk_fp8_f32 v54, v9, v11
	v_mul_f32_e32 v9, 0x43800000, v101
	v_mul_f32_e32 v11, 0x43800000, v105
	v_mul_f32_e32 v90, 0x43800000, v90
	v_mul_f32_e32 v94, 0x43800000, v94
	v_mul_f32_e32 v13, 0x43800000, v106
	v_mul_f32_e32 v14, 0x43800000, v110
	v_cvt_pk_fp8_f32 v55, v9, v11
	v_mul_f32_e32 v91, 0x43800000, v91
	v_mul_f32_e32 v95, 0x43800000, v95
	v_cvt_pk_fp8_f32 v120, v90, v94 op_sel:[0,0,1]
	v_cvt_pk_fp8_f32 v15, v13, v14 op_sel:[0,0,1]
	v_mul_f32_e32 v92, 0x43800000, v92
	v_mul_f32_e32 v96, 0x43800000, v96
	v_cvt_pk_fp8_f32 v121, v91, v95 op_sel:[0,0,1]
	v_mul_f32_e32 v13, 0x43800000, v108
	v_mul_f32_e32 v14, 0x43800000, v112
	v_cvt_pk_fp8_f32 v4, v92, v96 op_sel:[0,0,1]
	v_cvt_pk_fp8_f32 v54, v13, v14 op_sel:[0,0,1]
	v_mul_f32_e32 v9, 0x43800000, v109
	v_mul_f32_e32 v11, 0x43800000, v113
	v_cvt_pk_fp8_f32 v55, v9, v11 op_sel:[0,0,1]
	ds_write2_b32 v16, v120, v15 offset0:8 offset1:12
	ds_write2_b32 v16, v121, v53 offset0:25 offset1:29
	ds_write2_b32 v16, v4, v54 offset0:42 offset1:46
	ds_write2_b32 v16, v12, v55 offset0:59 offset1:63
	v_mov_b32_e32 v11, v5
	s_waitcnt lgkmcnt(0)
	v_lshl_add_u64 v[10:11], v[114:115], 0, v[10:11]
	v_lshl_add_u64 v[14:15], v[10:11], 0, v[6:7]
	ds_read2_b32 v[10:11], v27 offset1:1
	ds_read2_b32 v[12:13], v27 offset0:2 offset1:3
	v_or_b32_e32 v4, v0, v17
	ds_read2_b32 v[54:55], v28 offset1:1
	ds_read2_b32 v[56:57], v29 offset1:1
	v_lshlrev_b32_e32 v4, 10, v4
	v_lshl_add_u64 v[58:59], v[14:15], 0, v[4:5]
	v_or_b32_e32 v4, v0, v18
	v_lshlrev_b32_e32 v4, 10, v4
	s_waitcnt lgkmcnt(2)
	global_store_dwordx4 v[58:59], v[10:13], off
	s_nop 1
	v_lshl_add_u64 v[10:11], v[14:15], 0, v[4:5]
	s_waitcnt lgkmcnt(0)
	global_store_dwordx4 v[10:11], v[54:57], off
	ds_read2_b32 v[10:11], v30 offset1:1
	ds_read2_b32 v[12:13], v31 offset1:1
	ds_read2_b32 v[54:55], v32 offset1:1
	ds_read2_b32 v[56:57], v33 offset1:1
	v_or_b32_e32 v4, v0, v19
	v_lshlrev_b32_e32 v4, 10, v4
	v_or_b32_e32 v0, v0, v20
	v_lshl_add_u64 v[58:59], v[14:15], 0, v[4:5]
	v_lshlrev_b32_e32 v4, 10, v0
	s_waitcnt lgkmcnt(2)
	global_store_dwordx4 v[58:59], v[10:13], off
	s_nop 1
	v_lshl_add_u64 v[10:11], v[14:15], 0, v[4:5]
	s_waitcnt lgkmcnt(0)
	global_store_dwordx4 v[10:11], v[54:57], off
	s_waitcnt lgkmcnt(0)
.LBB0_186:
	s_andn2_saveexec_b64 s[16:17], s[6:7]
	s_cbranch_execz .LBB0_188
	v_cmp_lt_u32_e64 s[4:5], s53, v11
	v_cndmask_b32_e32 v4, v40, v41, vcc
	v_lshl_add_u64 v[12:13], s[0:1], 0, v[4:5]
	v_cndmask_b32_e64 v4, 0, 1, s[4:5]
	v_lshlrev_b32_e32 v4, 3, v4
	v_lshl_add_u64 v[12:13], v[12:13], 0, v[4:5]
	global_load_dwordx2 v[12:13], v[12:13], off
	v_cndmask_b32_e64 v0, v38, v39, s[4:5]
	v_add_u32_e32 v0, v0, v11
	v_mov_b32_e32 v15, v5
	v_lshrrev_b32_e32 v14, 9, v0
	v_cndmask_b32_e32 v4, v42, v43, vcc
	v_and_or_b32 v53, v10, s54, v1
	v_lshlrev_b32_e32 v56, 8, v0
	v_lshlrev_b64 v[10:11], 23, v[14:15]
	v_lshl_add_u64 v[54:55], s[0:1], 0, v[4:5]
	v_and_b32_e32 v4, 0xf00, v56
	global_load_dwordx2 v[114:115], v[54:55], off
	v_mov_b32_e32 v9, v5
	v_mov_b32_e32 v118, v5
	v_mov_b32_e32 v119, v5
	v_mov_b32_e32 v120, v5
	v_mov_b32_e32 v117, v5
	v_mov_b32_e32 v121, v5
	v_mov_b32_e32 v127, v5
	v_mov_b32_e32 v122, v5
	v_mov_b32_e32 v126, v5
	v_mov_b32_e32 v123, v5
	v_mov_b32_e32 v124, v5
	v_mov_b32_e32 v125, v5
	v_lshlrev_b32_e32 v116, 2, v0
	v_lshlrev_b64 v[14:15], 22, v[14:15]
	v_lshlrev_b32_e32 v129, 6, v0
	v_lshlrev_b32_e32 v0, 7, v0
	v_and_b32_e32 v116, 0x7c0, v116
	v_cndmask_b32_e64 v128, 0, v44, s[4:5]
	v_and_b32_e32 v0, 0x700, v0
	v_and_b32_e32 v129, 64, v129
	v_or3_b32 v0, v129, v128, v0
	s_waitcnt vmcnt(0)
; #define LAS __attribute__((address_space(3)))
; __device__ __forceinline__ unsigned pk4_fp8(float a, float b, float c, float d) { unsigned w = 0u; w = __builtin_amdgcn_cvt_pk_fp8_f32(a, b, w, false); w = __builtin_amdgcn_cvt_pk_fp8_f32(c, d, w, true); return w; }
; __device__ __forceinline__ void conv_item8(const float* W, int K, int N, unsigned char* WT, int k0, int n0, int drow0, LAS unsigned* scr, int lane, float sc, bool rperm = false) {
;     const int q = lane >> 4, n4 = lane & 15;
;     f32x4 v[4][4];
; #pragma unroll
;     for (int i = 0; i < 4; ++i)
; #pragma unroll
;         for (int t = 0; t < 4; ++t) v[i][t] = __builtin_nontemporal_load((const f32x4*)(W + (size_t)(k0 + 4 * (4 * i + q) + t) * N + n0 + 4 * n4));
; #pragma unroll
;     for (int i = 0; i < 4; ++i) { const int rp = 4 * i + q; LAS unsigned* sp = scr + (4 * n4) * 17 + rp;
;         sp[0]  = pk4_fp8(v[i][0].x * sc, v[i][1].x * sc, v[i][2].x * sc, v[i][3].x * sc);
;         sp[17] = pk4_fp8(v[i][0].y * sc, v[i][1].y * sc, v[i][2].y * sc, v[i][3].y * sc);
;         sp[34] = pk4_fp8(v[i][0].z * sc, v[i][1].z * sc, v[i][2].z * sc, v[i][3].z * sc);
;         sp[51] = pk4_fp8(v[i][0].w * sc, v[i][1].w * sc, v[i][2].w * sc, v[i][3].w * sc); }
	v_lshl_add_u64 v[10:11], v[12:13], 0, v[10:11]
	v_lshl_add_u64 v[10:11], v[10:11], 0, v[4:5]
	v_lshlrev_b32_e32 v4, 14, v53
	v_lshl_add_u64 v[10:11], v[10:11], 0, v[8:9]
	v_lshl_add_u64 v[98:99], v[10:11], 0, v[4:5]
	v_add_co_u32_e64 v58, s[6:7], s39, v98
	global_load_dwordx4 v[10:13], v[98:99], off nt
	s_nop 0
	v_addc_co_u32_e64 v59, s[6:7], 0, v99, s[6:7]
	v_add_co_u32_e64 v62, s[6:7], s55, v98
	v_mov_b32_e32 v4, v5
	s_nop 0
	v_addc_co_u32_e64 v63, s[6:7], 0, v99, s[6:7]
	v_add_co_u32_e64 v70, s[6:7], s56, v98
	global_load_dwordx4 v[54:57], v[58:59], off offset:-4096 nt
	s_nop 0
	global_load_dwordx4 v[58:61], v[58:59], off nt
	s_nop 0
	global_load_dwordx4 v[62:65], v[62:63], off nt
	v_addc_co_u32_e64 v71, s[6:7], 0, v99, s[6:7]
	v_add_co_u32_e64 v78, s[6:7], s57, v98
	v_mov_b32_e32 v53, v5
	s_nop 0
	v_addc_co_u32_e64 v79, s[6:7], 0, v99, s[6:7]
	v_add_co_u32_e64 v86, s[6:7], s58, v98
	global_load_dwordx4 v[66:69], v[70:71], off offset:-4096 nt
	s_nop 0
	global_load_dwordx4 v[70:73], v[70:71], off nt
	s_nop 0
	global_load_dwordx4 v[74:77], v[78:79], off offset:-4096 nt
	s_nop 0
	global_load_dwordx4 v[78:81], v[78:79], off nt
	v_addc_co_u32_e64 v87, s[6:7], 0, v99, s[6:7]
	v_add_co_u32_e64 v94, s[6:7], s59, v98
	v_lshl_add_u64 v[14:15], v[114:115], 0, v[14:15]
	s_nop 0
	v_addc_co_u32_e64 v95, s[6:7], 0, v99, s[6:7]
	v_add_co_u32_e64 v102, s[6:7], s61, v98
	global_load_dwordx4 v[82:85], v[86:87], off offset:-4096 nt
	s_nop 0
	global_load_dwordx4 v[86:89], v[86:87], off nt
	s_nop 0
	global_load_dwordx4 v[90:93], v[94:95], off offset:-4096 nt
	s_nop 0
	global_load_dwordx4 v[94:97], v[94:95], off nt
	v_addc_co_u32_e64 v103, s[6:7], 0, v99, s[6:7]
	v_add_co_u32_e64 v110, s[6:7], s62, v98
	s_nop 1
	v_addc_co_u32_e64 v111, s[6:7], 0, v99, s[6:7]
	global_load_dwordx4 v[98:101], v[102:103], off offset:-4096 nt
	s_nop 0
	global_load_dwordx4 v[102:105], v[102:103], off nt
	s_nop 0
	global_load_dwordx4 v[106:109], v[110:111], off offset:-4096 nt
	s_nop 0
	global_load_dwordx4 v[110:113], v[110:111], off nt
	s_waitcnt vmcnt(15)
	v_mul_f32_e32 v10, 0x43800000, v10
	v_mul_f32_e32 v11, 0x43800000, v11
	v_mul_f32_e32 v12, 0x43800000, v12
	v_mul_f32_e32 v13, 0x43800000, v13
	s_waitcnt vmcnt(14)
	v_mul_f32_e32 v54, 0x43800000, v54
	v_mul_f32_e32 v55, 0x43800000, v55
	v_cvt_pk_fp8_f32 v4, v10, v54
	v_mul_f32_e32 v56, 0x43800000, v56
	v_cvt_pk_fp8_f32 v9, v11, v55
	v_mul_f32_e32 v57, 0x43800000, v57
	v_cvt_pk_fp8_f32 v53, v12, v56
	s_waitcnt vmcnt(13)
	v_mul_f32_e32 v58, 0x43800000, v58
	s_waitcnt vmcnt(12)
	v_mul_f32_e32 v62, 0x43800000, v62
	s_waitcnt vmcnt(11)
	v_mul_f32_e32 v66, 0x43800000, v66
	s_waitcnt vmcnt(10)
	v_mul_f32_e32 v70, 0x43800000, v70
	v_mul_f32_e32 v67, 0x43800000, v67
	v_mul_f32_e32 v71, 0x43800000, v71
	v_cvt_pk_fp8_f32 v118, v66, v70
	v_mul_f32_e32 v68, 0x43800000, v68
	v_mul_f32_e32 v72, 0x43800000, v72
	v_cvt_pk_fp8_f32 v119, v67, v71
	v_mul_f32_e32 v69, 0x43800000, v69
	v_mul_f32_e32 v73, 0x43800000, v73
	v_cvt_pk_fp8_f32 v120, v68, v72
	s_waitcnt vmcnt(9)
	v_mul_f32_e32 v74, 0x43800000, v74
	s_waitcnt vmcnt(8)
	v_mul_f32_e32 v78, 0x43800000, v78
	v_cvt_pk_fp8_f32 v117, v13, v57
	v_cvt_pk_fp8_f32 v121, v69, v73
	v_mul_f32_e32 v59, 0x43800000, v59
	v_mul_f32_e32 v63, 0x43800000, v63
	v_mul_f32_e32 v75, 0x43800000, v75
	v_mul_f32_e32 v79, 0x43800000, v79
	v_cvt_pk_fp8_f32 v4, v58, v62 op_sel:[0,0,1]
	v_cvt_pk_fp8_f32 v118, v74, v78 op_sel:[0,0,1]
	v_mul_f32_e32 v60, 0x43800000, v60
	v_mul_f32_e32 v64, 0x43800000, v64
	v_mul_f32_e32 v76, 0x43800000, v76
	v_mul_f32_e32 v80, 0x43800000, v80
	v_cvt_pk_fp8_f32 v9, v59, v63 op_sel:[0,0,1]
	v_cvt_pk_fp8_f32 v119, v75, v79 op_sel:[0,0,1]
	v_mul_f32_e32 v61, 0x43800000, v61
	v_mul_f32_e32 v65, 0x43800000, v65
	v_mul_f32_e32 v77, 0x43800000, v77
	v_mul_f32_e32 v81, 0x43800000, v81
	v_cvt_pk_fp8_f32 v53, v60, v64 op_sel:[0,0,1]
	v_cvt_pk_fp8_f32 v120, v76, v80 op_sel:[0,0,1]
	s_waitcnt vmcnt(7)
; #define LAS __attribute__((address_space(3)))
; __device__ __forceinline__ unsigned pk4_fp8(float a, float b, float c, float d) { unsigned w = 0u; w = __builtin_amdgcn_cvt_pk_fp8_f32(a, b, w, false); w = __builtin_amdgcn_cvt_pk_fp8_f32(c, d, w, true); return w; }
; __device__ __forceinline__ void conv_item8(const float* W, int K, int N, unsigned char* WT, int k0, int n0, int drow0, LAS unsigned* scr, int lane, float sc, bool rperm = false) {
;     ...
;         for (int t = 0; t < 4; ++t) v[i][t] = __builtin_nontemporal_load((const f32x4*)(W + (size_t)(k0 + 4 * (4 * i + q) + t) * N + n0 + 4 * n4));
; #pragma unroll
;     for (int i = 0; i < 4; ++i) { const int rp = 4 * i + q; LAS unsigned* sp = scr + (4 * n4) * 17 + rp;
;         sp[0]  = pk4_fp8(v[i][0].x * sc, v[i][1].x * sc, v[i][2].x * sc, v[i][3].x * sc);
;         sp[17] = pk4_fp8(v[i][0].y * sc, v[i][1].y * sc, v[i][2].y * sc, v[i][3].y * sc);
;         sp[34] = pk4_fp8(v[i][0].z * sc, v[i][1].z * sc, v[i][2].z * sc, v[i][3].z * sc);
;         sp[51] = pk4_fp8(v[i][0].w * sc, v[i][1].w * sc, v[i][2].w * sc, v[i][3].w * sc); }
;     asm volatile("s_waitcnt lgkmcnt(0)" ::: "memory");
;     const int c = lane & 3;
; #pragma unroll
;     for (int j = 0; j < 4; ++j) {
;         const int n = (lane >> 2) + 16 * j; const LAS unsigned* sp = scr + n * 17 + 4 * c;
;         u32x4 o; o.x = sp[0]; o.y = sp[1]; o.z = sp[2]; o.w = sp[3];
;         const int nr = (rperm && n < 32) ? ((n < 16) ? 2 * n : 2 * (n - 16) + 1) : n;
;         *(u32x4*)(WT + (size_t)(drow0 + nr) * K + k0 + 16 * c) = o;
;     }
;     asm volatile("s_waitcnt lgkmcnt(0)" ::: "memory");
	v_mul_f32_e32 v82, 0x43800000, v82
	s_waitcnt vmcnt(6)
	v_mul_f32_e32 v86, 0x43800000, v86
	v_cvt_pk_fp8_f32 v117, v61, v65 op_sel:[0,0,1]
	v_cvt_pk_fp8_f32 v121, v77, v81 op_sel:[0,0,1]
	v_mul_f32_e32 v83, 0x43800000, v83
	v_mul_f32_e32 v87, 0x43800000, v87
	v_cvt_pk_fp8_f32 v122, v82, v86
	ds_write2_b32 v16, v4, v118 offset1:4
	ds_write2_b32 v16, v9, v119 offset0:17 offset1:21
	ds_write2_b32 v16, v53, v120 offset0:34 offset1:38
	ds_write2_b32 v16, v117, v121 offset0:51 offset1:55
	v_mul_f32_e32 v84, 0x43800000, v84
	v_mul_f32_e32 v88, 0x43800000, v88
	v_cvt_pk_fp8_f32 v123, v83, v87
	v_mov_b32_e32 v12, v5
	v_mul_f32_e32 v85, 0x43800000, v85
	v_mul_f32_e32 v89, 0x43800000, v89
	v_cvt_pk_fp8_f32 v124, v84, v88
	v_mov_b32_e32 v13, v5
	s_waitcnt vmcnt(5)
	v_mul_f32_e32 v90, 0x43800000, v90
	s_waitcnt vmcnt(4)
	v_mul_f32_e32 v94, 0x43800000, v94
	v_cvt_pk_fp8_f32 v125, v85, v89
	v_mul_f32_e32 v91, 0x43800000, v91
	v_mul_f32_e32 v95, 0x43800000, v95
	v_cvt_pk_fp8_f32 v122, v90, v94 op_sel:[0,0,1]
	v_mul_f32_e32 v92, 0x43800000, v92
	v_mul_f32_e32 v96, 0x43800000, v96
	v_cvt_pk_fp8_f32 v123, v91, v95 op_sel:[0,0,1]
	v_mul_f32_e32 v93, 0x43800000, v93
	v_mul_f32_e32 v97, 0x43800000, v97
	v_cvt_pk_fp8_f32 v124, v92, v96 op_sel:[0,0,1]
	v_cvt_pk_fp8_f32 v125, v93, v97 op_sel:[0,0,1]
	v_mov_b32_e32 v117, v5
	s_waitcnt vmcnt(3)
	v_mul_f32_e32 v99, 0x43800000, v99
	s_waitcnt vmcnt(2)
	v_mul_f32_e32 v103, 0x43800000, v103
	v_cvt_pk_fp8_f32 v127, v99, v103
	v_mul_f32_e32 v98, 0x43800000, v98
	v_mul_f32_e32 v102, 0x43800000, v102
	v_cvt_pk_fp8_f32 v126, v98, v102
	s_waitcnt vmcnt(1)
	v_mul_f32_e32 v4, 0x43800000, v107
	s_waitcnt vmcnt(0)
	v_mul_f32_e32 v9, 0x43800000, v111
	v_cvt_pk_fp8_f32 v127, v4, v9 op_sel:[0,0,1]
	v_mul_f32_e32 v4, 0x43800000, v100
	v_mul_f32_e32 v9, 0x43800000, v104
	v_cvt_pk_fp8_f32 v12, v4, v9
	v_mul_f32_e32 v4, 0x43800000, v101
	v_mul_f32_e32 v9, 0x43800000, v105
	v_mul_f32_e32 v106, 0x43800000, v106
	v_mul_f32_e32 v110, 0x43800000, v110
	v_cvt_pk_fp8_f32 v13, v4, v9
	v_cvt_pk_fp8_f32 v126, v106, v110 op_sel:[0,0,1]
	v_mul_f32_e32 v10, 0x43800000, v108
	v_mul_f32_e32 v11, 0x43800000, v112
	v_cvt_pk_fp8_f32 v12, v10, v11 op_sel:[0,0,1]
	v_mul_f32_e32 v4, 0x43800000, v109
	v_mul_f32_e32 v9, 0x43800000, v113
	v_cvt_pk_fp8_f32 v13, v4, v9 op_sel:[0,0,1]
	ds_write2_b32 v16, v122, v126 offset0:8 offset1:12
	ds_write2_b32 v16, v123, v127 offset0:25 offset1:29
	ds_write2_b32 v16, v124, v12 offset0:42 offset1:46
	ds_write2_b32 v16, v125, v13 offset0:59 offset1:63
	s_waitcnt lgkmcnt(0)
	v_lshl_add_u64 v[10:11], v[14:15], 0, v[116:117]
	v_lshl_add_u64 v[14:15], v[10:11], 0, v[6:7]
	ds_read2_b32 v[10:11], v27 offset1:1
	ds_read2_b32 v[12:13], v27 offset0:2 offset1:3
	v_or_b32_e32 v4, v0, v17
	ds_read2_b32 v[54:55], v28 offset1:1
	ds_read2_b32 v[56:57], v29 offset1:1
	v_lshlrev_b32_e32 v4, 11, v4
	v_lshl_add_u64 v[58:59], v[14:15], 0, v[4:5]
	v_or_b32_e32 v4, v0, v18
	v_lshlrev_b32_e32 v4, 11, v4
	s_waitcnt lgkmcnt(2)
	global_store_dwordx4 v[58:59], v[10:13], off
	s_nop 1
	v_lshl_add_u64 v[10:11], v[14:15], 0, v[4:5]
	s_waitcnt lgkmcnt(0)
	global_store_dwordx4 v[10:11], v[54:57], off
	ds_read2_b32 v[10:11], v30 offset1:1
	ds_read2_b32 v[12:13], v31 offset1:1
	ds_read2_b32 v[54:55], v32 offset1:1
	ds_read2_b32 v[56:57], v33 offset1:1
	v_or_b32_e32 v4, v0, v19
	v_lshlrev_b32_e32 v4, 11, v4
	v_or_b32_e32 v0, v0, v20
	v_lshl_add_u64 v[58:59], v[14:15], 0, v[4:5]
	v_lshlrev_b32_e32 v4, 11, v0
	s_waitcnt lgkmcnt(2)
	global_store_dwordx4 v[58:59], v[10:13], off
	s_nop 1
	v_lshl_add_u64 v[10:11], v[14:15], 0, v[4:5]
	s_waitcnt lgkmcnt(0)
	global_store_dwordx4 v[10:11], v[54:57], off
	s_waitcnt lgkmcnt(0)

; #define LAS __attribute__((address_space(3)))
; __device__ __forceinline__ unsigned pk4_fp8(float a, float b, float c, float d) { unsigned w = 0u; w = __builtin_amdgcn_cvt_pk_fp8_f32(a, b, w, false); w = __builtin_amdgcn_cvt_pk_fp8_f32(c, d, w, true); return w; }
; __device__ __forceinline__ void conv_item8(const float* W, int K, int N, unsigned char* WT, int k0, int n0, int drow0, LAS unsigned* scr, int lane, float sc, bool rperm = false) {
;     const int q = lane >> 4, n4 = lane & 15;
;     f32x4 v[4][4];
; #pragma unroll
;     for (int i = 0; i < 4; ++i)
; #pragma unroll
;         for (int t = 0; t < 4; ++t) v[i][t] = __builtin_nontemporal_load((const f32x4*)(W + (size_t)(k0 + 4 * (4 * i + q) + t) * N + n0 + 4 * n4));
; #pragma unroll
;     for (int i = 0; i < 4; ++i) { const int rp = 4 * i + q; LAS unsigned* sp = scr + (4 * n4) * 17 + rp;
;         sp[0]  = pk4_fp8(v[i][0].x * sc, v[i][1].x * sc, v[i][2].x * sc, v[i][3].x * sc);
;         sp[17] = pk4_fp8(v[i][0].y * sc, v[i][1].y * sc, v[i][2].y * sc, v[i][3].y * sc);
;         sp[34] = pk4_fp8(v[i][0].z * sc, v[i][1].z * sc, v[i][2].z * sc, v[i][3].z * sc);
;         sp[51] = pk4_fp8(v[i][0].w * sc, v[i][1].w * sc, v[i][2].w * sc, v[i][3].w * sc); }
; __device__ __forceinline__ void conv_dispatch(const Params& p, int it, LAS unsigned* scr, int lane) {
;     ...
;     { const int e = r / 512, rr = r % 512, kb = rr / 32, nb = rr % 32;
;         conv_item8(p.in[l ? 23 : 12] + (size_t)e * DFF * D, DFF, D, (l ? p.wp[IX_WD1] : p.wp[IX_WD0]) + (size_t)e * D * DFF, kb * 64, nb * 64, nb * 64, scr, lane, F8_SWD); }
.LBB0_313:
	v_cmp_lt_i32_e32 vcc, s39, v1
	s_and_saveexec_b64 s[4:5], vcc
	s_xor_b64 s[16:17], exec, s[4:5]
	s_cbranch_execz .LBB0_323
	v_cmp_lt_i32_e32 vcc, s41, v1
	s_and_saveexec_b64 s[4:5], vcc
	s_xor_b64 s[18:19], exec, s[4:5]
	s_cbranch_execz .LBB0_320
	v_add_u32_e32 v2, 0x4c00, v1
	v_cmp_lt_u32_e32 vcc, s43, v2
	s_and_saveexec_b64 s[4:5], vcc
	s_xor_b64 s[4:5], exec, s[4:5]
	s_cbranch_execz .LBB0_317
	v_add_u32_e32 v0, 0x800, v1
	v_lshrrev_b32_e32 v2, 9, v0
	v_lshlrev_b64 v[16:17], 23, v[2:3]
	v_add_u32_e32 v0, 0xb800, v28
	v_lshl_add_u64 v[18:19], s[8:9], 0, v[16:17]
	v_and_b32_e32 v16, 0x3c0, v0
	v_add_u32_e32 v0, 0x170000, v27
	v_and_b32_e32 v0, 0x7c0, v0
	v_lshlrev_b64 v[74:75], 21, v[2:3]
	v_lshlrev_b32_e32 v2, 2, v0
	v_lshl_add_u64 v[18:19], v[18:19], 0, v[2:3]
	v_mov_b32_e32 v15, v3
	v_lshl_add_u64 v[18:19], v[18:19], 0, v[14:15]
	v_lshl_or_b32 v2, v16, 13, v29
	v_lshl_add_u64 v[18:19], v[18:19], 0, v[2:3]
	v_add_co_u32_e32 v46, vcc, s44, v18
	v_lshl_add_u64 v[106:107], s[10:11], 0, v[74:75]
	s_nop 0
	v_addc_co_u32_e32 v47, vcc, 0, v19, vcc
	global_load_dwordx4 v[42:45], v[18:19], off nt
	s_nop 0
	global_load_dwordx4 v[46:49], v[46:47], off nt
	v_add_co_u32_e32 v50, vcc, s45, v18
	s_nop 1
	v_addc_co_u32_e32 v51, vcc, 0, v19, vcc
	v_add_co_u32_e32 v54, vcc, s46, v18
	s_nop 1
	v_addc_co_u32_e32 v55, vcc, 0, v19, vcc
	global_load_dwordx4 v[50:53], v[50:51], off nt
	s_nop 0
	global_load_dwordx4 v[54:57], v[54:55], off nt
	v_add_co_u32_e32 v58, vcc, s47, v18
	s_nop 0
	s_nop 0
	v_addc_co_u32_e32 v59, vcc, 0, v19, vcc
	v_add_co_u32_e32 v62, vcc, s48, v18
	s_nop 0
	s_nop 0
	v_addc_co_u32_e32 v63, vcc, 0, v19, vcc
	global_load_dwordx4 v[58:61], v[58:59], off nt
	s_nop 0
	global_load_dwordx4 v[62:65], v[62:63], off nt
	v_add_co_u32_e32 v66, vcc, s49, v18
	s_nop 1
	v_addc_co_u32_e32 v67, vcc, 0, v19, vcc
	v_add_co_u32_e32 v70, vcc, s50, v18
	s_nop 1
	v_addc_co_u32_e32 v71, vcc, 0, v19, vcc
	global_load_dwordx4 v[66:69], v[66:67], off nt
	s_nop 0
	global_load_dwordx4 v[70:73], v[70:71], off nt
	v_add_co_u32_e32 v74, vcc, s51, v18
	s_nop 1
	v_addc_co_u32_e32 v75, vcc, 0, v19, vcc
	v_add_co_u32_e32 v78, vcc, s52, v18
	s_nop 1
	v_addc_co_u32_e32 v79, vcc, 0, v19, vcc
	global_load_dwordx4 v[74:77], v[74:75], off nt
	s_nop 0
	global_load_dwordx4 v[78:81], v[78:79], off nt
	v_add_co_u32_e32 v82, vcc, s53, v18
	s_nop 1
	v_addc_co_u32_e32 v83, vcc, 0, v19, vcc
	v_add_co_u32_e32 v86, vcc, s54, v18
	s_nop 1
	v_addc_co_u32_e32 v87, vcc, 0, v19, vcc
	global_load_dwordx4 v[82:85], v[82:83], off nt
	s_nop 0
	global_load_dwordx4 v[86:89], v[86:87], off nt
	v_add_co_u32_e32 v90, vcc, s55, v18
	s_nop 1
	v_addc_co_u32_e32 v91, vcc, 0, v19, vcc
	v_add_co_u32_e32 v94, vcc, s56, v18
	s_nop 1
	v_addc_co_u32_e32 v95, vcc, 0, v19, vcc
	global_load_dwordx4 v[90:93], v[90:91], off nt
	s_nop 0
	global_load_dwordx4 v[94:97], v[94:95], off nt
	v_add_co_u32_e32 v98, vcc, s57, v18
	s_nop 1
	v_addc_co_u32_e32 v99, vcc, 0, v19, vcc
	v_add_co_u32_e32 v18, vcc, s58, v18
	s_nop 1
	v_addc_co_u32_e32 v19, vcc, 0, v19, vcc
	global_load_dwordx4 v[98:101], v[98:99], off nt
	s_nop 0
	global_load_dwordx4 v[102:105], v[18:19], off nt
	s_waitcnt vmcnt(15)
	v_mul_f32_e32 v2, 0x43800000, v42
	s_waitcnt vmcnt(14)
	v_mul_f32_e32 v15, 0x43800000, v46
	v_mov_b32_e32 v42, v3
	v_mov_b32_e32 v46, v3
	s_waitcnt vmcnt(13)
	v_mul_f32_e32 v17, 0x43800000, v50
	v_mov_b32_e32 v19, v3
	v_cvt_pk_fp8_f32 v19, v2, v15
	v_mul_f32_e32 v2, 0x43800000, v43
	v_mul_f32_e32 v15, 0x43800000, v47
	v_cvt_pk_fp8_f32 v42, v2, v15
	v_mul_f32_e32 v2, 0x43800000, v51
	s_waitcnt vmcnt(12)
	v_mul_f32_e32 v15, 0x43800000, v55
	v_mov_b32_e32 v43, v3
	v_cvt_pk_fp8_f32 v42, v2, v15 op_sel:[0,0,1]
	v_mul_f32_e32 v2, 0x43800000, v44
	v_mul_f32_e32 v15, 0x43800000, v48
	v_cvt_pk_fp8_f32 v43, v2, v15
	v_mul_f32_e32 v2, 0x43800000, v45
	v_mul_f32_e32 v15, 0x43800000, v49
	v_mov_b32_e32 v44, v3
	v_cvt_pk_fp8_f32 v44, v2, v15
	v_mul_f32_e32 v2, 0x43800000, v53
	v_mul_f32_e32 v15, 0x43800000, v57
	v_mov_b32_e32 v45, v3
	v_cvt_pk_fp8_f32 v44, v2, v15 op_sel:[0,0,1]
	s_waitcnt vmcnt(11)
	v_mul_f32_e32 v2, 0x43800000, v58
	s_waitcnt vmcnt(10)
	v_mul_f32_e32 v15, 0x43800000, v62
	v_cvt_pk_fp8_f32 v45, v2, v15
	v_mul_f32_e32 v2, 0x43800000, v59
	v_mul_f32_e32 v15, 0x43800000, v63
	v_cvt_pk_fp8_f32 v46, v2, v15
	v_mul_f32_e32 v18, 0x43800000, v54
	v_mov_b32_e32 v47, v3
	v_cvt_pk_fp8_f32 v19, v17, v18 op_sel:[0,0,1]
	v_mul_f32_e32 v17, 0x43800000, v52
	v_mul_f32_e32 v18, 0x43800000, v56
	v_mov_b32_e32 v48, v3
	v_cvt_pk_fp8_f32 v43, v17, v18 op_sel:[0,0,1]
	s_waitcnt vmcnt(9)
	v_mul_f32_e32 v2, 0x43800000, v67
	s_waitcnt vmcnt(8)
	v_mul_f32_e32 v15, 0x43800000, v71
	v_cvt_pk_fp8_f32 v46, v2, v15 op_sel:[0,0,1]
	v_mul_f32_e32 v2, 0x43800000, v60
	v_mul_f32_e32 v15, 0x43800000, v64
	v_cvt_pk_fp8_f32 v47, v2, v15
	v_mul_f32_e32 v2, 0x43800000, v61
	v_mul_f32_e32 v15, 0x43800000, v65
	v_mul_f32_e32 v17, 0x43800000, v66
	v_mul_f32_e32 v18, 0x43800000, v70
	v_cvt_pk_fp8_f32 v48, v2, v15
	v_cvt_pk_fp8_f32 v45, v17, v18 op_sel:[0,0,1]
	v_mul_f32_e32 v17, 0x43800000, v68
	v_mul_f32_e32 v18, 0x43800000, v72
	v_cvt_pk_fp8_f32 v47, v17, v18 op_sel:[0,0,1]
	v_mul_f32_e32 v2, 0x43800000, v69
	v_mul_f32_e32 v15, 0x43800000, v73
	v_cvt_pk_fp8_f32 v48, v2, v15 op_sel:[0,0,1]
	ds_write2_b32 v22, v19, v45 offset1:4
	ds_write2_b32 v22, v42, v46 offset0:17 offset1:21
	ds_write2_b32 v22, v43, v47 offset0:34 offset1:38
	ds_write2_b32 v22, v44, v48 offset0:51 offset1:55
	s_waitcnt vmcnt(7)
	v_mul_f32_e32 v2, 0x43800000, v74
	s_waitcnt vmcnt(6)
; #define LAS __attribute__((address_space(3)))
; __device__ __forceinline__ unsigned pk4_fp8(float a, float b, float c, float d) { unsigned w = 0u; w = __builtin_amdgcn_cvt_pk_fp8_f32(a, b, w, false); w = __builtin_amdgcn_cvt_pk_fp8_f32(c, d, w, true); return w; }
; __device__ __forceinline__ void conv_item8(const float* W, int K, int N, unsigned char* WT, int k0, int n0, int drow0, LAS unsigned* scr, int lane, float sc, bool rperm = false) {
;     ...
;         for (int t = 0; t < 4; ++t) v[i][t] = __builtin_nontemporal_load((const f32x4*)(W + (size_t)(k0 + 4 * (4 * i + q) + t) * N + n0 + 4 * n4));
; #pragma unroll
;     for (int i = 0; i < 4; ++i) { const int rp = 4 * i + q; LAS unsigned* sp = scr + (4 * n4) * 17 + rp;
;         sp[0]  = pk4_fp8(v[i][0].x * sc, v[i][1].x * sc, v[i][2].x * sc, v[i][3].x * sc);
;         sp[17] = pk4_fp8(v[i][0].y * sc, v[i][1].y * sc, v[i][2].y * sc, v[i][3].y * sc);
;         sp[34] = pk4_fp8(v[i][0].z * sc, v[i][1].z * sc, v[i][2].z * sc, v[i][3].z * sc);
;         sp[51] = pk4_fp8(v[i][0].w * sc, v[i][1].w * sc, v[i][2].w * sc, v[i][3].w * sc); }
;     asm volatile("s_waitcnt lgkmcnt(0)" ::: "memory");
;     const int c = lane & 3;
; #pragma unroll
;     for (int j = 0; j < 4; ++j) {
;         const int n = (lane >> 2) + 16 * j; const LAS unsigned* sp = scr + n * 17 + 4 * c;
;         u32x4 o; o.x = sp[0]; o.y = sp[1]; o.z = sp[2]; o.w = sp[3];
;         const int nr = (rperm && n < 32) ? ((n < 16) ? 2 * n : 2 * (n - 16) + 1) : n;
;         *(u32x4*)(WT + (size_t)(drow0 + nr) * K + k0 + 16 * c) = o;
;     }
;     asm volatile("s_waitcnt lgkmcnt(0)" ::: "memory");
; __device__ __forceinline__ void conv_dispatch(const Params& p, int it, LAS unsigned* scr, int lane) {
;     ...
;     if (r < 2 * I_G) { const int up = r >= I_G; if (up) r -= I_G; const int e = r / 512, rr = r % 512, kb = rr / 16, nb = rr % 16, n0 = nb * 64;
;         conv_item8(p.in[(l ? 21 : 10) + up] + (size_t)e * D * DFF, D, DFF, (l ? p.wp[IX_WGU1] : p.wp[IX_WGU0]) + (size_t)e * 2048 * D, kb * 64, n0, (n0 >> 7) * 256 + (n0 & 127) + up * 128, scr, lane, F8_SW);
;         return; } r -= 2 * I_G;
	v_mul_f32_e32 v15, 0x43800000, v78
	v_mov_b32_e32 v19, v3
	v_cvt_pk_fp8_f32 v19, v2, v15
	v_mul_f32_e32 v2, 0x43800000, v75
	v_mul_f32_e32 v15, 0x43800000, v79
	v_mov_b32_e32 v42, v3
	v_cvt_pk_fp8_f32 v42, v2, v15
	s_waitcnt vmcnt(5)
	v_mul_f32_e32 v2, 0x43800000, v83
	s_waitcnt vmcnt(4)
	v_mul_f32_e32 v15, 0x43800000, v87
	v_mov_b32_e32 v43, v3
	v_cvt_pk_fp8_f32 v42, v2, v15 op_sel:[0,0,1]
	v_mul_f32_e32 v2, 0x43800000, v76
	v_mul_f32_e32 v15, 0x43800000, v80
	v_cvt_pk_fp8_f32 v43, v2, v15
	v_mul_f32_e32 v2, 0x43800000, v77
	v_mul_f32_e32 v15, 0x43800000, v81
	v_mov_b32_e32 v44, v3
	v_cvt_pk_fp8_f32 v44, v2, v15
	v_mul_f32_e32 v2, 0x43800000, v85
	v_mul_f32_e32 v15, 0x43800000, v89
	v_mov_b32_e32 v45, v3
	v_cvt_pk_fp8_f32 v44, v2, v15 op_sel:[0,0,1]
	s_waitcnt vmcnt(3)
	v_mul_f32_e32 v2, 0x43800000, v90
	s_waitcnt vmcnt(2)
	v_mul_f32_e32 v15, 0x43800000, v94
	v_cvt_pk_fp8_f32 v45, v2, v15
	v_mul_f32_e32 v2, 0x43800000, v91
	v_mul_f32_e32 v15, 0x43800000, v95
	v_mov_b32_e32 v46, v3
	v_cvt_pk_fp8_f32 v46, v2, v15
	s_waitcnt vmcnt(1)
	v_mul_f32_e32 v2, 0x43800000, v99
	s_waitcnt vmcnt(0)
	v_mul_f32_e32 v15, 0x43800000, v103
	v_mul_f32_e32 v17, 0x43800000, v82
	v_mul_f32_e32 v18, 0x43800000, v86
	v_cvt_pk_fp8_f32 v46, v2, v15 op_sel:[0,0,1]
	v_mul_f32_e32 v2, 0x43800000, v92
	v_mul_f32_e32 v15, 0x43800000, v96
	v_mov_b32_e32 v47, v3
	v_cvt_pk_fp8_f32 v19, v17, v18 op_sel:[0,0,1]
	v_mul_f32_e32 v17, 0x43800000, v84
	v_mul_f32_e32 v18, 0x43800000, v88
	v_cvt_pk_fp8_f32 v47, v2, v15
	v_mul_f32_e32 v2, 0x43800000, v93
	v_mul_f32_e32 v15, 0x43800000, v97
	v_mov_b32_e32 v48, v3
	v_cvt_pk_fp8_f32 v43, v17, v18 op_sel:[0,0,1]
	v_mul_f32_e32 v17, 0x43800000, v98
	v_mul_f32_e32 v18, 0x43800000, v102
	v_cvt_pk_fp8_f32 v48, v2, v15
	v_cvt_pk_fp8_f32 v45, v17, v18 op_sel:[0,0,1]
	v_mul_f32_e32 v17, 0x43800000, v100
	v_mul_f32_e32 v18, 0x43800000, v104
	v_cvt_pk_fp8_f32 v47, v17, v18 op_sel:[0,0,1]
	v_mul_f32_e32 v2, 0x43800000, v101
	v_mul_f32_e32 v15, 0x43800000, v105
	v_cvt_pk_fp8_f32 v48, v2, v15 op_sel:[0,0,1]
	ds_write2_b32 v22, v19, v45 offset0:8 offset1:12
	ds_write2_b32 v22, v42, v46 offset0:25 offset1:29
	ds_write2_b32 v22, v43, v47 offset0:42 offset1:46
	ds_write2_b32 v22, v44, v48 offset0:59 offset1:63
	v_mov_b32_e32 v17, v3
	s_waitcnt lgkmcnt(0)
	v_lshl_add_u64 v[16:17], v[106:107], 0, v[16:17]
	v_lshl_add_u64 v[46:47], v[16:17], 0, v[4:5]
	ds_read2_b32 v[16:17], v30 offset1:1
	ds_read2_b32 v[18:19], v30 offset0:2 offset1:3
	v_or_b32_e32 v2, v0, v23
	ds_read2_b32 v[42:43], v31 offset1:1
	ds_read2_b32 v[44:45], v32 offset1:1
	v_lshlrev_b32_e32 v2, 10, v2
	v_lshl_add_u64 v[48:49], v[46:47], 0, v[2:3]
	v_or_b32_e32 v2, v0, v24
	v_lshlrev_b32_e32 v2, 10, v2
	s_waitcnt lgkmcnt(2)
	global_store_dwordx4 v[48:49], v[16:19], off
	s_nop 1
	v_lshl_add_u64 v[16:17], v[46:47], 0, v[2:3]
	s_waitcnt lgkmcnt(0)
	global_store_dwordx4 v[16:17], v[42:45], off
	ds_read2_b32 v[16:17], v33 offset1:1
	ds_read2_b32 v[18:19], v34 offset1:1
	ds_read2_b32 v[42:43], v35 offset1:1
	ds_read2_b32 v[44:45], v36 offset1:1
	v_or_b32_e32 v2, v0, v25
	v_lshlrev_b32_e32 v2, 10, v2
	v_or_b32_e32 v0, v0, v26
	v_lshl_add_u64 v[48:49], v[46:47], 0, v[2:3]
	v_lshlrev_b32_e32 v2, 10, v0
	s_waitcnt lgkmcnt(2)
	global_store_dwordx4 v[48:49], v[16:19], off
	s_nop 1
	v_lshl_add_u64 v[16:17], v[46:47], 0, v[2:3]
	s_waitcnt lgkmcnt(0)
	global_store_dwordx4 v[16:17], v[42:45], off
	s_waitcnt lgkmcnt(0)
.LBB0_317:
	s_andn2_saveexec_b64 s[36:37], s[4:5]
	s_cbranch_execz .LBB0_319
	v_cmp_lt_u32_e32 vcc, s59, v2
	v_mov_b32_e32 v103, v3
	v_and_or_b32 v42, v1, s61, v20
	v_cndmask_b32_e32 v2, v39, v40, vcc
	v_lshl_add_u64 v[16:17], s[0:1], 0, v[2:3]
	global_load_dwordx2 v[16:17], v[16:17], off
	v_cndmask_b32_e32 v0, v37, v38, vcc
	v_add3_u32 v0, v0, v1, s42
	v_lshrrev_b32_e32 v102, 9, v0
	v_lshlrev_b32_e32 v2, 8, v0
	v_lshlrev_b64 v[18:19], 23, v[102:103]
	v_and_b32_e32 v2, 0xf00, v2
	v_mov_b32_e32 v15, v3
	v_mov_b32_e32 v107, v3
	v_mov_b32_e32 v108, v3
	v_mov_b32_e32 v105, v3
	v_mov_b32_e32 v109, v3
	v_mov_b32_e32 v106, v3
	v_mov_b32_e32 v110, v3
	v_mov_b32_e32 v111, v3
	v_mov_b32_e32 v115, v3
	v_mov_b32_e32 v112, v3
	v_mov_b32_e32 v116, v3
	v_mov_b32_e32 v113, v3
	v_mov_b32_e32 v114, v3
	v_lshlrev_b32_e32 v104, 2, v0
	v_lshlrev_b64 v[102:103], 22, v[102:103]
	v_lshlrev_b32_e32 v118, 6, v0
	v_lshlrev_b32_e32 v0, 7, v0
	v_and_b32_e32 v104, 0x7c0, v104
	v_lshl_add_u64 v[102:103], s[12:13], 0, v[102:103]
	v_cndmask_b32_e32 v117, 0, v41, vcc
	v_and_b32_e32 v0, 0x700, v0
	v_and_b32_e32 v118, 64, v118
	v_or3_b32 v0, v118, v117, v0
	s_waitcnt vmcnt(0)
	v_lshl_add_u64 v[16:17], v[16:17], 0, v[18:19]
	v_lshl_add_u64 v[16:17], v[16:17], 0, v[2:3]
	v_lshlrev_b32_e32 v2, 14, v42
	v_lshl_add_u64 v[16:17], v[16:17], 0, v[14:15]
	v_lshl_add_u64 v[86:87], v[16:17], 0, v[2:3]
	v_add_co_u32_e64 v46, s[4:5], s44, v86
	global_load_dwordx4 v[16:19], v[86:87], off nt
	s_nop 0
	v_addc_co_u32_e64 v47, s[4:5], 0, v87, s[4:5]
	v_add_co_u32_e64 v50, s[4:5], s62, v86
	v_mov_b32_e32 v2, v3
	s_nop 0
	v_addc_co_u32_e64 v51, s[4:5], 0, v87, s[4:5]
	v_add_co_u32_e64 v58, s[4:5], s63, v86
	global_load_dwordx4 v[42:45], v[46:47], off offset:-4096 nt
	s_nop 0
	global_load_dwordx4 v[46:49], v[46:47], off nt
	s_nop 0
	global_load_dwordx4 v[50:53], v[50:51], off nt
	v_addc_co_u32_e64 v59, s[4:5], 0, v87, s[4:5]
	v_add_co_u32_e64 v66, s[4:5], s64, v86
	s_nop 1
	v_addc_co_u32_e64 v67, s[4:5], 0, v87, s[4:5]
	v_add_co_u32_e64 v74, s[4:5], s65, v86
	global_load_dwordx4 v[54:57], v[58:59], off offset:-4096 nt
	s_nop 0
	global_load_dwordx4 v[58:61], v[58:59], off nt
	s_nop 0
	global_load_dwordx4 v[62:65], v[66:67], off offset:-4096 nt
	s_nop 0
	global_load_dwordx4 v[66:69], v[66:67], off nt
	v_addc_co_u32_e64 v75, s[4:5], 0, v87, s[4:5]
	v_add_co_u32_e64 v82, s[4:5], s71, v86
	s_nop 1
	v_addc_co_u32_e64 v83, s[4:5], 0, v87, s[4:5]
	v_add_co_u32_e64 v90, s[4:5], s72, v86
	global_load_dwordx4 v[70:73], v[74:75], off offset:-4096 nt
	s_nop 0
	global_load_dwordx4 v[74:77], v[74:75], off nt
	s_nop 0
	global_load_dwordx4 v[78:81], v[82:83], off offset:-4096 nt
	s_nop 0
	global_load_dwordx4 v[82:85], v[82:83], off nt
	v_addc_co_u32_e64 v91, s[4:5], 0, v87, s[4:5]
	v_add_co_u32_e64 v98, s[4:5], s73, v86
	s_nop 0
	s_nop 0
	v_addc_co_u32_e64 v99, s[4:5], 0, v87, s[4:5]
	global_load_dwordx4 v[86:89], v[90:91], off offset:-4096 nt
	s_nop 0
	global_load_dwordx4 v[90:93], v[90:91], off nt
	s_nop 0
	global_load_dwordx4 v[94:97], v[98:99], off offset:-4096 nt
	s_nop 0
	global_load_dwordx4 v[98:101], v[98:99], off nt
	s_waitcnt vmcnt(15)
; #define LAS __attribute__((address_space(3)))
; __device__ __forceinline__ unsigned pk4_fp8(float a, float b, float c, float d) { unsigned w = 0u; w = __builtin_amdgcn_cvt_pk_fp8_f32(a, b, w, false); w = __builtin_amdgcn_cvt_pk_fp8_f32(c, d, w, true); return w; }
; __device__ __forceinline__ void conv_item8(const float* W, int K, int N, unsigned char* WT, int k0, int n0, int drow0, LAS unsigned* scr, int lane, float sc, bool rperm = false) {
;     const int q = lane >> 4, n4 = lane & 15;
;     f32x4 v[4][4];
; #pragma unroll
;     for (int i = 0; i < 4; ++i)
; #pragma unroll
;         for (int t = 0; t < 4; ++t) v[i][t] = __builtin_nontemporal_load((const f32x4*)(W + (size_t)(k0 + 4 * (4 * i + q) + t) * N + n0 + 4 * n4));
; #pragma unroll
;     for (int i = 0; i < 4; ++i) { const int rp = 4 * i + q; LAS unsigned* sp = scr + (4 * n4) * 17 + rp;
;         sp[0]  = pk4_fp8(v[i][0].x * sc, v[i][1].x * sc, v[i][2].x * sc, v[i][3].x * sc);
;         sp[17] = pk4_fp8(v[i][0].y * sc, v[i][1].y * sc, v[i][2].y * sc, v[i][3].y * sc);
;         sp[34] = pk4_fp8(v[i][0].z * sc, v[i][1].z * sc, v[i][2].z * sc, v[i][3].z * sc);
;         sp[51] = pk4_fp8(v[i][0].w * sc, v[i][1].w * sc, v[i][2].w * sc, v[i][3].w * sc); }
;     asm volatile("s_waitcnt lgkmcnt(0)" ::: "memory");
;     const int c = lane & 3;
; #pragma unroll
;     for (int j = 0; j < 4; ++j) {
;         const int n = (lane >> 2) + 16 * j; const LAS unsigned* sp = scr + n * 17 + 4 * c;
;         u32x4 o; o.x = sp[0]; o.y = sp[1]; o.z = sp[2]; o.w = sp[3];
;         const int nr = (rperm && n < 32) ? ((n < 16) ? 2 * n : 2 * (n - 16) + 1) : n;
;         *(u32x4*)(WT + (size_t)(drow0 + nr) * K + k0 + 16 * c) = o;
;     }
;     asm volatile("s_waitcnt lgkmcnt(0)" ::: "memory");
	v_mul_f32_e32 v16, 0x43800000, v16
	s_waitcnt vmcnt(14)
	v_mul_f32_e32 v42, 0x43800000, v42
	v_mul_f32_e32 v17, 0x43800000, v17
	v_mul_f32_e32 v43, 0x43800000, v43
	v_cvt_pk_fp8_f32 v2, v16, v42
	v_mul_f32_e32 v18, 0x43800000, v18
	v_mul_f32_e32 v44, 0x43800000, v44
	v_cvt_pk_fp8_f32 v15, v17, v43
	v_mul_f32_e32 v19, 0x43800000, v19
	v_mul_f32_e32 v45, 0x43800000, v45
	v_cvt_pk_fp8_f32 v105, v18, v44
	s_waitcnt vmcnt(13)
	v_mul_f32_e32 v46, 0x43800000, v46
	s_waitcnt vmcnt(12)
	v_mul_f32_e32 v50, 0x43800000, v50
	v_cvt_pk_fp8_f32 v106, v19, v45
	v_mul_f32_e32 v47, 0x43800000, v47
	v_mul_f32_e32 v51, 0x43800000, v51
	v_cvt_pk_fp8_f32 v2, v46, v50 op_sel:[0,0,1]
	v_mul_f32_e32 v48, 0x43800000, v48
	v_mul_f32_e32 v52, 0x43800000, v52
	v_cvt_pk_fp8_f32 v15, v47, v51 op_sel:[0,0,1]
	v_mul_f32_e32 v49, 0x43800000, v49
	v_mul_f32_e32 v53, 0x43800000, v53
	v_cvt_pk_fp8_f32 v105, v48, v52 op_sel:[0,0,1]
	v_cvt_pk_fp8_f32 v106, v49, v53 op_sel:[0,0,1]
	v_mov_b32_e32 v18, v3
	v_mov_b32_e32 v19, v3
	s_waitcnt vmcnt(11)
	v_mul_f32_e32 v54, 0x43800000, v54
	s_waitcnt vmcnt(10)
	v_mul_f32_e32 v58, 0x43800000, v58
	v_mul_f32_e32 v55, 0x43800000, v55
	v_mul_f32_e32 v59, 0x43800000, v59
	v_cvt_pk_fp8_f32 v107, v54, v58
	v_mul_f32_e32 v56, 0x43800000, v56
	v_mul_f32_e32 v60, 0x43800000, v60
	v_cvt_pk_fp8_f32 v108, v55, v59
	v_mul_f32_e32 v57, 0x43800000, v57
	v_mul_f32_e32 v61, 0x43800000, v61
	v_cvt_pk_fp8_f32 v109, v56, v60
	s_waitcnt vmcnt(9)
	v_mul_f32_e32 v62, 0x43800000, v62
	s_waitcnt vmcnt(8)
	v_mul_f32_e32 v66, 0x43800000, v66
	v_cvt_pk_fp8_f32 v110, v57, v61
	v_mul_f32_e32 v63, 0x43800000, v63
	v_mul_f32_e32 v67, 0x43800000, v67
	v_cvt_pk_fp8_f32 v107, v62, v66 op_sel:[0,0,1]
	v_mul_f32_e32 v64, 0x43800000, v64
	v_mul_f32_e32 v68, 0x43800000, v68
	v_cvt_pk_fp8_f32 v108, v63, v67 op_sel:[0,0,1]
	v_mul_f32_e32 v65, 0x43800000, v65
	v_mul_f32_e32 v69, 0x43800000, v69
	s_waitcnt vmcnt(7)
	v_mul_f32_e32 v70, 0x43800000, v70
	s_waitcnt vmcnt(6)
	v_mul_f32_e32 v74, 0x43800000, v74
	s_waitcnt vmcnt(3)
	v_mul_f32_e32 v86, 0x43800000, v86
	s_waitcnt vmcnt(2)
	v_mul_f32_e32 v90, 0x43800000, v90
	v_cvt_pk_fp8_f32 v109, v64, v68 op_sel:[0,0,1]
	v_mul_f32_e32 v71, 0x43800000, v71
	v_mul_f32_e32 v75, 0x43800000, v75
	v_mul_f32_e32 v87, 0x43800000, v87
	v_mul_f32_e32 v91, 0x43800000, v91
	v_cvt_pk_fp8_f32 v111, v70, v74
	v_cvt_pk_fp8_f32 v115, v86, v90
	v_cvt_pk_fp8_f32 v110, v65, v69 op_sel:[0,0,1]
	v_mul_f32_e32 v72, 0x43800000, v72
	v_mul_f32_e32 v76, 0x43800000, v76
	v_cvt_pk_fp8_f32 v112, v71, v75
	v_cvt_pk_fp8_f32 v116, v87, v91
	ds_write2_b32 v22, v2, v107 offset1:4
	ds_write2_b32 v22, v15, v108 offset0:17 offset1:21
	ds_write2_b32 v22, v105, v109 offset0:34 offset1:38
	ds_write2_b32 v22, v106, v110 offset0:51 offset1:55
	v_mul_f32_e32 v2, 0x43800000, v88
	v_mul_f32_e32 v15, 0x43800000, v92
	v_mul_f32_e32 v73, 0x43800000, v73
	v_mul_f32_e32 v77, 0x43800000, v77
	v_cvt_pk_fp8_f32 v113, v72, v76
	v_cvt_pk_fp8_f32 v18, v2, v15
	v_mul_f32_e32 v2, 0x43800000, v89
	v_mul_f32_e32 v15, 0x43800000, v93
	v_mul_f32_e32 v78, 0x43800000, v78
	v_mul_f32_e32 v82, 0x43800000, v82
	s_waitcnt vmcnt(1)
	v_mul_f32_e32 v94, 0x43800000, v94
	s_waitcnt vmcnt(0)
	v_mul_f32_e32 v98, 0x43800000, v98
	v_cvt_pk_fp8_f32 v114, v73, v77
	v_cvt_pk_fp8_f32 v19, v2, v15
	v_mul_f32_e32 v79, 0x43800000, v79
	v_mul_f32_e32 v83, 0x43800000, v83
	v_mul_f32_e32 v95, 0x43800000, v95
	v_mul_f32_e32 v99, 0x43800000, v99
	v_cvt_pk_fp8_f32 v111, v78, v82 op_sel:[0,0,1]
	v_cvt_pk_fp8_f32 v115, v94, v98 op_sel:[0,0,1]
	v_mul_f32_e32 v80, 0x43800000, v80
	v_mul_f32_e32 v84, 0x43800000, v84
	v_cvt_pk_fp8_f32 v112, v79, v83 op_sel:[0,0,1]
	v_cvt_pk_fp8_f32 v116, v95, v99 op_sel:[0,0,1]
	v_mul_f32_e32 v16, 0x43800000, v96
	v_mul_f32_e32 v17, 0x43800000, v100
	v_mul_f32_e32 v81, 0x43800000, v81
	v_mul_f32_e32 v85, 0x43800000, v85
	v_cvt_pk_fp8_f32 v113, v80, v84 op_sel:[0,0,1]
	v_cvt_pk_fp8_f32 v18, v16, v17 op_sel:[0,0,1]
	v_mul_f32_e32 v2, 0x43800000, v97
	v_mul_f32_e32 v15, 0x43800000, v101
	v_cvt_pk_fp8_f32 v114, v81, v85 op_sel:[0,0,1]
	v_cvt_pk_fp8_f32 v19, v2, v15 op_sel:[0,0,1]
	ds_write2_b32 v22, v111, v115 offset0:8 offset1:12
	ds_write2_b32 v22, v112, v116 offset0:25 offset1:29
	ds_write2_b32 v22, v113, v18 offset0:42 offset1:46
	ds_write2_b32 v22, v114, v19 offset0:59 offset1:63
	v_mov_b32_e32 v105, v3
	s_waitcnt lgkmcnt(0)
	v_lshl_add_u64 v[16:17], v[102:103], 0, v[104:105]
	v_lshl_add_u64 v[46:47], v[16:17], 0, v[4:5]
	ds_read2_b32 v[16:17], v30 offset1:1
	ds_read2_b32 v[18:19], v30 offset0:2 offset1:3
	v_or_b32_e32 v2, v0, v23
	ds_read2_b32 v[42:43], v31 offset1:1
	ds_read2_b32 v[44:45], v32 offset1:1
	v_lshlrev_b32_e32 v2, 11, v2
	v_lshl_add_u64 v[48:49], v[46:47], 0, v[2:3]
	v_or_b32_e32 v2, v0, v24
	v_lshlrev_b32_e32 v2, 11, v2
	s_waitcnt lgkmcnt(2)
	global_store_dwordx4 v[48:49], v[16:19], off
	s_nop 1
	v_lshl_add_u64 v[16:17], v[46:47], 0, v[2:3]
	s_waitcnt lgkmcnt(0)
	global_store_dwordx4 v[16:17], v[42:45], off
	ds_read2_b32 v[16:17], v33 offset1:1
	ds_read2_b32 v[18:19], v34 offset1:1
	ds_read2_b32 v[42:43], v35 offset1:1
	ds_read2_b32 v[44:45], v36 offset1:1
	v_or_b32_e32 v2, v0, v25
	v_lshlrev_b32_e32 v2, 11, v2
	v_or_b32_e32 v0, v0, v26
	v_lshl_add_u64 v[48:49], v[46:47], 0, v[2:3]
	v_lshlrev_b32_e32 v2, 11, v0
	s_waitcnt lgkmcnt(2)
	global_store_dwordx4 v[48:49], v[16:19], off
	s_nop 1
	v_lshl_add_u64 v[16:17], v[46:47], 0, v[2:3]
	s_waitcnt lgkmcnt(0)
	global_store_dwordx4 v[16:17], v[42:45], off
	s_waitcnt lgkmcnt(0)

; #define LAS __attribute__((address_space(3)))
; __device__ __forceinline__ unsigned pk4_fp8(float a, float b, float c, float d) { unsigned w = 0u; w = __builtin_amdgcn_cvt_pk_fp8_f32(a, b, w, false); w = __builtin_amdgcn_cvt_pk_fp8_f32(c, d, w, true); return w; }
; __device__ __forceinline__ void conv_item8(const float* W, int K, int N, unsigned char* WT, int k0, int n0, int drow0, LAS unsigned* scr, int lane, float sc, bool rperm = false) {
;     const int q = lane >> 4, n4 = lane & 15;
;     f32x4 v[4][4];
; #pragma unroll
;     for (int i = 0; i < 4; ++i)
; #pragma unroll
;         for (int t = 0; t < 4; ++t) v[i][t] = __builtin_nontemporal_load((const f32x4*)(W + (size_t)(k0 + 4 * (4 * i + q) + t) * N + n0 + 4 * n4));
; #pragma unroll
;     for (int i = 0; i < 4; ++i) { const int rp = 4 * i + q; LAS unsigned* sp = scr + (4 * n4) * 17 + rp;
;         sp[0]  = pk4_fp8(v[i][0].x * sc, v[i][1].x * sc, v[i][2].x * sc, v[i][3].x * sc);
;         sp[17] = pk4_fp8(v[i][0].y * sc, v[i][1].y * sc, v[i][2].y * sc, v[i][3].y * sc);
;         sp[34] = pk4_fp8(v[i][0].z * sc, v[i][1].z * sc, v[i][2].z * sc, v[i][3].z * sc);
;         sp[51] = pk4_fp8(v[i][0].w * sc, v[i][1].w * sc, v[i][2].w * sc, v[i][3].w * sc); }
; __device__ __forceinline__ void conv_dispatch(const Params& p, int it, LAS unsigned* scr, int lane) {
;     ...
;     if (r < I_OUT) { if (OUT_F8) conv_item8(p.in[l ? 19 : 8], D, D, l ? p.wp[IX_WOUT1] : p.wp[IX_WOUT0], (r / 32) * 64, (r % 32) * 64, (r % 32) * 64, scr, lane, F8_SWD);
;         else conv_item(p.in[l ? 19 : 8], D, D, (bf16_t*)(l ? p.wp[IX_WOUT1] : p.wp[IX_WOUT0]), (r / 32) * 64, (r % 32) * 64, (r % 32) * 64, scr, lane); return; } r -= I_OUT;
.LBB0_320:
	s_andn2_saveexec_b64 s[4:5], s[18:19]
	s_cbranch_execz .LBB0_322
	v_add_u32_e32 v0, 0x9800, v28
	v_and_b32_e32 v16, 0x1ffc0, v0
	v_and_b32_e32 v0, 0x7c0, v27
	v_or_b32_e32 v15, v16, v21
	v_lshlrev_b32_e32 v2, 2, v0
	v_lshl_add_u64 v[18:19], v[6:7], 0, v[2:3]
	v_lshlrev_b32_e32 v2, 13, v15
	v_lshl_add_u64 v[18:19], v[18:19], 0, v[2:3]
	v_add_co_u32_e32 v46, vcc, 0x2000, v18
	s_nop 1
	v_addc_co_u32_e32 v47, vcc, 0, v19, vcc
	global_load_dwordx4 v[42:45], v[18:19], off nt
	s_nop 0
	global_load_dwordx4 v[46:49], v[46:47], off nt
	v_add_co_u32_e32 v50, vcc, 0x4000, v18
	s_nop 1
	v_addc_co_u32_e32 v51, vcc, 0, v19, vcc
	v_add_co_u32_e32 v54, vcc, 0x6000, v18
	s_nop 1
	v_addc_co_u32_e32 v55, vcc, 0, v19, vcc
	global_load_dwordx4 v[50:53], v[50:51], off nt
	s_nop 0
	global_load_dwordx4 v[54:57], v[54:55], off nt
	v_add_co_u32_e32 v58, vcc, 0x20000, v18
	s_nop 0
	s_nop 0
	v_addc_co_u32_e32 v59, vcc, 0, v19, vcc
	v_add_co_u32_e32 v62, vcc, 0x22000, v18
	s_nop 0
	s_nop 0
	v_addc_co_u32_e32 v63, vcc, 0, v19, vcc
	global_load_dwordx4 v[58:61], v[58:59], off nt
	s_nop 0
	global_load_dwordx4 v[62:65], v[62:63], off nt
	v_add_co_u32_e32 v66, vcc, 0x24000, v18
	s_nop 1
	v_addc_co_u32_e32 v67, vcc, 0, v19, vcc
	v_add_co_u32_e32 v70, vcc, 0x26000, v18
	s_nop 1
	v_addc_co_u32_e32 v71, vcc, 0, v19, vcc
	global_load_dwordx4 v[66:69], v[66:67], off nt
	s_nop 0
	global_load_dwordx4 v[70:73], v[70:71], off nt
	v_add_co_u32_e32 v74, vcc, 0x40000, v18
	s_nop 1
	v_addc_co_u32_e32 v75, vcc, 0, v19, vcc
	v_add_co_u32_e32 v78, vcc, 0x42000, v18
	s_nop 1
	v_addc_co_u32_e32 v79, vcc, 0, v19, vcc
	global_load_dwordx4 v[74:77], v[74:75], off nt
	s_nop 0
	global_load_dwordx4 v[78:81], v[78:79], off nt
	v_add_co_u32_e32 v82, vcc, 0x44000, v18
	s_nop 1
	v_addc_co_u32_e32 v83, vcc, 0, v19, vcc
	v_add_co_u32_e32 v86, vcc, 0x46000, v18
	s_nop 1
	v_addc_co_u32_e32 v87, vcc, 0, v19, vcc
	global_load_dwordx4 v[82:85], v[82:83], off nt
	s_nop 0
	global_load_dwordx4 v[86:89], v[86:87], off nt
	v_add_co_u32_e32 v90, vcc, 0x60000, v18
	s_nop 1
	v_addc_co_u32_e32 v91, vcc, 0, v19, vcc
	v_add_co_u32_e32 v94, vcc, 0x62000, v18
	s_nop 1
	v_addc_co_u32_e32 v95, vcc, 0, v19, vcc
	global_load_dwordx4 v[90:93], v[90:91], off nt
	s_nop 0
	global_load_dwordx4 v[94:97], v[94:95], off nt
	v_add_co_u32_e32 v98, vcc, 0x64000, v18
	s_nop 1
	v_addc_co_u32_e32 v99, vcc, 0, v19, vcc
	v_add_co_u32_e32 v18, vcc, 0x66000, v18
	s_nop 1
	v_addc_co_u32_e32 v19, vcc, 0, v19, vcc
	global_load_dwordx4 v[98:101], v[98:99], off nt
	s_nop 0
	global_load_dwordx4 v[102:105], v[18:19], off nt
	s_waitcnt vmcnt(15)
	v_mul_f32_e32 v2, 0x43800000, v42
	s_waitcnt vmcnt(14)
	v_mul_f32_e32 v15, 0x43800000, v46
	v_mov_b32_e32 v42, v3
	v_mov_b32_e32 v46, v3
	s_waitcnt vmcnt(13)
	v_mul_f32_e32 v17, 0x43800000, v50
	v_mov_b32_e32 v19, v3
	v_cvt_pk_fp8_f32 v19, v2, v15
	v_mul_f32_e32 v2, 0x43800000, v43
	v_mul_f32_e32 v15, 0x43800000, v47
	v_cvt_pk_fp8_f32 v42, v2, v15
	v_mul_f32_e32 v2, 0x43800000, v51
	s_waitcnt vmcnt(12)
	v_mul_f32_e32 v15, 0x43800000, v55
	v_mov_b32_e32 v43, v3
	v_cvt_pk_fp8_f32 v42, v2, v15 op_sel:[0,0,1]
	v_mul_f32_e32 v2, 0x43800000, v44
	v_mul_f32_e32 v15, 0x43800000, v48
	v_cvt_pk_fp8_f32 v43, v2, v15
	v_mul_f32_e32 v2, 0x43800000, v45
	v_mul_f32_e32 v15, 0x43800000, v49
	v_mov_b32_e32 v44, v3
	v_cvt_pk_fp8_f32 v44, v2, v15
	v_mul_f32_e32 v2, 0x43800000, v53
	v_mul_f32_e32 v15, 0x43800000, v57
	v_mov_b32_e32 v45, v3
	v_cvt_pk_fp8_f32 v44, v2, v15 op_sel:[0,0,1]
	s_waitcnt vmcnt(11)
	v_mul_f32_e32 v2, 0x43800000, v58
	s_waitcnt vmcnt(10)
	v_mul_f32_e32 v15, 0x43800000, v62
	v_cvt_pk_fp8_f32 v45, v2, v15
	v_mul_f32_e32 v2, 0x43800000, v59
	v_mul_f32_e32 v15, 0x43800000, v63
	v_cvt_pk_fp8_f32 v46, v2, v15
	v_mul_f32_e32 v18, 0x43800000, v54
	v_mov_b32_e32 v47, v3
	v_cvt_pk_fp8_f32 v19, v17, v18 op_sel:[0,0,1]
	v_mul_f32_e32 v17, 0x43800000, v52
	v_mul_f32_e32 v18, 0x43800000, v56
	v_mov_b32_e32 v48, v3
	v_cvt_pk_fp8_f32 v43, v17, v18 op_sel:[0,0,1]
	s_waitcnt vmcnt(9)
	v_mul_f32_e32 v2, 0x43800000, v67
	s_waitcnt vmcnt(8)
; #define LAS __attribute__((address_space(3)))
; __device__ __forceinline__ unsigned pk4_fp8(float a, float b, float c, float d) { unsigned w = 0u; w = __builtin_amdgcn_cvt_pk_fp8_f32(a, b, w, false); w = __builtin_amdgcn_cvt_pk_fp8_f32(c, d, w, true); return w; }
; __device__ __forceinline__ void conv_item8(const float* W, int K, int N, unsigned char* WT, int k0, int n0, int drow0, LAS unsigned* scr, int lane, float sc, bool rperm = false) {
;     ...
;         for (int t = 0; t < 4; ++t) v[i][t] = __builtin_nontemporal_load((const f32x4*)(W + (size_t)(k0 + 4 * (4 * i + q) + t) * N + n0 + 4 * n4));
; #pragma unroll
;     for (int i = 0; i < 4; ++i) { const int rp = 4 * i + q; LAS unsigned* sp = scr + (4 * n4) * 17 + rp;
;         sp[0]  = pk4_fp8(v[i][0].x * sc, v[i][1].x * sc, v[i][2].x * sc, v[i][3].x * sc);
;         sp[17] = pk4_fp8(v[i][0].y * sc, v[i][1].y * sc, v[i][2].y * sc, v[i][3].y * sc);
;         sp[34] = pk4_fp8(v[i][0].z * sc, v[i][1].z * sc, v[i][2].z * sc, v[i][3].z * sc);
;         sp[51] = pk4_fp8(v[i][0].w * sc, v[i][1].w * sc, v[i][2].w * sc, v[i][3].w * sc); }
;     asm volatile("s_waitcnt lgkmcnt(0)" ::: "memory");
;     const int c = lane & 3;
; #pragma unroll
;     for (int j = 0; j < 4; ++j) {
;         const int n = (lane >> 2) + 16 * j; const LAS unsigned* sp = scr + n * 17 + 4 * c;
;         u32x4 o; o.x = sp[0]; o.y = sp[1]; o.z = sp[2]; o.w = sp[3];
;         const int nr = (rperm && n < 32) ? ((n < 16) ? 2 * n : 2 * (n - 16) + 1) : n;
;         *(u32x4*)(WT + (size_t)(drow0 + nr) * K + k0 + 16 * c) = o;
;     }
;     asm volatile("s_waitcnt lgkmcnt(0)" ::: "memory");
	v_mul_f32_e32 v15, 0x43800000, v71
	v_cvt_pk_fp8_f32 v46, v2, v15 op_sel:[0,0,1]
	v_mul_f32_e32 v2, 0x43800000, v60
	v_mul_f32_e32 v15, 0x43800000, v64
	v_cvt_pk_fp8_f32 v47, v2, v15
	v_mul_f32_e32 v2, 0x43800000, v61
	v_mul_f32_e32 v15, 0x43800000, v65
	v_mul_f32_e32 v17, 0x43800000, v66
	v_mul_f32_e32 v18, 0x43800000, v70
	v_cvt_pk_fp8_f32 v48, v2, v15
	v_cvt_pk_fp8_f32 v45, v17, v18 op_sel:[0,0,1]
	v_mul_f32_e32 v17, 0x43800000, v68
	v_mul_f32_e32 v18, 0x43800000, v72
	v_cvt_pk_fp8_f32 v47, v17, v18 op_sel:[0,0,1]
	v_mul_f32_e32 v2, 0x43800000, v69
	v_mul_f32_e32 v15, 0x43800000, v73
	v_cvt_pk_fp8_f32 v48, v2, v15 op_sel:[0,0,1]
	ds_write2_b32 v22, v19, v45 offset1:4
	ds_write2_b32 v22, v42, v46 offset0:17 offset1:21
	ds_write2_b32 v22, v43, v47 offset0:34 offset1:38
	ds_write2_b32 v22, v44, v48 offset0:51 offset1:55
	s_waitcnt vmcnt(7)
	v_mul_f32_e32 v2, 0x43800000, v74
	s_waitcnt vmcnt(6)
	v_mul_f32_e32 v15, 0x43800000, v78
	v_mov_b32_e32 v19, v3
	v_cvt_pk_fp8_f32 v19, v2, v15
	v_mul_f32_e32 v2, 0x43800000, v75
	v_mul_f32_e32 v15, 0x43800000, v79
	v_mov_b32_e32 v42, v3
	v_cvt_pk_fp8_f32 v42, v2, v15
	s_waitcnt vmcnt(5)
	v_mul_f32_e32 v2, 0x43800000, v83
	s_waitcnt vmcnt(4)
	v_mul_f32_e32 v15, 0x43800000, v87
	v_mov_b32_e32 v43, v3
	v_cvt_pk_fp8_f32 v42, v2, v15 op_sel:[0,0,1]
	v_mul_f32_e32 v2, 0x43800000, v76
	v_mul_f32_e32 v15, 0x43800000, v80
	v_cvt_pk_fp8_f32 v43, v2, v15
	v_mul_f32_e32 v2, 0x43800000, v77
	v_mul_f32_e32 v15, 0x43800000, v81
	v_mov_b32_e32 v44, v3
	v_cvt_pk_fp8_f32 v44, v2, v15
	v_mul_f32_e32 v2, 0x43800000, v85
	v_mul_f32_e32 v15, 0x43800000, v89
	v_mov_b32_e32 v45, v3
	v_cvt_pk_fp8_f32 v44, v2, v15 op_sel:[0,0,1]
	s_waitcnt vmcnt(3)
	v_mul_f32_e32 v2, 0x43800000, v90
	s_waitcnt vmcnt(2)
	v_mul_f32_e32 v15, 0x43800000, v94
	v_cvt_pk_fp8_f32 v45, v2, v15
	v_mul_f32_e32 v2, 0x43800000, v91
	v_mul_f32_e32 v15, 0x43800000, v95
	v_mov_b32_e32 v46, v3
	v_cvt_pk_fp8_f32 v46, v2, v15
	s_waitcnt vmcnt(1)
	v_mul_f32_e32 v2, 0x43800000, v99
	s_waitcnt vmcnt(0)
	v_mul_f32_e32 v15, 0x43800000, v103
	v_mul_f32_e32 v17, 0x43800000, v82
	v_mul_f32_e32 v18, 0x43800000, v86
	v_cvt_pk_fp8_f32 v46, v2, v15 op_sel:[0,0,1]
	v_mul_f32_e32 v2, 0x43800000, v92
	v_mul_f32_e32 v15, 0x43800000, v96
	v_mov_b32_e32 v47, v3
	v_cvt_pk_fp8_f32 v19, v17, v18 op_sel:[0,0,1]
	v_mul_f32_e32 v17, 0x43800000, v84
	v_mul_f32_e32 v18, 0x43800000, v88
	v_cvt_pk_fp8_f32 v47, v2, v15
	v_mul_f32_e32 v2, 0x43800000, v93
	v_mul_f32_e32 v15, 0x43800000, v97
	v_mov_b32_e32 v48, v3
	v_cvt_pk_fp8_f32 v43, v17, v18 op_sel:[0,0,1]
	v_mul_f32_e32 v17, 0x43800000, v98
	v_mul_f32_e32 v18, 0x43800000, v102
	v_cvt_pk_fp8_f32 v48, v2, v15
	v_cvt_pk_fp8_f32 v45, v17, v18 op_sel:[0,0,1]
	v_mul_f32_e32 v17, 0x43800000, v100
	v_mul_f32_e32 v18, 0x43800000, v104
	v_cvt_pk_fp8_f32 v47, v17, v18 op_sel:[0,0,1]
	v_mul_f32_e32 v2, 0x43800000, v101
	v_mul_f32_e32 v15, 0x43800000, v105
	v_cvt_pk_fp8_f32 v48, v2, v15 op_sel:[0,0,1]
	ds_write2_b32 v22, v19, v45 offset0:8 offset1:12
	ds_write2_b32 v22, v42, v46 offset0:25 offset1:29
	ds_write2_b32 v22, v43, v47 offset0:42 offset1:46
	ds_write2_b32 v22, v44, v48 offset0:59 offset1:63
	s_waitcnt lgkmcnt(0)
	v_mov_b32_e32 v17, v3
	v_lshl_add_u64 v[46:47], v[8:9], 0, v[16:17]
	ds_read2_b32 v[16:17], v30 offset1:1
	ds_read2_b32 v[18:19], v30 offset0:2 offset1:3
	v_or_b32_e32 v2, v0, v23
	ds_read2_b32 v[42:43], v31 offset1:1
	ds_read2_b32 v[44:45], v32 offset1:1
	v_lshlrev_b32_e32 v2, 11, v2
	v_lshl_add_u64 v[48:49], v[46:47], 0, v[2:3]
	v_or_b32_e32 v2, v0, v24
	v_lshlrev_b32_e32 v2, 11, v2
	s_waitcnt lgkmcnt(2)
	global_store_dwordx4 v[48:49], v[16:19], off
	s_nop 1
	v_lshl_add_u64 v[16:17], v[46:47], 0, v[2:3]
	s_waitcnt lgkmcnt(0)
	global_store_dwordx4 v[16:17], v[42:45], off
	ds_read2_b32 v[16:17], v33 offset1:1
	ds_read2_b32 v[18:19], v34 offset1:1
	ds_read2_b32 v[42:43], v35 offset1:1
	ds_read2_b32 v[44:45], v36 offset1:1
	v_or_b32_e32 v2, v0, v25
	v_lshlrev_b32_e32 v2, 11, v2
	v_or_b32_e32 v0, v0, v26
	v_lshl_add_u64 v[48:49], v[46:47], 0, v[2:3]
	v_lshlrev_b32_e32 v2, 11, v0
	s_waitcnt lgkmcnt(2)
	global_store_dwordx4 v[48:49], v[16:19], off
	s_nop 1
	v_lshl_add_u64 v[16:17], v[46:47], 0, v[2:3]
	s_waitcnt lgkmcnt(0)
	global_store_dwordx4 v[16:17], v[42:45], off
	s_waitcnt lgkmcnt(0)

; #define LAS __attribute__((address_space(3)))
; __device__ __forceinline__ unsigned pk4_fp8(float a, float b, float c, float d) { unsigned w = 0u; w = __builtin_amdgcn_cvt_pk_fp8_f32(a, b, w, false); w = __builtin_amdgcn_cvt_pk_fp8_f32(c, d, w, true); return w; }
; __device__ __forceinline__ void conv_item8(const float* W, int K, int N, unsigned char* WT, int k0, int n0, int drow0, LAS unsigned* scr, int lane, float sc, bool rperm = false) {
;     const int q = lane >> 4, n4 = lane & 15;
;     f32x4 v[4][4];
; #pragma unroll
;     for (int i = 0; i < 4; ++i)
; #pragma unroll
;         for (int t = 0; t < 4; ++t) v[i][t] = __builtin_nontemporal_load((const f32x4*)(W + (size_t)(k0 + 4 * (4 * i + q) + t) * N + n0 + 4 * n4));
; #pragma unroll
;     for (int i = 0; i < 4; ++i) { const int rp = 4 * i + q; LAS unsigned* sp = scr + (4 * n4) * 17 + rp;
;         sp[0]  = pk4_fp8(v[i][0].x * sc, v[i][1].x * sc, v[i][2].x * sc, v[i][3].x * sc);
;         sp[17] = pk4_fp8(v[i][0].y * sc, v[i][1].y * sc, v[i][2].y * sc, v[i][3].y * sc);
;         sp[34] = pk4_fp8(v[i][0].z * sc, v[i][1].z * sc, v[i][2].z * sc, v[i][3].z * sc);
;         sp[51] = pk4_fp8(v[i][0].w * sc, v[i][1].w * sc, v[i][2].w * sc, v[i][3].w * sc); }
; __device__ __forceinline__ void conv_dispatch(const Params& p, int it, LAS unsigned* scr, int lane) {
;     ...
;     { const int e = r / 512, rr = r % 512, kb = rr / 32, nb = rr % 32;
;         conv_item8(p.in[l ? 23 : 12] + (size_t)e * DFF * D, DFF, D, (l ? p.wp[IX_WD1] : p.wp[IX_WD0]) + (size_t)e * D * DFF, kb * 64, nb * 64, nb * 64, scr, lane, F8_SWD); }
.LBB0_920:
	s_movk_i32 s6, 0x73ff
	v_add_u32_e32 v4, 0xffff8c00, v78
	v_cmp_lt_i32_e32 vcc, s6, v78
	v_mov_b32_e32 v2, 0x1000
	v_mov_b32_e32 v5, 0xc00
	v_cndmask_b32_e32 v2, v2, v5, vcc
	v_cndmask_b32_e32 v4, v78, v4, vcc
	v_cmp_ge_i32_e64 s[6:7], v4, v2
	s_and_saveexec_b64 s[8:9], s[6:7]
	s_xor_b64 s[8:9], exec, s[8:9]
	s_cbranch_execz .LBB0_930
	v_sub_u32_e32 v5, v4, v2
	s_movk_i32 s6, 0x3ff
	v_cmp_lt_i32_e64 s[6:7], s6, v5
	s_and_saveexec_b64 s[86:87], s[6:7]
	s_xor_b64 s[86:87], exec, s[86:87]
	s_cbranch_execz .LBB0_927
	s_movk_i32 s6, 0x43ff
	v_cmp_lt_u32_e64 s[6:7], s6, v5
	s_and_saveexec_b64 s[88:89], s[6:7]
	s_xor_b64 s[88:89], exec, s[88:89]
	s_cbranch_execz .LBB0_924
	v_add_u32_e32 v2, 0xffffbc00, v5
	v_lshrrev_b32_e32 v6, 9, v2
	v_mov_b32_e32 v2, 0x60
	v_mov_b32_e32 v5, 0xb8
	v_cndmask_b32_e32 v2, v2, v5, vcc
	v_lshl_add_u64 v[8:9], s[0:1], 0, v[2:3]
	global_load_dwordx2 v[8:9], v[8:9], off
	v_mov_b32_e32 v7, v3
	v_lshlrev_b64 v[10:11], 23, v[6:7]
	v_mov_b32_e32 v2, s37
	v_mov_b32_e32 v5, s39
	v_mov_b32_e32 v71, v3
	v_lshlrev_b64 v[6:7], 21, v[6:7]
	v_mov_b32_e32 v75, v3
	s_waitcnt vmcnt(0)
	v_lshl_add_u64 v[8:9], v[8:9], 0, v[10:11]
	v_cndmask_b32_e32 v11, v2, v5, vcc
	v_mov_b32_e32 v2, s36
	v_mov_b32_e32 v5, s38
	v_cndmask_b32_e32 v10, v2, v5, vcc
	v_lshlrev_b32_e32 v2, 1, v4
	v_and_b32_e32 v74, 0x3c0, v2
	v_lshlrev_b32_e32 v2, 6, v4
	v_and_b32_e32 v76, 0x7c0, v2
	v_lshlrev_b32_e32 v2, 2, v76
	v_lshl_add_u64 v[4:5], v[8:9], 0, v[2:3]
	v_lshl_add_u64 v[4:5], v[4:5], 0, v[70:71]
	v_lshl_or_b32 v2, v74, 13, v87
	v_lshl_add_u64 v[20:21], v[4:5], 0, v[2:3]
	v_add_co_u32_e64 v4, s[6:7], s77, v20
	global_load_dwordx4 v[48:51], v[20:21], off nt
	s_nop 0
	v_addc_co_u32_e64 v5, s[6:7], 0, v21, s[6:7]
	s_movk_i32 s6, 0x4000
	global_load_dwordx4 v[52:55], v[4:5], off nt
	v_add_co_u32_e64 v4, s[6:7], s6, v20
	v_lshl_add_u64 v[72:73], v[10:11], 0, v[6:7]
	s_nop 0
	v_addc_co_u32_e64 v5, s[6:7], 0, v21, s[6:7]
	s_movk_i32 s6, 0x6000
	global_load_dwordx4 v[60:63], v[4:5], off nt
	v_add_co_u32_e64 v4, s[6:7], s6, v20
	s_nop 1
	v_addc_co_u32_e64 v5, s[6:7], 0, v21, s[6:7]
	s_mov_b32 s6, 0x20000
	global_load_dwordx4 v[64:67], v[4:5], off nt
	v_add_co_u32_e64 v4, s[6:7], s6, v20
	s_nop 1
	v_addc_co_u32_e64 v5, s[6:7], 0, v21, s[6:7]
	s_mov_b32 s6, 0x22000
	global_load_dwordx4 v[36:39], v[4:5], off nt
	v_add_co_u32_e64 v4, s[6:7], s6, v20
	s_nop 1
	v_addc_co_u32_e64 v5, s[6:7], 0, v21, s[6:7]
	s_mov_b32 s6, 0x24000
	global_load_dwordx4 v[40:43], v[4:5], off nt
	v_add_co_u32_e64 v4, s[6:7], s6, v20
	s_nop 1
	v_addc_co_u32_e64 v5, s[6:7], 0, v21, s[6:7]
	s_mov_b32 s6, 0x26000
	global_load_dwordx4 v[44:47], v[4:5], off nt
	v_add_co_u32_e64 v4, s[6:7], s6, v20
	s_nop 0
	s_nop 0
	v_addc_co_u32_e64 v5, s[6:7], 0, v21, s[6:7]
	s_mov_b32 s6, 0x40000
	global_load_dwordx4 v[56:59], v[4:5], off nt
	v_add_co_u32_e64 v4, s[6:7], s6, v20
	s_nop 0
	s_nop 0
	v_addc_co_u32_e64 v5, s[6:7], 0, v21, s[6:7]
	s_mov_b32 s6, 0x42000
	global_load_dwordx4 v[12:15], v[4:5], off nt
	v_add_co_u32_e64 v4, s[6:7], s6, v20
	s_nop 0
	s_nop 0
	v_addc_co_u32_e64 v5, s[6:7], 0, v21, s[6:7]
	s_mov_b32 s6, 0x44000
	global_load_dwordx4 v[24:27], v[4:5], off nt
	v_add_co_u32_e64 v4, s[6:7], s6, v20
	s_nop 0
	s_nop 0
	v_addc_co_u32_e64 v5, s[6:7], 0, v21, s[6:7]
	s_mov_b32 s6, 0x46000
	global_load_dwordx4 v[28:31], v[4:5], off nt
	v_add_co_u32_e64 v4, s[6:7], s6, v20
	s_nop 0
	s_nop 0
	v_addc_co_u32_e64 v5, s[6:7], 0, v21, s[6:7]
	global_load_dwordx4 v[32:35], v[4:5], off nt
	s_mov_b32 s6, 0x60000
	v_add_co_u32_e64 v4, s[6:7], s6, v20
	s_nop 0
	s_nop 0
	v_addc_co_u32_e64 v5, s[6:7], 0, v21, s[6:7]
	s_mov_b32 s6, 0x62000
	s_nop 0
	v_add_co_u32_e64 v8, s[6:7], s6, v20
	global_load_dwordx4 v[4:7], v[4:5], off nt
	s_nop 0
	v_addc_co_u32_e64 v9, s[6:7], 0, v21, s[6:7]
	s_mov_b32 s6, 0x64000
	s_nop 0
	v_add_co_u32_e64 v16, s[6:7], s6, v20
	global_load_dwordx4 v[8:11], v[8:9], off nt
	s_nop 0
	v_addc_co_u32_e64 v17, s[6:7], 0, v21, s[6:7]
	s_mov_b32 s6, 0x66000
	s_nop 0
	v_add_co_u32_e64 v20, s[6:7], s6, v20
	global_load_dwordx4 v[16:19], v[16:17], off nt
	s_nop 0
	v_addc_co_u32_e64 v21, s[6:7], 0, v21, s[6:7]
	global_load_dwordx4 v[20:23], v[20:21], off nt
	s_waitcnt vmcnt(15)
	v_mul_f32_e32 v2, 0x43800000, v48
	s_waitcnt vmcnt(14)
	v_mul_f32_e32 v48, 0x43800000, v52
	s_waitcnt vmcnt(13)
	v_mul_f32_e32 v52, 0x43800000, v60
	s_waitcnt vmcnt(12)
	v_mul_f32_e32 v60, 0x43800000, v64
	v_mov_b32_e32 v64, v3
	v_cvt_pk_fp8_f32 v64, v2, v48
	v_mul_f32_e32 v2, 0x43800000, v49
	v_mul_f32_e32 v48, 0x43800000, v53
	v_mov_b32_e32 v53, v3
	v_cvt_pk_fp8_f32 v53, v2, v48
	v_cvt_pk_fp8_f32 v64, v52, v60 op_sel:[0,0,1]
	v_mul_f32_e32 v49, 0x43800000, v61
	v_mul_f32_e32 v52, 0x43800000, v65
	v_cvt_pk_fp8_f32 v53, v49, v52 op_sel:[0,0,1]
	v_mul_f32_e32 v2, 0x43800000, v50
	v_mul_f32_e32 v48, 0x43800000, v54
	v_mov_b32_e32 v52, v3
	v_cvt_pk_fp8_f32 v52, v2, v48
	v_mul_f32_e32 v2, 0x43800000, v51
	v_mul_f32_e32 v48, 0x43800000, v55
	v_mov_b32_e32 v51, v3
	v_cvt_pk_fp8_f32 v51, v2, v48
	s_waitcnt vmcnt(11)
	v_mul_f32_e32 v2, 0x43800000, v36
	s_waitcnt vmcnt(10)
	v_mul_f32_e32 v36, 0x43800000, v40
	v_mov_b32_e32 v48, v3
	v_cvt_pk_fp8_f32 v48, v2, v36
	v_mul_f32_e32 v2, 0x43800000, v37
	v_mul_f32_e32 v36, 0x43800000, v41
	v_mov_b32_e32 v41, v3
	v_cvt_pk_fp8_f32 v41, v2, v36
	s_waitcnt vmcnt(9)
	v_mul_f32_e32 v40, 0x43800000, v44
	v_mul_f32_e32 v37, 0x43800000, v45
	v_mul_f32_e32 v2, 0x43800000, v38
	v_mul_f32_e32 v36, 0x43800000, v42
	v_mul_f32_e32 v49, 0x43800000, v62
	v_mul_f32_e32 v50, 0x43800000, v66
	v_cvt_pk_fp8_f32 v52, v49, v50 op_sel:[0,0,1]
	s_waitcnt vmcnt(8)
; #define LAS __attribute__((address_space(3)))
; __device__ __forceinline__ unsigned pk4_fp8(float a, float b, float c, float d) { unsigned w = 0u; w = __builtin_amdgcn_cvt_pk_fp8_f32(a, b, w, false); w = __builtin_amdgcn_cvt_pk_fp8_f32(c, d, w, true); return w; }
; __device__ __forceinline__ void conv_item8(const float* W, int K, int N, unsigned char* WT, int k0, int n0, int drow0, LAS unsigned* scr, int lane, float sc, bool rperm = false) {
;     ...
;         for (int t = 0; t < 4; ++t) v[i][t] = __builtin_nontemporal_load((const f32x4*)(W + (size_t)(k0 + 4 * (4 * i + q) + t) * N + n0 + 4 * n4));
; #pragma unroll
;     for (int i = 0; i < 4; ++i) { const int rp = 4 * i + q; LAS unsigned* sp = scr + (4 * n4) * 17 + rp;
;         sp[0]  = pk4_fp8(v[i][0].x * sc, v[i][1].x * sc, v[i][2].x * sc, v[i][3].x * sc);
;         sp[17] = pk4_fp8(v[i][0].y * sc, v[i][1].y * sc, v[i][2].y * sc, v[i][3].y * sc);
;         sp[34] = pk4_fp8(v[i][0].z * sc, v[i][1].z * sc, v[i][2].z * sc, v[i][3].z * sc);
;         sp[51] = pk4_fp8(v[i][0].w * sc, v[i][1].w * sc, v[i][2].w * sc, v[i][3].w * sc); }
;     asm volatile("s_waitcnt lgkmcnt(0)" ::: "memory");
;     const int c = lane & 3;
; #pragma unroll
;     for (int j = 0; j < 4; ++j) {
;         const int n = (lane >> 2) + 16 * j; const LAS unsigned* sp = scr + n * 17 + 4 * c;
;         u32x4 o; o.x = sp[0]; o.y = sp[1]; o.z = sp[2]; o.w = sp[3];
;         const int nr = (rperm && n < 32) ? ((n < 16) ? 2 * n : 2 * (n - 16) + 1) : n;
;         *(u32x4*)(WT + (size_t)(drow0 + nr) * K + k0 + 16 * c) = o;
;     }
;     asm volatile("s_waitcnt lgkmcnt(0)" ::: "memory");
	v_mul_f32_e32 v44, 0x43800000, v56
	v_cvt_pk_fp8_f32 v48, v40, v44 op_sel:[0,0,1]
	v_mul_f32_e32 v40, 0x43800000, v57
	v_cvt_pk_fp8_f32 v41, v37, v40 op_sel:[0,0,1]
	v_mov_b32_e32 v40, v3
	v_cvt_pk_fp8_f32 v40, v2, v36
	v_mul_f32_e32 v2, 0x43800000, v39
	v_mul_f32_e32 v36, 0x43800000, v43
	v_mov_b32_e32 v39, v3
	v_cvt_pk_fp8_f32 v39, v2, v36
	s_waitcnt vmcnt(7)
	v_mul_f32_e32 v2, 0x43800000, v12
	v_mul_f32_e32 v37, 0x43800000, v46
	v_mul_f32_e32 v38, 0x43800000, v58
	v_mul_f32_e32 v49, 0x43800000, v63
	s_waitcnt vmcnt(6)
	v_mul_f32_e32 v12, 0x43800000, v24
	v_mul_f32_e32 v50, 0x43800000, v67
	v_cvt_pk_fp8_f32 v40, v37, v38 op_sel:[0,0,1]
	v_mul_f32_e32 v37, 0x43800000, v47
	v_mul_f32_e32 v38, 0x43800000, v59
	v_cvt_pk_fp8_f32 v51, v49, v50 op_sel:[0,0,1]
	v_cvt_pk_fp8_f32 v39, v37, v38 op_sel:[0,0,1]
	s_waitcnt vmcnt(5)
	v_mul_f32_e32 v24, 0x43800000, v28
	ds_write2_b32 v81, v64, v48 offset1:4
	ds_write2_b32 v81, v53, v41 offset0:17 offset1:21
	ds_write2_b32 v81, v52, v40 offset0:34 offset1:38
	ds_write2_b32 v81, v51, v39 offset0:51 offset1:55
	s_waitcnt vmcnt(4)
	v_mul_f32_e32 v28, 0x43800000, v32
	v_mov_b32_e32 v32, v3
	v_cvt_pk_fp8_f32 v32, v2, v12
	v_mul_f32_e32 v2, 0x43800000, v13
	v_mul_f32_e32 v12, 0x43800000, v25
	v_mov_b32_e32 v25, v3
	v_cvt_pk_fp8_f32 v25, v2, v12
	v_cvt_pk_fp8_f32 v32, v24, v28 op_sel:[0,0,1]
	v_mul_f32_e32 v13, 0x43800000, v29
	v_mul_f32_e32 v24, 0x43800000, v33
	v_cvt_pk_fp8_f32 v25, v13, v24 op_sel:[0,0,1]
	v_mul_f32_e32 v2, 0x43800000, v14
	v_mul_f32_e32 v12, 0x43800000, v26
	v_mov_b32_e32 v24, v3
	v_cvt_pk_fp8_f32 v24, v2, v12
	v_mul_f32_e32 v2, 0x43800000, v15
	v_mul_f32_e32 v12, 0x43800000, v27
	v_mov_b32_e32 v15, v3
	v_cvt_pk_fp8_f32 v15, v2, v12
	v_mul_f32_e32 v13, 0x43800000, v30
	v_mul_f32_e32 v14, 0x43800000, v34
	v_cvt_pk_fp8_f32 v24, v13, v14 op_sel:[0,0,1]
	v_mul_f32_e32 v13, 0x43800000, v31
	v_mul_f32_e32 v14, 0x43800000, v35
	v_cvt_pk_fp8_f32 v15, v13, v14 op_sel:[0,0,1]
	s_waitcnt vmcnt(3)
	v_mul_f32_e32 v2, 0x43800000, v4
	s_waitcnt vmcnt(2)
	v_mul_f32_e32 v4, 0x43800000, v8
	v_mov_b32_e32 v13, v3
	v_cvt_pk_fp8_f32 v13, v2, v4
	v_mul_f32_e32 v2, 0x43800000, v5
	v_mul_f32_e32 v4, 0x43800000, v9
	v_mov_b32_e32 v9, v3
	v_cvt_pk_fp8_f32 v9, v2, v4
	s_waitcnt vmcnt(1)
	v_mul_f32_e32 v8, 0x43800000, v16
	s_waitcnt vmcnt(0)
	v_mul_f32_e32 v12, 0x43800000, v20
	v_cvt_pk_fp8_f32 v13, v8, v12 op_sel:[0,0,1]
	v_mul_f32_e32 v5, 0x43800000, v17
	v_mul_f32_e32 v8, 0x43800000, v21
	v_cvt_pk_fp8_f32 v9, v5, v8 op_sel:[0,0,1]
	v_mul_f32_e32 v2, 0x43800000, v6
	v_mul_f32_e32 v4, 0x43800000, v10
	v_mov_b32_e32 v8, v3
	v_cvt_pk_fp8_f32 v8, v2, v4
	v_mul_f32_e32 v2, 0x43800000, v7
	v_mul_f32_e32 v4, 0x43800000, v11
	v_mov_b32_e32 v7, v3
	v_cvt_pk_fp8_f32 v7, v2, v4
	v_mul_f32_e32 v5, 0x43800000, v18
	v_mul_f32_e32 v6, 0x43800000, v22
	v_cvt_pk_fp8_f32 v8, v5, v6 op_sel:[0,0,1]
	v_mul_f32_e32 v5, 0x43800000, v19
	v_mul_f32_e32 v6, 0x43800000, v23
	v_cvt_pk_fp8_f32 v7, v5, v6 op_sel:[0,0,1]
	ds_write2_b32 v81, v32, v13 offset0:8 offset1:12
	ds_write2_b32 v81, v25, v9 offset0:25 offset1:29
	ds_write2_b32 v81, v24, v8 offset0:42 offset1:46
	ds_write2_b32 v81, v15, v7 offset0:59 offset1:63
	s_waitcnt lgkmcnt(0)
	v_lshl_add_u64 v[4:5], v[72:73], 0, v[74:75]
	v_lshl_add_u64 v[8:9], v[4:5], 0, v[68:69]
	ds_read2_b32 v[4:5], v88 offset1:1
	ds_read2_b32 v[6:7], v88 offset0:2 offset1:3
	v_or_b32_e32 v2, v76, v82
	v_lshlrev_b32_e32 v2, 10, v2
	v_lshl_add_u64 v[10:11], v[8:9], 0, v[2:3]
	v_or_b32_e32 v2, v76, v83
	s_waitcnt lgkmcnt(0)
	global_store_dwordx4 v[10:11], v[4:7], off
	ds_read2_b32 v[4:5], v89 offset1:1
	ds_read2_b32 v[6:7], v90 offset1:1
	v_lshlrev_b32_e32 v2, 10, v2
	v_lshl_add_u64 v[10:11], v[8:9], 0, v[2:3]
	v_or_b32_e32 v2, v76, v84
	v_lshlrev_b32_e32 v2, 10, v2
	s_waitcnt lgkmcnt(0)
	global_store_dwordx4 v[10:11], v[4:7], off
	ds_read2_b32 v[4:5], v91 offset1:1
	ds_read2_b32 v[6:7], v92 offset1:1
	v_lshl_add_u64 v[10:11], v[8:9], 0, v[2:3]
	v_or_b32_e32 v2, v76, v85
	v_lshlrev_b32_e32 v2, 10, v2
	v_lshl_add_u64 v[8:9], v[8:9], 0, v[2:3]
	s_waitcnt lgkmcnt(0)
	global_store_dwordx4 v[10:11], v[4:7], off
	ds_read2_b32 v[4:5], v93 offset1:1
	ds_read2_b32 v[6:7], v94 offset1:1
	s_waitcnt lgkmcnt(0)
	global_store_dwordx4 v[8:9], v[4:7], off
	s_waitcnt lgkmcnt(0)
; #define LAS __attribute__((address_space(3)))
; __device__ __forceinline__ unsigned pk4_fp8(float a, float b, float c, float d) { unsigned w = 0u; w = __builtin_amdgcn_cvt_pk_fp8_f32(a, b, w, false); w = __builtin_amdgcn_cvt_pk_fp8_f32(c, d, w, true); return w; }
; __device__ __forceinline__ void conv_item8(const float* W, int K, int N, unsigned char* WT, int k0, int n0, int drow0, LAS unsigned* scr, int lane, float sc, bool rperm = false) {
;     const int q = lane >> 4, n4 = lane & 15;
;     f32x4 v[4][4];
; #pragma unroll
;     for (int i = 0; i < 4; ++i)
; #pragma unroll
;         for (int t = 0; t < 4; ++t) v[i][t] = __builtin_nontemporal_load((const f32x4*)(W + (size_t)(k0 + 4 * (4 * i + q) + t) * N + n0 + 4 * n4));
; #pragma unroll
;     for (int i = 0; i < 4; ++i) { const int rp = 4 * i + q; LAS unsigned* sp = scr + (4 * n4) * 17 + rp;
;         sp[0]  = pk4_fp8(v[i][0].x * sc, v[i][1].x * sc, v[i][2].x * sc, v[i][3].x * sc);
;         sp[17] = pk4_fp8(v[i][0].y * sc, v[i][1].y * sc, v[i][2].y * sc, v[i][3].y * sc);
;         sp[34] = pk4_fp8(v[i][0].z * sc, v[i][1].z * sc, v[i][2].z * sc, v[i][3].z * sc);
;         sp[51] = pk4_fp8(v[i][0].w * sc, v[i][1].w * sc, v[i][2].w * sc, v[i][3].w * sc); }
; __device__ __forceinline__ void conv_dispatch(const Params& p, int it, LAS unsigned* scr, int lane) {
;     ...
;     if (r < 2 * I_G) { const int up = r >= I_G; if (up) r -= I_G; const int e = r / 512, rr = r % 512, kb = rr / 16, nb = rr % 16, n0 = nb * 64;
;         conv_item8(p.in[(l ? 21 : 10) + up] + (size_t)e * D * DFF, D, DFF, (l ? p.wp[IX_WGU1] : p.wp[IX_WGU0]) + (size_t)e * 2048 * D, kb * 64, n0, (n0 >> 7) * 256 + (n0 & 127) + up * 128, scr, lane, F8_SW);
;         return; } r -= 2 * I_G;
.LBB0_924:
	s_andn2_saveexec_b64 s[88:89], s[88:89]
	s_cbranch_execz .LBB0_926
	s_movk_i32 s6, 0x23ff
	v_cmp_lt_u32_e64 s[6:7], s6, v5
	v_mov_b32_e32 v0, 0xfffffc00
	v_mov_b32_e32 v1, 0xffffdc00
	v_cndmask_b32_e64 v2, v0, v1, s[6:7]
	v_mov_b32_e32 v0, 0x50
	v_mov_b32_e32 v1, 0xa8
	v_add_u32_e32 v5, v2, v5
	v_cndmask_b32_e32 v2, v0, v1, vcc
	v_lshl_add_u64 v[8:9], s[0:1], 0, v[2:3]
	v_cndmask_b32_e64 v2, 0, 1, s[6:7]
	v_lshlrev_b32_e32 v2, 3, v2
	v_lshl_add_u64 v[8:9], v[8:9], 0, v[2:3]
	global_load_dwordx2 v[8:9], v[8:9], off
	v_lshrrev_b32_e32 v6, 9, v5
	v_mov_b32_e32 v7, v3
	v_lshlrev_b64 v[10:11], 23, v[6:7]
	v_mov_b32_e32 v2, s41
	v_lshlrev_b32_e32 v12, 6, v5
	v_lshlrev_b64 v[6:7], 22, v[6:7]
	v_mov_b32_e32 v71, v3
	v_mov_b32_e32 v75, v3
	s_waitcnt vmcnt(0)
	v_lshl_add_u64 v[8:9], v[8:9], 0, v[10:11]
	v_mov_b32_e32 v10, s43
	v_cndmask_b32_e32 v11, v2, v10, vcc
	v_mov_b32_e32 v2, s40
	v_mov_b32_e32 v10, s42
	v_cndmask_b32_e32 v10, v2, v10, vcc
	v_lshlrev_b32_e32 v2, 2, v5
	v_and_b32_e32 v74, 0x7c0, v2
	v_lshlrev_b32_e32 v2, 7, v5
	v_lshl_add_u64 v[72:73], v[10:11], 0, v[6:7]
	v_and_b32_e32 v2, 0x700, v2
	v_and_b32_e32 v6, 64, v12
	v_cndmask_b32_e64 v7, 0, v95, s[6:7]
	v_or3_b32 v76, v6, v7, v2
	v_lshlrev_b32_e32 v2, 8, v5
	s_movk_i32 s6, 0x1f0
	v_and_b32_e32 v2, 0xf00, v2
	v_and_or_b32 v6, v4, s6, v79
	v_lshl_add_u64 v[4:5], v[8:9], 0, v[2:3]
	v_lshl_add_u64 v[4:5], v[4:5], 0, v[70:71]
	v_lshlrev_b32_e32 v2, 14, v6
	v_lshl_add_u64 v[12:13], v[4:5], 0, v[2:3]
	v_add_co_u32_e64 v4, s[6:7], s77, v12
	global_load_dwordx4 v[52:55], v[12:13], off nt
	s_nop 0
	v_addc_co_u32_e64 v5, s[6:7], 0, v13, s[6:7]
	s_movk_i32 s6, 0x3000
	global_load_dwordx4 v[56:59], v[4:5], off offset:-4096 nt
	global_load_dwordx4 v[60:63], v[4:5], off nt
	v_add_co_u32_e64 v4, s[6:7], s6, v12
	s_nop 1
	v_addc_co_u32_e64 v5, s[6:7], 0, v13, s[6:7]
	global_load_dwordx4 v[64:67], v[4:5], off nt
	s_mov_b32 s6, 0x11000
	v_add_co_u32_e64 v4, s[6:7], s6, v12
	s_nop 1
	v_addc_co_u32_e64 v5, s[6:7], 0, v13, s[6:7]
	s_mov_b32 s6, 0x13000
	global_load_dwordx4 v[36:39], v[4:5], off offset:-4096 nt
	global_load_dwordx4 v[40:43], v[4:5], off nt
	v_add_co_u32_e64 v4, s[6:7], s6, v12
	s_nop 1
	v_addc_co_u32_e64 v5, s[6:7], 0, v13, s[6:7]
	global_load_dwordx4 v[44:47], v[4:5], off offset:-4096 nt
	global_load_dwordx4 v[48:51], v[4:5], off nt
	s_mov_b32 s6, 0x21000
	v_add_co_u32_e64 v4, s[6:7], s6, v12
	s_nop 1
	v_addc_co_u32_e64 v5, s[6:7], 0, v13, s[6:7]
	s_mov_b32 s6, 0x23000
	global_load_dwordx4 v[20:23], v[4:5], off offset:-4096 nt
	global_load_dwordx4 v[24:27], v[4:5], off nt
	v_add_co_u32_e64 v4, s[6:7], s6, v12
	s_nop 0
	s_nop 0
	v_addc_co_u32_e64 v5, s[6:7], 0, v13, s[6:7]
	global_load_dwordx4 v[28:31], v[4:5], off offset:-4096 nt
	global_load_dwordx4 v[32:35], v[4:5], off nt
	s_mov_b32 s6, 0x31000
	v_add_co_u32_e64 v8, s[6:7], s6, v12
	s_nop 0
	s_nop 0
	v_addc_co_u32_e64 v9, s[6:7], 0, v13, s[6:7]
	s_mov_b32 s6, 0x33000
	s_nop 0
	v_add_co_u32_e64 v16, s[6:7], s6, v12
	global_load_dwordx4 v[4:7], v[8:9], off offset:-4096 nt
	s_nop 0
	global_load_dwordx4 v[8:11], v[8:9], off nt
	v_addc_co_u32_e64 v17, s[6:7], 0, v13, s[6:7]
	global_load_dwordx4 v[12:15], v[16:17], off offset:-4096 nt
	s_nop 0
	global_load_dwordx4 v[16:19], v[16:17], off nt
	s_waitcnt vmcnt(15)
	v_mul_f32_e32 v2, 0x43800000, v52
	s_waitcnt vmcnt(14)
	v_mul_f32_e32 v52, 0x43800000, v56
	s_waitcnt vmcnt(13)
	v_mul_f32_e32 v56, 0x43800000, v60
	s_waitcnt vmcnt(12)
	v_mul_f32_e32 v60, 0x43800000, v64
	v_mov_b32_e32 v64, v3
	v_cvt_pk_fp8_f32 v64, v2, v52
	v_mul_f32_e32 v2, 0x43800000, v53
	v_mul_f32_e32 v52, 0x43800000, v57
	v_mov_b32_e32 v57, v3
	v_cvt_pk_fp8_f32 v57, v2, v52
	v_cvt_pk_fp8_f32 v64, v56, v60 op_sel:[0,0,1]
	v_mul_f32_e32 v53, 0x43800000, v61
	v_mul_f32_e32 v56, 0x43800000, v65
	v_cvt_pk_fp8_f32 v57, v53, v56 op_sel:[0,0,1]
	v_mul_f32_e32 v2, 0x43800000, v54
	v_mul_f32_e32 v52, 0x43800000, v58
	v_mov_b32_e32 v56, v3
	v_cvt_pk_fp8_f32 v56, v2, v52
	v_mul_f32_e32 v2, 0x43800000, v55
	v_mul_f32_e32 v52, 0x43800000, v59
	v_mov_b32_e32 v55, v3
	v_cvt_pk_fp8_f32 v55, v2, v52
	s_waitcnt vmcnt(11)
	v_mul_f32_e32 v2, 0x43800000, v36
	s_waitcnt vmcnt(10)
	v_mul_f32_e32 v36, 0x43800000, v40
	s_waitcnt vmcnt(9)
	v_mul_f32_e32 v40, 0x43800000, v44
	s_waitcnt vmcnt(8)
; #define LAS __attribute__((address_space(3)))
; __device__ __forceinline__ unsigned pk4_fp8(float a, float b, float c, float d) { unsigned w = 0u; w = __builtin_amdgcn_cvt_pk_fp8_f32(a, b, w, false); w = __builtin_amdgcn_cvt_pk_fp8_f32(c, d, w, true); return w; }
; __device__ __forceinline__ void conv_item8(const float* W, int K, int N, unsigned char* WT, int k0, int n0, int drow0, LAS unsigned* scr, int lane, float sc, bool rperm = false) {
;     ...
;         for (int t = 0; t < 4; ++t) v[i][t] = __builtin_nontemporal_load((const f32x4*)(W + (size_t)(k0 + 4 * (4 * i + q) + t) * N + n0 + 4 * n4));
; #pragma unroll
;     for (int i = 0; i < 4; ++i) { const int rp = 4 * i + q; LAS unsigned* sp = scr + (4 * n4) * 17 + rp;
;         sp[0]  = pk4_fp8(v[i][0].x * sc, v[i][1].x * sc, v[i][2].x * sc, v[i][3].x * sc);
;         sp[17] = pk4_fp8(v[i][0].y * sc, v[i][1].y * sc, v[i][2].y * sc, v[i][3].y * sc);
;         sp[34] = pk4_fp8(v[i][0].z * sc, v[i][1].z * sc, v[i][2].z * sc, v[i][3].z * sc);
;         sp[51] = pk4_fp8(v[i][0].w * sc, v[i][1].w * sc, v[i][2].w * sc, v[i][3].w * sc); }
;     asm volatile("s_waitcnt lgkmcnt(0)" ::: "memory");
;     const int c = lane & 3;
; #pragma unroll
;     for (int j = 0; j < 4; ++j) {
;         const int n = (lane >> 2) + 16 * j; const LAS unsigned* sp = scr + n * 17 + 4 * c;
;         u32x4 o; o.x = sp[0]; o.y = sp[1]; o.z = sp[2]; o.w = sp[3];
;         const int nr = (rperm && n < 32) ? ((n < 16) ? 2 * n : 2 * (n - 16) + 1) : n;
;         *(u32x4*)(WT + (size_t)(drow0 + nr) * K + k0 + 16 * c) = o;
;     }
;     asm volatile("s_waitcnt lgkmcnt(0)" ::: "memory");
	v_mul_f32_e32 v44, 0x43800000, v48
	v_mov_b32_e32 v48, v3
	v_cvt_pk_fp8_f32 v48, v2, v36
	v_mul_f32_e32 v2, 0x43800000, v37
	v_mul_f32_e32 v36, 0x43800000, v41
	v_mov_b32_e32 v41, v3
	v_cvt_pk_fp8_f32 v41, v2, v36
	v_cvt_pk_fp8_f32 v48, v40, v44 op_sel:[0,0,1]
	v_mul_f32_e32 v37, 0x43800000, v45
	v_mul_f32_e32 v40, 0x43800000, v49
	v_cvt_pk_fp8_f32 v41, v37, v40 op_sel:[0,0,1]
	v_mul_f32_e32 v2, 0x43800000, v38
	v_mul_f32_e32 v36, 0x43800000, v42
	v_mov_b32_e32 v40, v3
	v_cvt_pk_fp8_f32 v40, v2, v36
	v_mul_f32_e32 v2, 0x43800000, v39
	v_mul_f32_e32 v36, 0x43800000, v43
	v_mov_b32_e32 v39, v3
	v_cvt_pk_fp8_f32 v39, v2, v36
	v_mul_f32_e32 v53, 0x43800000, v62
	v_mul_f32_e32 v54, 0x43800000, v66
	v_mul_f32_e32 v37, 0x43800000, v46
	v_mul_f32_e32 v38, 0x43800000, v50
	v_cvt_pk_fp8_f32 v56, v53, v54 op_sel:[0,0,1]
	v_mul_f32_e32 v53, 0x43800000, v63
	v_mul_f32_e32 v54, 0x43800000, v67
	v_cvt_pk_fp8_f32 v40, v37, v38 op_sel:[0,0,1]
	v_mul_f32_e32 v37, 0x43800000, v47
	v_mul_f32_e32 v38, 0x43800000, v51
	v_cvt_pk_fp8_f32 v55, v53, v54 op_sel:[0,0,1]
	v_cvt_pk_fp8_f32 v39, v37, v38 op_sel:[0,0,1]
	ds_write2_b32 v81, v64, v48 offset1:4
	ds_write2_b32 v81, v57, v41 offset0:17 offset1:21
	ds_write2_b32 v81, v56, v40 offset0:34 offset1:38
	ds_write2_b32 v81, v55, v39 offset0:51 offset1:55
	s_waitcnt vmcnt(7)
	v_mul_f32_e32 v2, 0x43800000, v20
	s_waitcnt vmcnt(6)
	v_mul_f32_e32 v20, 0x43800000, v24
	s_waitcnt vmcnt(5)
	v_mul_f32_e32 v24, 0x43800000, v28
	s_waitcnt vmcnt(4)
	v_mul_f32_e32 v28, 0x43800000, v32
	v_mov_b32_e32 v32, v3
	v_cvt_pk_fp8_f32 v32, v2, v20
	v_mul_f32_e32 v2, 0x43800000, v21
	v_mul_f32_e32 v20, 0x43800000, v25
	v_mov_b32_e32 v25, v3
	v_cvt_pk_fp8_f32 v25, v2, v20
	v_cvt_pk_fp8_f32 v32, v24, v28 op_sel:[0,0,1]
	v_mul_f32_e32 v21, 0x43800000, v29
	v_mul_f32_e32 v24, 0x43800000, v33
	v_cvt_pk_fp8_f32 v25, v21, v24 op_sel:[0,0,1]
	v_mul_f32_e32 v2, 0x43800000, v22
	v_mul_f32_e32 v20, 0x43800000, v26
	v_mov_b32_e32 v24, v3
	v_cvt_pk_fp8_f32 v24, v2, v20
	v_mul_f32_e32 v2, 0x43800000, v23
	v_mul_f32_e32 v20, 0x43800000, v27
	v_mov_b32_e32 v23, v3
	v_cvt_pk_fp8_f32 v23, v2, v20
	s_waitcnt vmcnt(3)
	v_mul_f32_e32 v2, 0x43800000, v4
	s_waitcnt vmcnt(2)
	v_mul_f32_e32 v4, 0x43800000, v8
	s_waitcnt vmcnt(1)
	v_mul_f32_e32 v8, 0x43800000, v12
	s_waitcnt vmcnt(0)
	v_mul_f32_e32 v12, 0x43800000, v16
	v_mov_b32_e32 v16, v3
	v_cvt_pk_fp8_f32 v16, v2, v4
	v_mul_f32_e32 v2, 0x43800000, v5
	v_mul_f32_e32 v4, 0x43800000, v9
	v_mov_b32_e32 v9, v3
	v_cvt_pk_fp8_f32 v9, v2, v4
	v_cvt_pk_fp8_f32 v16, v8, v12 op_sel:[0,0,1]
	v_mul_f32_e32 v5, 0x43800000, v13
	v_mul_f32_e32 v8, 0x43800000, v17
	v_cvt_pk_fp8_f32 v9, v5, v8 op_sel:[0,0,1]
	v_mul_f32_e32 v2, 0x43800000, v6
	v_mul_f32_e32 v4, 0x43800000, v10
	v_mov_b32_e32 v8, v3
	v_cvt_pk_fp8_f32 v8, v2, v4
	v_mul_f32_e32 v2, 0x43800000, v7
	v_mul_f32_e32 v4, 0x43800000, v11
	v_mov_b32_e32 v7, v3
	v_cvt_pk_fp8_f32 v7, v2, v4
	v_mul_f32_e32 v21, 0x43800000, v30
	v_mul_f32_e32 v22, 0x43800000, v34
	v_mul_f32_e32 v5, 0x43800000, v14
	v_mul_f32_e32 v6, 0x43800000, v18
	v_cvt_pk_fp8_f32 v24, v21, v22 op_sel:[0,0,1]
	v_mul_f32_e32 v21, 0x43800000, v31
	v_mul_f32_e32 v22, 0x43800000, v35
	v_cvt_pk_fp8_f32 v8, v5, v6 op_sel:[0,0,1]
	v_mul_f32_e32 v5, 0x43800000, v15
	v_mul_f32_e32 v6, 0x43800000, v19
	v_cvt_pk_fp8_f32 v23, v21, v22 op_sel:[0,0,1]
	v_cvt_pk_fp8_f32 v7, v5, v6 op_sel:[0,0,1]
	ds_write2_b32 v81, v32, v16 offset0:8 offset1:12
	ds_write2_b32 v81, v25, v9 offset0:25 offset1:29
	ds_write2_b32 v81, v24, v8 offset0:42 offset1:46
	ds_write2_b32 v81, v23, v7 offset0:59 offset1:63
	s_waitcnt lgkmcnt(0)
	v_lshl_add_u64 v[4:5], v[72:73], 0, v[74:75]
	v_lshl_add_u64 v[8:9], v[4:5], 0, v[68:69]
	ds_read2_b32 v[4:5], v88 offset1:1
	ds_read2_b32 v[6:7], v88 offset0:2 offset1:3
	v_or_b32_e32 v2, v76, v82
	v_lshlrev_b32_e32 v2, 11, v2
	v_lshl_add_u64 v[10:11], v[8:9], 0, v[2:3]
	v_or_b32_e32 v2, v76, v83
	s_waitcnt lgkmcnt(0)
	global_store_dwordx4 v[10:11], v[4:7], off
	ds_read2_b32 v[4:5], v89 offset1:1
	ds_read2_b32 v[6:7], v90 offset1:1
	v_lshlrev_b32_e32 v2, 11, v2
	v_lshl_add_u64 v[10:11], v[8:9], 0, v[2:3]
	v_or_b32_e32 v2, v76, v84
	v_lshlrev_b32_e32 v2, 11, v2
	s_waitcnt lgkmcnt(0)
	global_store_dwordx4 v[10:11], v[4:7], off
	ds_read2_b32 v[4:5], v91 offset1:1
	ds_read2_b32 v[6:7], v92 offset1:1
	v_lshl_add_u64 v[10:11], v[8:9], 0, v[2:3]
	v_or_b32_e32 v2, v76, v85
	v_lshlrev_b32_e32 v2, 11, v2
	v_lshl_add_u64 v[8:9], v[8:9], 0, v[2:3]
	s_waitcnt lgkmcnt(0)
	global_store_dwordx4 v[10:11], v[4:7], off
	ds_read2_b32 v[4:5], v93 offset1:1
	ds_read2_b32 v[6:7], v94 offset1:1
	s_waitcnt lgkmcnt(0)
	global_store_dwordx4 v[8:9], v[4:7], off
	s_waitcnt lgkmcnt(0)

; #define LAS __attribute__((address_space(3)))
; __device__ __forceinline__ unsigned pk4_fp8(float a, float b, float c, float d) { unsigned w = 0u; w = __builtin_amdgcn_cvt_pk_fp8_f32(a, b, w, false); w = __builtin_amdgcn_cvt_pk_fp8_f32(c, d, w, true); return w; }
; __device__ __forceinline__ void conv_item8(const float* W, int K, int N, unsigned char* WT, int k0, int n0, int drow0, LAS unsigned* scr, int lane, float sc, bool rperm = false) {
;     const int q = lane >> 4, n4 = lane & 15;
;     f32x4 v[4][4];
; #pragma unroll
;     for (int i = 0; i < 4; ++i)
; #pragma unroll
;         for (int t = 0; t < 4; ++t) v[i][t] = __builtin_nontemporal_load((const f32x4*)(W + (size_t)(k0 + 4 * (4 * i + q) + t) * N + n0 + 4 * n4));
; #pragma unroll
;     for (int i = 0; i < 4; ++i) { const int rp = 4 * i + q; LAS unsigned* sp = scr + (4 * n4) * 17 + rp;
;         sp[0]  = pk4_fp8(v[i][0].x * sc, v[i][1].x * sc, v[i][2].x * sc, v[i][3].x * sc);
;         sp[17] = pk4_fp8(v[i][0].y * sc, v[i][1].y * sc, v[i][2].y * sc, v[i][3].y * sc);
;         sp[34] = pk4_fp8(v[i][0].z * sc, v[i][1].z * sc, v[i][2].z * sc, v[i][3].z * sc);
;         sp[51] = pk4_fp8(v[i][0].w * sc, v[i][1].w * sc, v[i][2].w * sc, v[i][3].w * sc); }
; __device__ __forceinline__ void conv_dispatch(const Params& p, int it, LAS unsigned* scr, int lane) {
;     ...
;     if (r < I_OUT) { if (OUT_F8) conv_item8(p.in[l ? 19 : 8], D, D, l ? p.wp[IX_WOUT1] : p.wp[IX_WOUT0], (r / 32) * 64, (r % 32) * 64, (r % 32) * 64, scr, lane, F8_SWD);
;         else conv_item(p.in[l ? 19 : 8], D, D, (bf16_t*)(l ? p.wp[IX_WOUT1] : p.wp[IX_WOUT0]), (r / 32) * 64, (r % 32) * 64, (r % 32) * 64, scr, lane); return; } r -= I_OUT;
.LBB0_927:
	s_andn2_saveexec_b64 s[6:7], s[86:87]
	s_cbranch_execz .LBB0_929
	v_cndmask_b32_e32 v2, 64, v96, vcc
	v_lshl_add_u64 v[6:7], s[0:1], 0, v[2:3]
	global_load_dwordx2 v[6:7], v[6:7], off
	v_mov_b32_e32 v2, s49
	v_mov_b32_e32 v4, s51
	v_cndmask_b32_e32 v75, v2, v4, vcc
	v_mov_b32_e32 v2, s48
	v_mov_b32_e32 v4, s50
	v_cndmask_b32_e32 v74, v2, v4, vcc
	v_ashrrev_i16_e32 v2, 15, v5
	v_lshrrev_b16_e32 v2, 11, v2
	v_add_u16_e32 v2, v5, v2
	v_ashrrev_i16_e32 v4, 5, v2
	v_and_b32_e32 v2, 0xffffffe0, v2
	v_lshlrev_b32_sdwa v76, v97, sext(v4) dst_sel:DWORD dst_unused:UNUSED_PAD src0_sel:DWORD src1_sel:WORD_0
	v_sub_u16_e32 v2, v5, v2
	v_lshlrev_b32_sdwa v72, v97, sext(v2) dst_sel:DWORD dst_unused:UNUSED_PAD src0_sel:DWORD src1_sel:WORD_0
	v_or_b32_e32 v28, v76, v80
	v_ashrrev_i32_e32 v73, 31, v72
	v_or_b32_e32 v8, 33, v28
	v_mov_b32_e32 v71, v3
	v_ashrrev_i32_e32 v29, 31, v28
	v_ashrrev_i32_e32 v9, 31, v8
	v_lshlrev_b64 v[8:9], 13, v[8:9]
	v_or_b32_e32 v12, 34, v28
	v_ashrrev_i32_e32 v13, 31, v12
	v_lshlrev_b64 v[12:13], 13, v[12:13]
	v_or_b32_e32 v16, 35, v28
	v_ashrrev_i32_e32 v17, 31, v16
	v_lshlrev_b64 v[16:17], 13, v[16:17]
	v_or_b32_e32 v20, 49, v28
	v_ashrrev_i32_e32 v21, 31, v20
	v_lshlrev_b64 v[20:21], 13, v[20:21]
	v_or_b32_e32 v24, 50, v28
	v_ashrrev_i32_e32 v25, 31, v24
	v_lshlrev_b64 v[24:25], 13, v[24:25]
	v_ashrrev_i32_e32 v77, 31, v76
	s_waitcnt vmcnt(0)
	v_lshl_add_u64 v[4:5], v[72:73], 2, v[6:7]
	v_lshl_add_u64 v[30:31], v[4:5], 0, v[70:71]
	v_lshlrev_b64 v[4:5], 13, v[28:29]
	v_lshl_add_u64 v[4:5], v[30:31], 0, v[4:5]
	v_lshl_add_u64 v[8:9], v[30:31], 0, v[8:9]
	global_load_dwordx4 v[48:51], v[4:5], off nt
	v_lshl_add_u64 v[12:13], v[30:31], 0, v[12:13]
	global_load_dwordx4 v[8:11], v[8:9], off nt
	v_or_b32_e32 v4, 1, v28
	v_ashrrev_i32_e32 v5, 31, v4
	v_lshlrev_b64 v[4:5], 13, v[4:5]
	v_lshl_add_u64 v[4:5], v[30:31], 0, v[4:5]
	global_load_dwordx4 v[56:59], v[4:5], off nt
	v_lshl_add_u64 v[16:17], v[30:31], 0, v[16:17]
	global_load_dwordx4 v[12:15], v[12:13], off nt
	v_or_b32_e32 v4, 2, v28
	v_ashrrev_i32_e32 v5, 31, v4
	v_lshlrev_b64 v[4:5], 13, v[4:5]
	v_lshl_add_u64 v[4:5], v[30:31], 0, v[4:5]
	global_load_dwordx4 v[60:63], v[4:5], off nt
	global_load_dwordx4 v[32:35], v[16:17], off nt
	v_or_b32_e32 v4, 3, v28
	v_or_b32_e32 v16, 48, v28
	v_ashrrev_i32_e32 v5, 31, v4
	v_ashrrev_i32_e32 v17, 31, v16
	v_lshlrev_b64 v[4:5], 13, v[4:5]
	v_lshlrev_b64 v[16:17], 13, v[16:17]
	v_lshl_add_u64 v[4:5], v[30:31], 0, v[4:5]
	v_lshl_add_u64 v[16:17], v[30:31], 0, v[16:17]
	global_load_dwordx4 v[64:67], v[4:5], off nt
	v_lshl_add_u64 v[20:21], v[30:31], 0, v[20:21]
	global_load_dwordx4 v[16:19], v[16:17], off nt
	v_or_b32_e32 v4, 16, v28
	v_ashrrev_i32_e32 v5, 31, v4
	v_lshlrev_b64 v[4:5], 13, v[4:5]
	v_lshl_add_u64 v[4:5], v[30:31], 0, v[4:5]
	global_load_dwordx4 v[36:39], v[4:5], off nt
	v_lshl_add_u64 v[24:25], v[30:31], 0, v[24:25]
	global_load_dwordx4 v[20:23], v[20:21], off nt
	v_or_b32_e32 v4, 17, v28
	v_ashrrev_i32_e32 v5, 31, v4
	v_lshlrev_b64 v[4:5], 13, v[4:5]
	v_lshl_add_u64 v[4:5], v[30:31], 0, v[4:5]
	global_load_dwordx4 v[40:43], v[4:5], off nt
	global_load_dwordx4 v[24:27], v[24:25], off nt
	v_or_b32_e32 v4, 18, v28
	v_ashrrev_i32_e32 v5, 31, v4
	v_lshlrev_b64 v[4:5], 13, v[4:5]
	v_lshl_add_u64 v[4:5], v[30:31], 0, v[4:5]
	global_load_dwordx4 v[44:47], v[4:5], off nt
	v_or_b32_e32 v4, 19, v28
	v_ashrrev_i32_e32 v5, 31, v4
	v_lshlrev_b64 v[4:5], 13, v[4:5]
	v_lshl_add_u64 v[4:5], v[30:31], 0, v[4:5]
	global_load_dwordx4 v[52:55], v[4:5], off nt
	v_or_b32_e32 v4, 32, v28
	v_ashrrev_i32_e32 v5, 31, v4
	v_lshlrev_b64 v[4:5], 13, v[4:5]
	v_lshl_add_u64 v[4:5], v[30:31], 0, v[4:5]
	global_load_dwordx4 v[4:7], v[4:5], off nt
	v_or_b32_e32 v28, 51, v28
	v_ashrrev_i32_e32 v29, 31, v28
	v_lshlrev_b64 v[28:29], 13, v[28:29]
	v_lshl_add_u64 v[28:29], v[30:31], 0, v[28:29]
	global_load_dwordx4 v[28:31], v[28:29], off nt
	s_waitcnt vmcnt(15)
	v_mul_f32_e32 v2, 0x43800000, v48
	s_waitcnt vmcnt(13)
	v_mul_f32_e32 v48, 0x43800000, v56
	s_waitcnt vmcnt(11)
	v_mul_f32_e32 v56, 0x43800000, v60
	s_waitcnt vmcnt(9)
	v_mul_f32_e32 v60, 0x43800000, v64
	v_mov_b32_e32 v64, v3
	v_cvt_pk_fp8_f32 v64, v2, v48
	v_mul_f32_e32 v2, 0x43800000, v49
	v_mul_f32_e32 v48, 0x43800000, v57
	v_mov_b32_e32 v57, v3
	v_cvt_pk_fp8_f32 v57, v2, v48
	v_cvt_pk_fp8_f32 v64, v56, v60 op_sel:[0,0,1]
	v_mul_f32_e32 v49, 0x43800000, v61
	v_mul_f32_e32 v56, 0x43800000, v65
	v_cvt_pk_fp8_f32 v57, v49, v56 op_sel:[0,0,1]
	v_mul_f32_e32 v2, 0x43800000, v50
	v_mul_f32_e32 v48, 0x43800000, v58
	v_mov_b32_e32 v56, v3
	v_cvt_pk_fp8_f32 v56, v2, v48
	v_mul_f32_e32 v2, 0x43800000, v51
	v_mul_f32_e32 v48, 0x43800000, v59
	v_mov_b32_e32 v51, v3
	v_cvt_pk_fp8_f32 v51, v2, v48
	s_waitcnt vmcnt(7)
	v_mul_f32_e32 v2, 0x43800000, v36
	s_waitcnt vmcnt(5)
; #define LAS __attribute__((address_space(3)))
; __device__ __forceinline__ unsigned pk4_fp8(float a, float b, float c, float d) { unsigned w = 0u; w = __builtin_amdgcn_cvt_pk_fp8_f32(a, b, w, false); w = __builtin_amdgcn_cvt_pk_fp8_f32(c, d, w, true); return w; }
; __device__ __forceinline__ void conv_item8(const float* W, int K, int N, unsigned char* WT, int k0, int n0, int drow0, LAS unsigned* scr, int lane, float sc, bool rperm = false) {
;     ...
;         for (int t = 0; t < 4; ++t) v[i][t] = __builtin_nontemporal_load((const f32x4*)(W + (size_t)(k0 + 4 * (4 * i + q) + t) * N + n0 + 4 * n4));
; #pragma unroll
;     for (int i = 0; i < 4; ++i) { const int rp = 4 * i + q; LAS unsigned* sp = scr + (4 * n4) * 17 + rp;
;         sp[0]  = pk4_fp8(v[i][0].x * sc, v[i][1].x * sc, v[i][2].x * sc, v[i][3].x * sc);
;         sp[17] = pk4_fp8(v[i][0].y * sc, v[i][1].y * sc, v[i][2].y * sc, v[i][3].y * sc);
;         sp[34] = pk4_fp8(v[i][0].z * sc, v[i][1].z * sc, v[i][2].z * sc, v[i][3].z * sc);
;         sp[51] = pk4_fp8(v[i][0].w * sc, v[i][1].w * sc, v[i][2].w * sc, v[i][3].w * sc); }
;     asm volatile("s_waitcnt lgkmcnt(0)" ::: "memory");
;     const int c = lane & 3;
; #pragma unroll
;     for (int j = 0; j < 4; ++j) {
;         const int n = (lane >> 2) + 16 * j; const LAS unsigned* sp = scr + n * 17 + 4 * c;
;         u32x4 o; o.x = sp[0]; o.y = sp[1]; o.z = sp[2]; o.w = sp[3];
;         const int nr = (rperm && n < 32) ? ((n < 16) ? 2 * n : 2 * (n - 16) + 1) : n;
;         *(u32x4*)(WT + (size_t)(drow0 + nr) * K + k0 + 16 * c) = o;
;     }
;     asm volatile("s_waitcnt lgkmcnt(0)" ::: "memory");
	v_mul_f32_e32 v36, 0x43800000, v40
	v_mov_b32_e32 v48, v3
	v_cvt_pk_fp8_f32 v48, v2, v36
	v_mul_f32_e32 v2, 0x43800000, v37
	v_mul_f32_e32 v36, 0x43800000, v41
	v_mov_b32_e32 v41, v3
	v_cvt_pk_fp8_f32 v41, v2, v36
	v_mul_f32_e32 v2, 0x43800000, v38
	v_mul_f32_e32 v36, 0x43800000, v42
	v_mul_f32_e32 v49, 0x43800000, v62
	v_mul_f32_e32 v50, 0x43800000, v66
	v_cvt_pk_fp8_f32 v56, v49, v50 op_sel:[0,0,1]
	v_mul_f32_e32 v49, 0x43800000, v63
	v_mul_f32_e32 v50, 0x43800000, v67
	v_cvt_pk_fp8_f32 v51, v49, v50 op_sel:[0,0,1]
	s_waitcnt vmcnt(3)
	v_mul_f32_e32 v40, 0x43800000, v44
	v_mul_f32_e32 v37, 0x43800000, v45
	s_waitcnt vmcnt(2)
	v_mul_f32_e32 v44, 0x43800000, v52
	v_cvt_pk_fp8_f32 v48, v40, v44 op_sel:[0,0,1]
	v_mul_f32_e32 v40, 0x43800000, v53
	v_cvt_pk_fp8_f32 v41, v37, v40 op_sel:[0,0,1]
	v_mov_b32_e32 v40, v3
	v_cvt_pk_fp8_f32 v40, v2, v36
	v_mul_f32_e32 v2, 0x43800000, v39
	v_mul_f32_e32 v36, 0x43800000, v43
	v_mov_b32_e32 v39, v3
	v_cvt_pk_fp8_f32 v39, v2, v36
	s_waitcnt vmcnt(1)
	v_mul_f32_e32 v2, 0x43800000, v4
	v_mul_f32_e32 v4, 0x43800000, v8
	v_mul_f32_e32 v8, 0x43800000, v12
	v_mul_f32_e32 v12, 0x43800000, v32
	v_mov_b32_e32 v32, v3
	v_cvt_pk_fp8_f32 v32, v2, v4
	v_mul_f32_e32 v2, 0x43800000, v5
	v_mul_f32_e32 v4, 0x43800000, v9
	v_mov_b32_e32 v9, v3
	v_cvt_pk_fp8_f32 v9, v2, v4
	v_cvt_pk_fp8_f32 v32, v8, v12 op_sel:[0,0,1]
	v_mul_f32_e32 v5, 0x43800000, v13
	v_mul_f32_e32 v8, 0x43800000, v33
	v_cvt_pk_fp8_f32 v9, v5, v8 op_sel:[0,0,1]
	v_mul_f32_e32 v2, 0x43800000, v6
	v_mul_f32_e32 v4, 0x43800000, v10
	v_mov_b32_e32 v8, v3
	v_cvt_pk_fp8_f32 v8, v2, v4
	v_mul_f32_e32 v2, 0x43800000, v7
	v_mul_f32_e32 v4, 0x43800000, v11
	v_mov_b32_e32 v7, v3
	v_cvt_pk_fp8_f32 v7, v2, v4
	v_mul_f32_e32 v2, 0x43800000, v16
	v_mul_f32_e32 v4, 0x43800000, v20
	v_mov_b32_e32 v10, v3
	v_cvt_pk_fp8_f32 v10, v2, v4
	v_mul_f32_e32 v5, 0x43800000, v14
	v_mul_f32_e32 v6, 0x43800000, v34
	v_cvt_pk_fp8_f32 v8, v5, v6 op_sel:[0,0,1]
	v_mul_f32_e32 v5, 0x43800000, v15
	v_mul_f32_e32 v6, 0x43800000, v35
	v_cvt_pk_fp8_f32 v7, v5, v6 op_sel:[0,0,1]
	v_mul_f32_e32 v5, 0x43800000, v24
	s_waitcnt vmcnt(0)
	v_mul_f32_e32 v6, 0x43800000, v28
	v_cvt_pk_fp8_f32 v10, v5, v6 op_sel:[0,0,1]
	v_mul_f32_e32 v2, 0x43800000, v17
	v_mul_f32_e32 v4, 0x43800000, v21
	v_mul_f32_e32 v5, 0x43800000, v25
	ds_write2_b32 v81, v32, v10 offset0:8 offset1:12
	v_mov_b32_e32 v10, v3
	v_cvt_pk_fp8_f32 v10, v2, v4
	v_mul_f32_e32 v6, 0x43800000, v29
	v_mul_f32_e32 v2, 0x43800000, v18
	v_mul_f32_e32 v4, 0x43800000, v22
	v_cvt_pk_fp8_f32 v10, v5, v6 op_sel:[0,0,1]
	v_mul_f32_e32 v5, 0x43800000, v26
	v_mul_f32_e32 v6, 0x43800000, v30
	v_mul_f32_e32 v37, 0x43800000, v46
	ds_write2_b32 v81, v9, v10 offset0:25 offset1:29
	v_mov_b32_e32 v9, v3
	v_cvt_pk_fp8_f32 v9, v2, v4
	v_mul_f32_e32 v2, 0x43800000, v19
	v_mul_f32_e32 v4, 0x43800000, v23
	v_mul_f32_e32 v38, 0x43800000, v54
	v_cvt_pk_fp8_f32 v9, v5, v6 op_sel:[0,0,1]
	v_cvt_pk_fp8_f32 v40, v37, v38 op_sel:[0,0,1]
	v_mul_f32_e32 v37, 0x43800000, v47
	v_mul_f32_e32 v38, 0x43800000, v55
	ds_write2_b32 v81, v8, v9 offset0:42 offset1:46
	v_mov_b32_e32 v8, v3
	v_cvt_pk_fp8_f32 v8, v2, v4
	v_mul_f32_e32 v5, 0x43800000, v27
	v_mul_f32_e32 v6, 0x43800000, v31
	v_cvt_pk_fp8_f32 v39, v37, v38 op_sel:[0,0,1]
	v_cvt_pk_fp8_f32 v8, v5, v6 op_sel:[0,0,1]
	ds_write2_b32 v81, v64, v48 offset1:4
	ds_write2_b32 v81, v57, v41 offset0:17 offset1:21
	ds_write2_b32 v81, v56, v40 offset0:34 offset1:38
	ds_write2_b32 v81, v51, v39 offset0:51 offset1:55
	ds_write2_b32 v81, v7, v8 offset0:59 offset1:63
	s_waitcnt lgkmcnt(0)
	v_lshl_add_u64 v[4:5], v[74:75], 0, v[76:77]
	v_lshl_add_u64 v[8:9], v[4:5], 0, v[68:69]
	ds_read2_b32 v[4:5], v88 offset1:1
	ds_read2_b32 v[6:7], v88 offset0:2 offset1:3
	v_or_b32_e32 v10, v72, v82
	v_ashrrev_i32_e32 v11, 31, v10
	v_lshlrev_b64 v[10:11], 11, v[10:11]
	v_lshl_add_u64 v[10:11], v[8:9], 0, v[10:11]
	s_waitcnt lgkmcnt(0)
	global_store_dwordx4 v[10:11], v[4:7], off
	ds_read2_b32 v[4:5], v89 offset1:1
	ds_read2_b32 v[6:7], v90 offset1:1
	v_or_b32_e32 v10, v72, v83
	v_ashrrev_i32_e32 v11, 31, v10
	v_lshlrev_b64 v[10:11], 11, v[10:11]
	v_lshl_add_u64 v[10:11], v[8:9], 0, v[10:11]
	s_waitcnt lgkmcnt(0)
	global_store_dwordx4 v[10:11], v[4:7], off
	ds_read2_b32 v[4:5], v91 offset1:1
	ds_read2_b32 v[6:7], v92 offset1:1
	v_or_b32_e32 v10, v72, v84
	v_ashrrev_i32_e32 v11, 31, v10
	v_lshlrev_b64 v[10:11], 11, v[10:11]
	v_lshl_add_u64 v[10:11], v[8:9], 0, v[10:11]
	s_waitcnt lgkmcnt(0)
	global_store_dwordx4 v[10:11], v[4:7], off
	ds_read2_b32 v[4:5], v93 offset1:1
	ds_read2_b32 v[6:7], v94 offset1:1
	v_or_b32_e32 v10, v72, v85
	v_ashrrev_i32_e32 v11, 31, v10
	v_lshlrev_b64 v[10:11], 11, v[10:11]
	v_lshl_add_u64 v[8:9], v[8:9], 0, v[10:11]
	s_waitcnt lgkmcnt(0)
	global_store_dwordx4 v[8:9], v[4:7], off
	s_waitcnt lgkmcnt(0)

; #define LAS __attribute__((address_space(3)))
; __device__ __forceinline__ unsigned pk4_fp8(float a, float b, float c, float d) { unsigned w = 0u; w = __builtin_amdgcn_cvt_pk_fp8_f32(a, b, w, false); w = __builtin_amdgcn_cvt_pk_fp8_f32(c, d, w, true); return w; }
; __device__ __forceinline__ void conv_item8(const float* W, int K, int N, unsigned char* WT, int k0, int n0, int drow0, LAS unsigned* scr, int lane, float sc, bool rperm = false) {
;     const int q = lane >> 4, n4 = lane & 15;
;     f32x4 v[4][4];
; #pragma unroll
;     for (int i = 0; i < 4; ++i)
; #pragma unroll
;         for (int t = 0; t < 4; ++t) v[i][t] = __builtin_nontemporal_load((const f32x4*)(W + (size_t)(k0 + 4 * (4 * i + q) + t) * N + n0 + 4 * n4));
; #pragma unroll
;     for (int i = 0; i < 4; ++i) { const int rp = 4 * i + q; LAS unsigned* sp = scr + (4 * n4) * 17 + rp;
;         sp[0]  = pk4_fp8(v[i][0].x * sc, v[i][1].x * sc, v[i][2].x * sc, v[i][3].x * sc);
;         sp[17] = pk4_fp8(v[i][0].y * sc, v[i][1].y * sc, v[i][2].y * sc, v[i][3].y * sc);
;         sp[34] = pk4_fp8(v[i][0].z * sc, v[i][1].z * sc, v[i][2].z * sc, v[i][3].z * sc);
;         sp[51] = pk4_fp8(v[i][0].w * sc, v[i][1].w * sc, v[i][2].w * sc, v[i][3].w * sc); }
; __device__ __forceinline__ void conv_dispatch(const Params& p, int it, LAS unsigned* scr, int lane) {
;     ...
;     if (r < i_in) { const int N = l ? ODW : EVW, nb = N / 64;
;         conv_item8(p.in[l ? 16 : 5], D, N, l ? p.wp[IX_WIN1] : p.wp[IX_WIN0], (r / nb) * 64, (r % nb) * 64, (r % nb) * 64, scr, lane, F8_SW, l == 1 && (r % nb) < 64 && ((r % nb) & 1) == 0);
;         return; } r -= i_in;
.LBB0_930:
	s_andn2_saveexec_b64 s[86:87], s[8:9]
	s_cbranch_execz .LBB0_919
	v_cndmask_b32_e32 v2, 40, v95, vcc
	v_lshl_add_u64 v[6:7], s[0:1], 0, v[2:3]
	global_load_dwordx2 v[6:7], v[6:7], off
	v_cndmask_b32_e32 v18, v98, v99, vcc
	v_lshrrev_b32_e32 v5, 6, v18
	v_sub_u32_e32 v9, 0, v5
	v_max_i32_e32 v9, v5, v9
	v_cvt_f32_u32_e32 v10, v9
	v_mov_b32_e32 v2, s45
	v_mov_b32_e32 v8, s47
	v_sub_u32_e32 v11, 0, v9
	v_rcp_iflag_f32_e32 v10, v10
	v_cndmask_b32_e32 v73, v2, v8, vcc
	v_mov_b32_e32 v2, s44
	v_mov_b32_e32 v8, s46
	v_mul_f32_e32 v10, 0x4f7ffffe, v10
	v_cvt_u32_f32_e32 v10, v10
	v_cndmask_b32_e32 v72, v2, v8, vcc
	v_sub_u32_e32 v8, 0, v4
	v_max_i32_e32 v8, v4, v8
	v_mul_lo_u32 v11, v11, v10
	v_mul_hi_u32 v11, v10, v11
	v_add_u32_e32 v10, v10, v11
	v_mul_hi_u32 v10, v8, v10
	v_mul_lo_u32 v11, v10, v9
	v_sub_u32_e32 v8, v8, v11
	v_cmp_ge_u32_e64 s[6:7], v8, v9
	v_add_u32_e32 v11, 1, v10
	v_xor_b32_e32 v2, v4, v5
	v_cndmask_b32_e64 v10, v10, v11, s[6:7]
	v_sub_u32_e32 v11, v8, v9
	v_cndmask_b32_e64 v8, v8, v11, s[6:7]
	v_cmp_ge_u32_e64 s[6:7], v8, v9
	v_add_u32_e32 v8, 1, v10
	v_ashrrev_i32_e32 v2, 31, v2
	v_cndmask_b32_e64 v8, v10, v8, s[6:7]
	v_xor_b32_e32 v8, v8, v2
	v_sub_u32_e32 v2, v8, v2
	v_lshlrev_b32_e32 v76, 6, v2
	v_mul_lo_u32 v2, v2, v5
	v_sub_u32_e32 v2, v4, v2
	v_lshlrev_b32_e32 v74, 6, v2
	v_cmp_gt_i32_e64 s[6:7], 64, v2
	v_and_b32_e32 v2, 1, v2
	v_cmp_eq_u32_e64 s[8:9], 0, v2
	v_or_b32_e32 v2, v76, v80
	v_ashrrev_i32_e32 v75, 31, v74
	s_and_b64 s[6:7], s[6:7], s[8:9]
	v_mov_b32_e32 v71, v3
	v_or_b32_e32 v8, 49, v2
	s_and_b64 vcc, vcc, s[6:7]
	v_mad_i64_i32 v[8:9], s[6:7], v8, v18, 0
	v_or_b32_e32 v12, 50, v2
	v_mad_i64_i32 v[12:13], s[6:7], v12, v18, 0
	v_ashrrev_i32_e32 v77, 31, v76
	s_waitcnt vmcnt(0)
	v_lshl_add_u64 v[4:5], v[74:75], 2, v[6:7]
	v_lshl_add_u64 v[16:17], v[4:5], 0, v[70:71]
	v_mad_i64_i32 v[4:5], s[6:7], v2, v18, 0
	v_lshl_add_u64 v[4:5], v[4:5], 2, v[16:17]
	v_lshl_add_u64 v[8:9], v[8:9], 2, v[16:17]
	global_load_dwordx4 v[52:55], v[4:5], off nt
	v_lshl_add_u64 v[12:13], v[12:13], 2, v[16:17]
	global_load_dwordx4 v[8:11], v[8:9], off nt
	v_or_b32_e32 v4, 1, v2
	v_mad_i64_i32 v[4:5], s[6:7], v4, v18, 0
	v_lshl_add_u64 v[4:5], v[4:5], 2, v[16:17]
	global_load_dwordx4 v[56:59], v[4:5], off nt
	s_nop 0
	global_load_dwordx4 v[12:15], v[12:13], off nt
	v_or_b32_e32 v4, 2, v2
	v_mad_i64_i32 v[4:5], s[6:7], v4, v18, 0
	v_lshl_add_u64 v[4:5], v[4:5], 2, v[16:17]
	global_load_dwordx4 v[60:63], v[4:5], off nt
	v_or_b32_e32 v4, 3, v2
	v_mad_i64_i32 v[4:5], s[6:7], v4, v18, 0
	v_lshl_add_u64 v[4:5], v[4:5], 2, v[16:17]
	global_load_dwordx4 v[64:67], v[4:5], off nt
	v_or_b32_e32 v4, 16, v2
	v_mad_i64_i32 v[4:5], s[6:7], v4, v18, 0
	v_lshl_add_u64 v[4:5], v[4:5], 2, v[16:17]
	global_load_dwordx4 v[20:23], v[4:5], off nt
	v_or_b32_e32 v4, 17, v2
	v_mad_i64_i32 v[4:5], s[6:7], v4, v18, 0
	v_lshl_add_u64 v[4:5], v[4:5], 2, v[16:17]
	global_load_dwordx4 v[24:27], v[4:5], off nt
	v_or_b32_e32 v4, 18, v2
	v_mad_i64_i32 v[4:5], s[6:7], v4, v18, 0
	v_lshl_add_u64 v[4:5], v[4:5], 2, v[16:17]
	global_load_dwordx4 v[28:31], v[4:5], off nt
	v_or_b32_e32 v4, 19, v2
	v_mad_i64_i32 v[4:5], s[6:7], v4, v18, 0
	v_lshl_add_u64 v[4:5], v[4:5], 2, v[16:17]
	global_load_dwordx4 v[48:51], v[4:5], off nt
	v_or_b32_e32 v4, 32, v2
	v_mad_i64_i32 v[4:5], s[6:7], v4, v18, 0
	v_lshl_add_u64 v[4:5], v[4:5], 2, v[16:17]
	global_load_dwordx4 v[32:35], v[4:5], off nt
	v_or_b32_e32 v4, 33, v2
	v_mad_i64_i32 v[4:5], s[6:7], v4, v18, 0
	v_lshl_add_u64 v[4:5], v[4:5], 2, v[16:17]
	global_load_dwordx4 v[36:39], v[4:5], off nt
	v_or_b32_e32 v4, 34, v2
	v_mad_i64_i32 v[4:5], s[6:7], v4, v18, 0
	v_lshl_add_u64 v[4:5], v[4:5], 2, v[16:17]
	global_load_dwordx4 v[40:43], v[4:5], off nt
	v_or_b32_e32 v4, 35, v2
	v_mad_i64_i32 v[4:5], s[6:7], v4, v18, 0
	v_lshl_add_u64 v[4:5], v[4:5], 2, v[16:17]
	global_load_dwordx4 v[44:47], v[4:5], off nt
	v_or_b32_e32 v4, 48, v2
	v_or_b32_e32 v2, 51, v2
	v_mad_i64_i32 v[4:5], s[6:7], v4, v18, 0
	v_mad_i64_i32 v[18:19], s[6:7], v2, v18, 0
	v_lshl_add_u64 v[4:5], v[4:5], 2, v[16:17]
	v_lshl_add_u64 v[16:17], v[18:19], 2, v[16:17]
	global_load_dwordx4 v[4:7], v[4:5], off nt
	global_load_dwordx4 v[16:19], v[16:17], off nt
	s_waitcnt vmcnt(15)
	v_mul_f32_e32 v2, 0x43800000, v52
	s_waitcnt vmcnt(13)
	v_mul_f32_e32 v52, 0x43800000, v56
	s_waitcnt vmcnt(11)
	v_mul_f32_e32 v56, 0x43800000, v60
	s_waitcnt vmcnt(10)
	v_mul_f32_e32 v60, 0x43800000, v64
	v_mov_b32_e32 v64, v3
	v_cvt_pk_fp8_f32 v64, v2, v52
	v_mul_f32_e32 v2, 0x43800000, v53
	v_mul_f32_e32 v52, 0x43800000, v57
	v_mov_b32_e32 v57, v3
	v_cvt_pk_fp8_f32 v57, v2, v52
	v_cvt_pk_fp8_f32 v64, v56, v60 op_sel:[0,0,1]
	v_mul_f32_e32 v53, 0x43800000, v61
	v_mul_f32_e32 v56, 0x43800000, v65
	v_cvt_pk_fp8_f32 v57, v53, v56 op_sel:[0,0,1]
	v_mul_f32_e32 v2, 0x43800000, v54
	v_mul_f32_e32 v52, 0x43800000, v58
	v_mov_b32_e32 v56, v3
	v_cvt_pk_fp8_f32 v56, v2, v52
	v_mul_f32_e32 v2, 0x43800000, v55
	v_mul_f32_e32 v52, 0x43800000, v59
	v_mov_b32_e32 v55, v3
	v_cvt_pk_fp8_f32 v55, v2, v52
	s_waitcnt vmcnt(9)
; #define LAS __attribute__((address_space(3)))
; __device__ __forceinline__ unsigned pk4_fp8(float a, float b, float c, float d) { unsigned w = 0u; w = __builtin_amdgcn_cvt_pk_fp8_f32(a, b, w, false); w = __builtin_amdgcn_cvt_pk_fp8_f32(c, d, w, true); return w; }
; __device__ __forceinline__ void conv_item8(const float* W, int K, int N, unsigned char* WT, int k0, int n0, int drow0, LAS unsigned* scr, int lane, float sc, bool rperm = false) {
;     ...
;         for (int t = 0; t < 4; ++t) v[i][t] = __builtin_nontemporal_load((const f32x4*)(W + (size_t)(k0 + 4 * (4 * i + q) + t) * N + n0 + 4 * n4));
; #pragma unroll
;     for (int i = 0; i < 4; ++i) { const int rp = 4 * i + q; LAS unsigned* sp = scr + (4 * n4) * 17 + rp;
;         sp[0]  = pk4_fp8(v[i][0].x * sc, v[i][1].x * sc, v[i][2].x * sc, v[i][3].x * sc);
;         sp[17] = pk4_fp8(v[i][0].y * sc, v[i][1].y * sc, v[i][2].y * sc, v[i][3].y * sc);
;         sp[34] = pk4_fp8(v[i][0].z * sc, v[i][1].z * sc, v[i][2].z * sc, v[i][3].z * sc);
;         sp[51] = pk4_fp8(v[i][0].w * sc, v[i][1].w * sc, v[i][2].w * sc, v[i][3].w * sc); }
;     asm volatile("s_waitcnt lgkmcnt(0)" ::: "memory");
;     const int c = lane & 3;
; #pragma unroll
;     for (int j = 0; j < 4; ++j) {
;         const int n = (lane >> 2) + 16 * j; const LAS unsigned* sp = scr + n * 17 + 4 * c;
;         u32x4 o; o.x = sp[0]; o.y = sp[1]; o.z = sp[2]; o.w = sp[3];
;         const int nr = (rperm && n < 32) ? ((n < 16) ? 2 * n : 2 * (n - 16) + 1) : n;
;         *(u32x4*)(WT + (size_t)(drow0 + nr) * K + k0 + 16 * c) = o;
;     }
;     asm volatile("s_waitcnt lgkmcnt(0)" ::: "memory");
; __device__ __forceinline__ void conv_dispatch(const Params& p, int it, LAS unsigned* scr, int lane) {
;     ...
;     if (r < i_in) { const int N = l ? ODW : EVW, nb = N / 64;
;         conv_item8(p.in[l ? 16 : 5], D, N, l ? p.wp[IX_WIN1] : p.wp[IX_WIN0], (r / nb) * 64, (r % nb) * 64, (r % nb) * 64, scr, lane, F8_SW, l == 1 && (r % nb) < 64 && ((r % nb) & 1) == 0);
	v_mul_f32_e32 v2, 0x43800000, v20
	s_waitcnt vmcnt(8)
	v_mul_f32_e32 v20, 0x43800000, v24
	s_waitcnt vmcnt(7)
	v_mul_f32_e32 v24, 0x43800000, v28
	s_waitcnt vmcnt(6)
	v_mul_f32_e32 v28, 0x43800000, v48
	v_mov_b32_e32 v48, v3
	v_cvt_pk_fp8_f32 v48, v2, v20
	v_mul_f32_e32 v2, 0x43800000, v21
	v_mul_f32_e32 v20, 0x43800000, v25
	v_mov_b32_e32 v25, v3
	v_cvt_pk_fp8_f32 v25, v2, v20
	v_cvt_pk_fp8_f32 v48, v24, v28 op_sel:[0,0,1]
	v_mul_f32_e32 v21, 0x43800000, v29
	v_mul_f32_e32 v24, 0x43800000, v49
	v_cvt_pk_fp8_f32 v25, v21, v24 op_sel:[0,0,1]
	v_mul_f32_e32 v2, 0x43800000, v22
	v_mul_f32_e32 v20, 0x43800000, v26
	v_mov_b32_e32 v24, v3
	v_cvt_pk_fp8_f32 v24, v2, v20
	v_mul_f32_e32 v2, 0x43800000, v23
	v_mul_f32_e32 v20, 0x43800000, v27
	v_mov_b32_e32 v23, v3
	v_cvt_pk_fp8_f32 v23, v2, v20
	v_mul_f32_e32 v53, 0x43800000, v62
	v_mul_f32_e32 v54, 0x43800000, v66
	v_mul_f32_e32 v21, 0x43800000, v30
	v_mul_f32_e32 v22, 0x43800000, v50
	v_cvt_pk_fp8_f32 v56, v53, v54 op_sel:[0,0,1]
	v_mul_f32_e32 v53, 0x43800000, v63
	v_mul_f32_e32 v54, 0x43800000, v67
	v_cvt_pk_fp8_f32 v24, v21, v22 op_sel:[0,0,1]
	v_mul_f32_e32 v21, 0x43800000, v31
	v_mul_f32_e32 v22, 0x43800000, v51
	v_cvt_pk_fp8_f32 v55, v53, v54 op_sel:[0,0,1]
	v_cvt_pk_fp8_f32 v23, v21, v22 op_sel:[0,0,1]
	s_waitcnt vmcnt(5)
	v_mul_f32_e32 v2, 0x43800000, v32
	s_waitcnt vmcnt(4)
	v_mul_f32_e32 v20, 0x43800000, v36
	ds_write2_b32 v81, v56, v24 offset0:34 offset1:38
	ds_write2_b32 v81, v55, v23 offset0:51 offset1:55
	v_mov_b32_e32 v23, v3
	v_cvt_pk_fp8_f32 v23, v2, v20
	v_mul_f32_e32 v2, 0x43800000, v33
	v_mul_f32_e32 v20, 0x43800000, v37
	v_mov_b32_e32 v24, v3
	ds_write2_b32 v81, v57, v25 offset0:17 offset1:21
	v_cvt_pk_fp8_f32 v24, v2, v20
	v_mul_f32_e32 v2, 0x43800000, v34
	v_mul_f32_e32 v20, 0x43800000, v38
	v_mov_b32_e32 v25, v3
	v_cvt_pk_fp8_f32 v25, v2, v20
	v_mul_f32_e32 v2, 0x43800000, v35
	v_mul_f32_e32 v20, 0x43800000, v39
	v_mov_b32_e32 v26, v3
	v_cvt_pk_fp8_f32 v26, v2, v20
	s_waitcnt vmcnt(1)
	v_mul_f32_e32 v2, 0x43800000, v4
	v_mul_f32_e32 v4, 0x43800000, v8
	v_mul_f32_e32 v8, 0x43800000, v12
	s_waitcnt vmcnt(0)
	v_mul_f32_e32 v12, 0x43800000, v16
	v_mov_b32_e32 v16, v3
	v_cvt_pk_fp8_f32 v16, v2, v4
	v_mul_f32_e32 v2, 0x43800000, v5
	v_mul_f32_e32 v4, 0x43800000, v9
	v_mov_b32_e32 v9, v3
	v_cvt_pk_fp8_f32 v9, v2, v4
	v_cvt_pk_fp8_f32 v16, v8, v12 op_sel:[0,0,1]
	v_mul_f32_e32 v5, 0x43800000, v13
	v_mul_f32_e32 v8, 0x43800000, v17
	v_cvt_pk_fp8_f32 v9, v5, v8 op_sel:[0,0,1]
	v_mul_f32_e32 v2, 0x43800000, v6
	v_mul_f32_e32 v4, 0x43800000, v10
	v_mov_b32_e32 v8, v3
	v_cvt_pk_fp8_f32 v8, v2, v4
	v_mul_f32_e32 v2, 0x43800000, v7
	v_mul_f32_e32 v4, 0x43800000, v11
	v_mov_b32_e32 v7, v3
	v_mul_f32_e32 v21, 0x43800000, v40
	v_mul_f32_e32 v22, 0x43800000, v44
	v_cvt_pk_fp8_f32 v7, v2, v4
	v_cvt_pk_fp8_f32 v23, v21, v22 op_sel:[0,0,1]
	v_mul_f32_e32 v21, 0x43800000, v41
	v_mul_f32_e32 v22, 0x43800000, v45
	v_cvt_pk_fp8_f32 v24, v21, v22 op_sel:[0,0,1]
	v_mul_f32_e32 v21, 0x43800000, v42
	v_mul_f32_e32 v22, 0x43800000, v46
	v_mul_f32_e32 v5, 0x43800000, v14
	v_mul_f32_e32 v6, 0x43800000, v18
	v_cvt_pk_fp8_f32 v25, v21, v22 op_sel:[0,0,1]
	v_mul_f32_e32 v21, 0x43800000, v43
	v_mul_f32_e32 v22, 0x43800000, v47
	v_cvt_pk_fp8_f32 v8, v5, v6 op_sel:[0,0,1]
	v_mul_f32_e32 v5, 0x43800000, v15
	v_mul_f32_e32 v6, 0x43800000, v19
	v_cvt_pk_fp8_f32 v26, v21, v22 op_sel:[0,0,1]
	v_cvt_pk_fp8_f32 v7, v5, v6 op_sel:[0,0,1]
	ds_write2_b32 v81, v64, v48 offset1:4
	ds_write2_b32 v81, v23, v16 offset0:8 offset1:12
	ds_write2_b32 v81, v24, v9 offset0:25 offset1:29
	ds_write2_b32 v81, v25, v8 offset0:42 offset1:46
	ds_write2_b32 v81, v26, v7 offset0:59 offset1:63
	s_waitcnt lgkmcnt(0)
	v_lshl_add_u64 v[4:5], v[72:73], 0, v[76:77]
	v_lshl_add_u64 v[8:9], v[4:5], 0, v[68:69]
	ds_read2_b32 v[4:5], v88 offset1:1
	ds_read2_b32 v[6:7], v88 offset0:2 offset1:3
	v_cndmask_b32_e64 v2, 0, 1, vcc
	v_lshl_or_b32 v10, v82, v2, v74
	v_ashrrev_i32_e32 v11, 31, v10
	v_lshlrev_b64 v[10:11], 11, v[10:11]
	v_lshl_add_u64 v[10:11], v[8:9], 0, v[10:11]
	s_waitcnt lgkmcnt(0)
	global_store_dwordx4 v[10:11], v[4:7], off
	ds_read2_b32 v[4:5], v89 offset1:1
	ds_read2_b32 v[6:7], v90 offset1:1
	v_cndmask_b32_e32 v2, v83, v86, vcc
	v_or_b32_e32 v10, v2, v74
	v_ashrrev_i32_e32 v11, 31, v10
	v_lshlrev_b64 v[10:11], 11, v[10:11]
	v_lshl_add_u64 v[10:11], v[8:9], 0, v[10:11]
	s_waitcnt lgkmcnt(0)
	global_store_dwordx4 v[10:11], v[4:7], off
	ds_read2_b32 v[4:5], v91 offset1:1
	ds_read2_b32 v[6:7], v92 offset1:1
	v_or_b32_e32 v10, v74, v84
	v_ashrrev_i32_e32 v11, 31, v10
	v_lshlrev_b64 v[10:11], 11, v[10:11]
	v_lshl_add_u64 v[10:11], v[8:9], 0, v[10:11]
	s_waitcnt lgkmcnt(0)
	global_store_dwordx4 v[10:11], v[4:7], off
	ds_read2_b32 v[4:5], v93 offset1:1
	ds_read2_b32 v[6:7], v94 offset1:1
	v_or_b32_e32 v10, v74, v85
	v_ashrrev_i32_e32 v11, 31, v10
	v_lshlrev_b64 v[10:11], 11, v[10:11]
	v_lshl_add_u64 v[8:9], v[8:9], 0, v[10:11]
	s_waitcnt lgkmcnt(0)
	global_store_dwordx4 v[8:9], v[4:7], off
	s_waitcnt lgkmcnt(0)
	s_branch .LBB0_919

; #define LAS __attribute__((address_space(3)))
; __device__ __forceinline__ unsigned pk4_fp8(float a, float b, float c, float d) { unsigned w = 0u; w = __builtin_amdgcn_cvt_pk_fp8_f32(a, b, w, false); w = __builtin_amdgcn_cvt_pk_fp8_f32(c, d, w, true); return w; }
; __device__ __forceinline__ void conv_item8(const float* W, int K, int N, unsigned char* WT, int k0, int n0, int drow0, LAS unsigned* scr, int lane, float sc, bool rperm = false) {
;     const int q = lane >> 4, n4 = lane & 15;
;     f32x4 v[4][4];
; #pragma unroll
;     for (int i = 0; i < 4; ++i)
; #pragma unroll
;         for (int t = 0; t < 4; ++t) v[i][t] = __builtin_nontemporal_load((const f32x4*)(W + (size_t)(k0 + 4 * (4 * i + q) + t) * N + n0 + 4 * n4));
; #pragma unroll
;     for (int i = 0; i < 4; ++i) { const int rp = 4 * i + q; LAS unsigned* sp = scr + (4 * n4) * 17 + rp;
;         sp[0]  = pk4_fp8(v[i][0].x * sc, v[i][1].x * sc, v[i][2].x * sc, v[i][3].x * sc);
;         sp[17] = pk4_fp8(v[i][0].y * sc, v[i][1].y * sc, v[i][2].y * sc, v[i][3].y * sc);
;         sp[34] = pk4_fp8(v[i][0].z * sc, v[i][1].z * sc, v[i][2].z * sc, v[i][3].z * sc);
;         sp[51] = pk4_fp8(v[i][0].w * sc, v[i][1].w * sc, v[i][2].w * sc, v[i][3].w * sc); }
; __device__ __forceinline__ void conv_dispatch(const Params& p, int it, LAS unsigned* scr, int lane) {
;     ...
;     { const int e = r / 512, rr = r % 512, kb = rr / 32, nb = rr % 32;
;         conv_item8(p.in[l ? 23 : 12] + (size_t)e * DFF * D, DFF, D, (l ? p.wp[IX_WD1] : p.wp[IX_WD0]) + (size_t)e * D * DFF, kb * 64, nb * 64, nb * 64, scr, lane, F8_SWD); }
.LBB0_953:
	s_movk_i32 s6, 0x73ff
	v_add_u32_e32 v0, 0xffff8c00, v1
	v_cmp_lt_i32_e32 vcc, s6, v1
	s_nop 1
	v_cndmask_b32_e32 v3, v86, v87, vcc
	v_cndmask_b32_e32 v2, v1, v0, vcc
	v_cmp_ge_i32_e64 s[6:7], v2, v3
	s_and_saveexec_b64 s[8:9], s[6:7]
	s_xor_b64 s[8:9], exec, s[8:9]
	s_cbranch_execz .LBB0_963
	v_sub_u32_e32 v4, v2, v3
	s_movk_i32 s6, 0x3ff
	v_cmp_lt_i32_e64 s[6:7], s6, v4
	s_and_saveexec_b64 s[22:23], s[6:7]
	s_xor_b64 s[22:23], exec, s[22:23]
	s_cbranch_execz .LBB0_960
	s_movk_i32 s6, 0x43ff
	v_cmp_lt_u32_e64 s[6:7], s6, v4
	s_and_saveexec_b64 s[24:25], s[6:7]
	s_xor_b64 s[24:25], exec, s[24:25]
	s_cbranch_execz .LBB0_957
	v_cndmask_b32_e32 v66, v96, v97, vcc
	s_waitcnt vmcnt(2)
	v_lshl_add_u64 v[6:7], s[0:1], 0, v[66:67]
	global_load_dwordx2 v[6:7], v[6:7], off
	v_add_u32_e32 v0, 0xffffbc00, v4
	v_lshrrev_b32_e32 v4, 9, v0
	v_mov_b32_e32 v5, v67
	v_lshlrev_b64 v[8:9], 23, v[4:5]
	v_mov_b32_e32 v0, s37
	v_mov_b32_e32 v3, s39
	v_mov_b32_e32 v71, v67
	v_lshlrev_b64 v[4:5], 21, v[4:5]
	v_mov_b32_e32 v75, v67
	s_waitcnt vmcnt(0)
	v_lshl_add_u64 v[6:7], v[6:7], 0, v[8:9]
	v_cndmask_b32_e32 v9, v0, v3, vcc
	v_mov_b32_e32 v0, s36
	v_mov_b32_e32 v3, s38
	v_cndmask_b32_e32 v8, v0, v3, vcc
	v_lshlrev_b32_e32 v0, 1, v2
	v_and_b32_e32 v74, 0x3c0, v0
	v_lshlrev_b32_e32 v0, 6, v2
	v_and_b32_e32 v76, 0x7c0, v0
	v_lshlrev_b32_e32 v66, 2, v76
	v_lshl_add_u64 v[2:3], v[6:7], 0, v[66:67]
	v_lshl_add_u64 v[2:3], v[2:3], 0, v[70:71]
	v_lshl_or_b32 v66, v74, 13, v88
	v_lshl_add_u64 v[14:15], v[2:3], 0, v[66:67]
	v_add_co_u32_e64 v2, s[6:7], s4, v14
	global_load_dwordx4 v[46:49], v[14:15], off nt
	s_nop 0
	v_addc_co_u32_e64 v3, s[6:7], 0, v15, s[6:7]
	s_movk_i32 s6, 0x4000
	global_load_dwordx4 v[50:53], v[2:3], off nt
	v_add_co_u32_e64 v2, s[6:7], s6, v14
	v_lshl_add_u64 v[72:73], v[8:9], 0, v[4:5]
	s_nop 0
	v_addc_co_u32_e64 v3, s[6:7], 0, v15, s[6:7]
	s_movk_i32 s6, 0x6000
	global_load_dwordx4 v[58:61], v[2:3], off nt
	v_add_co_u32_e64 v2, s[6:7], s6, v14
	s_nop 1
	v_addc_co_u32_e64 v3, s[6:7], 0, v15, s[6:7]
	s_mov_b32 s6, 0x20000
	global_load_dwordx4 v[62:65], v[2:3], off nt
	v_add_co_u32_e64 v2, s[6:7], s6, v14
	s_nop 1
	v_addc_co_u32_e64 v3, s[6:7], 0, v15, s[6:7]
	s_mov_b32 s6, 0x22000
	global_load_dwordx4 v[34:37], v[2:3], off nt
	v_add_co_u32_e64 v2, s[6:7], s6, v14
	s_nop 1
	v_addc_co_u32_e64 v3, s[6:7], 0, v15, s[6:7]
	s_mov_b32 s6, 0x24000
	global_load_dwordx4 v[38:41], v[2:3], off nt
	v_add_co_u32_e64 v2, s[6:7], s6, v14
	s_nop 1
	v_addc_co_u32_e64 v3, s[6:7], 0, v15, s[6:7]
	global_load_dwordx4 v[42:45], v[2:3], off nt
	v_add_co_u32_e64 v2, s[6:7], s5, v14
	s_nop 0
	s_nop 0
	v_addc_co_u32_e64 v3, s[6:7], 0, v15, s[6:7]
	global_load_dwordx4 v[54:57], v[2:3], off nt
	v_add_co_u32_e64 v2, s[6:7], s16, v14
	s_nop 0
	s_nop 0
	v_addc_co_u32_e64 v3, s[6:7], 0, v15, s[6:7]
	global_load_dwordx4 v[18:21], v[2:3], off nt
	v_add_co_u32_e64 v2, s[6:7], s17, v14
	s_nop 0
	s_nop 0
	v_addc_co_u32_e64 v3, s[6:7], 0, v15, s[6:7]
	global_load_dwordx4 v[22:25], v[2:3], off nt
	v_add_co_u32_e64 v2, s[6:7], s58, v14
	s_nop 0
	s_nop 0
	v_addc_co_u32_e64 v3, s[6:7], 0, v15, s[6:7]
	global_load_dwordx4 v[26:29], v[2:3], off nt
	v_add_co_u32_e64 v2, s[6:7], s59, v14
	s_nop 0
	s_nop 0
	v_addc_co_u32_e64 v3, s[6:7], 0, v15, s[6:7]
	global_load_dwordx4 v[30:33], v[2:3], off nt
	v_add_co_u32_e64 v2, s[6:7], s62, v14
	s_nop 0
	s_nop 0
	v_addc_co_u32_e64 v3, s[6:7], 0, v15, s[6:7]
	v_add_co_u32_e64 v6, s[6:7], s63, v14
	global_load_dwordx4 v[2:5], v[2:3], off nt
	s_nop 0
	v_addc_co_u32_e64 v7, s[6:7], 0, v15, s[6:7]
	v_add_co_u32_e64 v10, s[6:7], s64, v14
	global_load_dwordx4 v[6:9], v[6:7], off nt
	s_nop 0
	v_addc_co_u32_e64 v11, s[6:7], 0, v15, s[6:7]
	v_add_co_u32_e64 v14, s[6:7], s65, v14
	global_load_dwordx4 v[10:13], v[10:11], off nt
	s_nop 0
	v_addc_co_u32_e64 v15, s[6:7], 0, v15, s[6:7]
	global_load_dwordx4 v[14:17], v[14:15], off nt
	s_waitcnt vmcnt(15)
	v_mul_f32_e32 v0, 0x43800000, v46
	s_waitcnt vmcnt(14)
	v_mul_f32_e32 v46, 0x43800000, v50
	s_waitcnt vmcnt(13)
	v_mul_f32_e32 v50, 0x43800000, v58
	s_waitcnt vmcnt(12)
	v_mul_f32_e32 v58, 0x43800000, v62
	v_mov_b32_e32 v62, v67
	v_cvt_pk_fp8_f32 v62, v0, v46
	v_mul_f32_e32 v0, 0x43800000, v47
	v_mul_f32_e32 v46, 0x43800000, v51
	v_mov_b32_e32 v51, v67
	v_cvt_pk_fp8_f32 v51, v0, v46
	v_cvt_pk_fp8_f32 v62, v50, v58 op_sel:[0,0,1]
	v_mul_f32_e32 v47, 0x43800000, v59
	v_mul_f32_e32 v50, 0x43800000, v63
	v_cvt_pk_fp8_f32 v51, v47, v50 op_sel:[0,0,1]
	v_mul_f32_e32 v0, 0x43800000, v48
	v_mul_f32_e32 v46, 0x43800000, v52
	v_mov_b32_e32 v50, v67
	v_cvt_pk_fp8_f32 v50, v0, v46
	v_mul_f32_e32 v0, 0x43800000, v49
	v_mul_f32_e32 v46, 0x43800000, v53
	v_mov_b32_e32 v49, v67
	v_cvt_pk_fp8_f32 v49, v0, v46
	s_waitcnt vmcnt(11)
	v_mul_f32_e32 v0, 0x43800000, v34
	s_waitcnt vmcnt(10)
	v_mul_f32_e32 v34, 0x43800000, v38
	v_mov_b32_e32 v46, v67
	v_cvt_pk_fp8_f32 v46, v0, v34
	v_mul_f32_e32 v0, 0x43800000, v35
	v_mul_f32_e32 v34, 0x43800000, v39
	v_mov_b32_e32 v39, v67
	v_cvt_pk_fp8_f32 v39, v0, v34
	v_mul_f32_e32 v0, 0x43800000, v36
	v_mul_f32_e32 v34, 0x43800000, v40
	v_mul_f32_e32 v47, 0x43800000, v60
	v_mul_f32_e32 v48, 0x43800000, v64
	v_cvt_pk_fp8_f32 v50, v47, v48 op_sel:[0,0,1]
	v_mul_f32_e32 v47, 0x43800000, v61
	v_mul_f32_e32 v48, 0x43800000, v65
	v_cvt_pk_fp8_f32 v49, v47, v48 op_sel:[0,0,1]
	s_waitcnt vmcnt(9)
	v_mul_f32_e32 v38, 0x43800000, v42
	v_mul_f32_e32 v35, 0x43800000, v43
	s_waitcnt vmcnt(8)
	v_mul_f32_e32 v42, 0x43800000, v54
	v_cvt_pk_fp8_f32 v46, v38, v42 op_sel:[0,0,1]
	v_mul_f32_e32 v38, 0x43800000, v55
	v_cvt_pk_fp8_f32 v39, v35, v38 op_sel:[0,0,1]
	v_mov_b32_e32 v38, v67
	v_cvt_pk_fp8_f32 v38, v0, v34
	v_mul_f32_e32 v0, 0x43800000, v37
	v_mul_f32_e32 v34, 0x43800000, v41
	v_mov_b32_e32 v37, v67
	v_cvt_pk_fp8_f32 v37, v0, v34
	s_waitcnt vmcnt(7)
; #define LAS __attribute__((address_space(3)))
; __device__ __forceinline__ unsigned pk4_fp8(float a, float b, float c, float d) { unsigned w = 0u; w = __builtin_amdgcn_cvt_pk_fp8_f32(a, b, w, false); w = __builtin_amdgcn_cvt_pk_fp8_f32(c, d, w, true); return w; }
; __device__ __forceinline__ void conv_item8(const float* W, int K, int N, unsigned char* WT, int k0, int n0, int drow0, LAS unsigned* scr, int lane, float sc, bool rperm = false) {
;     ...
;         for (int t = 0; t < 4; ++t) v[i][t] = __builtin_nontemporal_load((const f32x4*)(W + (size_t)(k0 + 4 * (4 * i + q) + t) * N + n0 + 4 * n4));
; #pragma unroll
;     for (int i = 0; i < 4; ++i) { const int rp = 4 * i + q; LAS unsigned* sp = scr + (4 * n4) * 17 + rp;
;         sp[0]  = pk4_fp8(v[i][0].x * sc, v[i][1].x * sc, v[i][2].x * sc, v[i][3].x * sc);
;         sp[17] = pk4_fp8(v[i][0].y * sc, v[i][1].y * sc, v[i][2].y * sc, v[i][3].y * sc);
;         sp[34] = pk4_fp8(v[i][0].z * sc, v[i][1].z * sc, v[i][2].z * sc, v[i][3].z * sc);
;         sp[51] = pk4_fp8(v[i][0].w * sc, v[i][1].w * sc, v[i][2].w * sc, v[i][3].w * sc); }
;     asm volatile("s_waitcnt lgkmcnt(0)" ::: "memory");
;     const int c = lane & 3;
; #pragma unroll
;     for (int j = 0; j < 4; ++j) {
;         const int n = (lane >> 2) + 16 * j; const LAS unsigned* sp = scr + n * 17 + 4 * c;
;         u32x4 o; o.x = sp[0]; o.y = sp[1]; o.z = sp[2]; o.w = sp[3];
;         const int nr = (rperm && n < 32) ? ((n < 16) ? 2 * n : 2 * (n - 16) + 1) : n;
;         *(u32x4*)(WT + (size_t)(drow0 + nr) * K + k0 + 16 * c) = o;
;     }
; __device__ __forceinline__ void conv_dispatch(const Params& p, int it, LAS unsigned* scr, int lane) {
;     ...
;     if (r < 2 * I_G) { const int up = r >= I_G; if (up) r -= I_G; const int e = r / 512, rr = r % 512, kb = rr / 16, nb = rr % 16, n0 = nb * 64;
;         conv_item8(p.in[(l ? 21 : 10) + up] + (size_t)e * D * DFF, D, DFF, (l ? p.wp[IX_WGU1] : p.wp[IX_WGU0]) + (size_t)e * 2048 * D, kb * 64, n0, (n0 >> 7) * 256 + (n0 & 127) + up * 128, scr, lane, F8_SW);
	v_mul_f32_e32 v0, 0x43800000, v18
	v_mul_f32_e32 v35, 0x43800000, v44
	s_waitcnt vmcnt(6)
	v_mul_f32_e32 v18, 0x43800000, v22
	v_mul_f32_e32 v36, 0x43800000, v56
	v_cvt_pk_fp8_f32 v38, v35, v36 op_sel:[0,0,1]
	v_mul_f32_e32 v35, 0x43800000, v45
	v_mul_f32_e32 v36, 0x43800000, v57
	v_cvt_pk_fp8_f32 v37, v35, v36 op_sel:[0,0,1]
	s_waitcnt vmcnt(5)
	v_mul_f32_e32 v22, 0x43800000, v26
	ds_write2_b32 v80, v62, v46 offset1:4
	ds_write2_b32 v80, v51, v39 offset0:17 offset1:21
	ds_write2_b32 v80, v50, v38 offset0:34 offset1:38
	ds_write2_b32 v80, v49, v37 offset0:51 offset1:55
	s_waitcnt vmcnt(4)
	v_mul_f32_e32 v26, 0x43800000, v30
	v_mov_b32_e32 v30, v67
	v_cvt_pk_fp8_f32 v30, v0, v18
	v_mul_f32_e32 v0, 0x43800000, v19
	v_mul_f32_e32 v18, 0x43800000, v23
	v_mov_b32_e32 v23, v67
	v_cvt_pk_fp8_f32 v23, v0, v18
	v_cvt_pk_fp8_f32 v30, v22, v26 op_sel:[0,0,1]
	v_mul_f32_e32 v19, 0x43800000, v27
	v_mul_f32_e32 v22, 0x43800000, v31
	v_cvt_pk_fp8_f32 v23, v19, v22 op_sel:[0,0,1]
	v_mul_f32_e32 v0, 0x43800000, v20
	v_mul_f32_e32 v18, 0x43800000, v24
	v_mov_b32_e32 v22, v67
	v_cvt_pk_fp8_f32 v22, v0, v18
	v_mul_f32_e32 v0, 0x43800000, v21
	v_mul_f32_e32 v18, 0x43800000, v25
	v_mov_b32_e32 v21, v67
	v_cvt_pk_fp8_f32 v21, v0, v18
	s_waitcnt vmcnt(3)
	v_mul_f32_e32 v0, 0x43800000, v2
	s_waitcnt vmcnt(2)
	v_mul_f32_e32 v2, 0x43800000, v6
	s_waitcnt vmcnt(1)
	v_mul_f32_e32 v6, 0x43800000, v10
	s_waitcnt vmcnt(0)
	v_mul_f32_e32 v10, 0x43800000, v14
	v_mov_b32_e32 v14, v67
	v_cvt_pk_fp8_f32 v14, v0, v2
	v_mul_f32_e32 v0, 0x43800000, v3
	v_mul_f32_e32 v2, 0x43800000, v7
	v_mov_b32_e32 v7, v67
	v_cvt_pk_fp8_f32 v7, v0, v2
	v_cvt_pk_fp8_f32 v14, v6, v10 op_sel:[0,0,1]
	v_mul_f32_e32 v3, 0x43800000, v11
	v_mul_f32_e32 v6, 0x43800000, v15
	v_cvt_pk_fp8_f32 v7, v3, v6 op_sel:[0,0,1]
	v_mul_f32_e32 v0, 0x43800000, v4
	v_mul_f32_e32 v2, 0x43800000, v8
	v_mov_b32_e32 v6, v67
	v_cvt_pk_fp8_f32 v6, v0, v2
	v_mul_f32_e32 v0, 0x43800000, v5
	v_mul_f32_e32 v2, 0x43800000, v9
	v_mov_b32_e32 v5, v67
	v_cvt_pk_fp8_f32 v5, v0, v2
	v_mul_f32_e32 v19, 0x43800000, v28
	v_mul_f32_e32 v20, 0x43800000, v32
	v_mul_f32_e32 v3, 0x43800000, v12
	v_mul_f32_e32 v4, 0x43800000, v16
	v_cvt_pk_fp8_f32 v22, v19, v20 op_sel:[0,0,1]
	v_mul_f32_e32 v19, 0x43800000, v29
	v_mul_f32_e32 v20, 0x43800000, v33
	v_cvt_pk_fp8_f32 v6, v3, v4 op_sel:[0,0,1]
	v_mul_f32_e32 v3, 0x43800000, v13
	v_mul_f32_e32 v4, 0x43800000, v17
	v_cvt_pk_fp8_f32 v21, v19, v20 op_sel:[0,0,1]
	v_cvt_pk_fp8_f32 v5, v3, v4 op_sel:[0,0,1]
	ds_write2_b32 v80, v30, v14 offset0:8 offset1:12
	ds_write2_b32 v80, v23, v7 offset0:25 offset1:29
	ds_write2_b32 v80, v22, v6 offset0:42 offset1:46
	ds_write2_b32 v80, v21, v5 offset0:59 offset1:63
	s_waitcnt lgkmcnt(0)
	v_lshl_add_u64 v[2:3], v[72:73], 0, v[74:75]
	v_lshl_add_u64 v[6:7], v[2:3], 0, v[68:69]
	ds_read2_b32 v[2:3], v89 offset1:1
	ds_read2_b32 v[4:5], v89 offset0:2 offset1:3
	v_or_b32_e32 v0, v76, v81
	v_lshlrev_b32_e32 v66, 10, v0
	v_lshl_add_u64 v[8:9], v[6:7], 0, v[66:67]
	v_or_b32_e32 v0, v76, v82
	s_waitcnt lgkmcnt(0)
	global_store_dwordx4 v[8:9], v[2:5], off
	ds_read2_b32 v[2:3], v90 offset1:1
	ds_read2_b32 v[4:5], v91 offset1:1
	v_lshlrev_b32_e32 v66, 10, v0
	v_lshl_add_u64 v[8:9], v[6:7], 0, v[66:67]
	v_or_b32_e32 v0, v76, v83
	v_lshlrev_b32_e32 v66, 10, v0
	s_waitcnt lgkmcnt(0)
	global_store_dwordx4 v[8:9], v[2:5], off
	ds_read2_b32 v[2:3], v92 offset1:1
	ds_read2_b32 v[4:5], v93 offset1:1
	v_lshl_add_u64 v[8:9], v[6:7], 0, v[66:67]
	v_or_b32_e32 v0, v76, v84
	v_lshlrev_b32_e32 v66, 10, v0
	v_lshl_add_u64 v[6:7], v[6:7], 0, v[66:67]
	s_waitcnt lgkmcnt(0)
	global_store_dwordx4 v[8:9], v[2:5], off
	ds_read2_b32 v[2:3], v94 offset1:1
	ds_read2_b32 v[4:5], v95 offset1:1
	s_waitcnt lgkmcnt(0)
	global_store_dwordx4 v[6:7], v[2:5], off
	s_waitcnt lgkmcnt(0)
.LBB0_957:
	s_andn2_saveexec_b64 s[24:25], s[24:25]
	s_cbranch_execz .LBB0_959
	v_cmp_lt_u32_e64 s[6:7], s76, v4
	v_cndmask_b32_e32 v66, v100, v101, vcc
	s_waitcnt vmcnt(2)
	v_lshl_add_u64 v[6:7], s[0:1], 0, v[66:67]
	v_cndmask_b32_e64 v5, 0, 1, s[6:7]
	v_lshlrev_b32_e32 v66, 3, v5
	v_lshl_add_u64 v[6:7], v[6:7], 0, v[66:67]
	global_load_dwordx2 v[6:7], v[6:7], off
	v_cndmask_b32_e64 v0, v98, v99, s[6:7]
	v_add_u32_e32 v0, v0, v4
	v_lshrrev_b32_e32 v4, 9, v0
	v_mov_b32_e32 v5, v67
	v_lshlrev_b64 v[8:9], 23, v[4:5]
	v_mov_b32_e32 v10, s42
	v_lshlrev_b64 v[4:5], 22, v[4:5]
	v_lshlrev_b32_e32 v3, 6, v0
	v_and_b32_e32 v3, 64, v3
	v_mov_b32_e32 v71, v67
	s_waitcnt vmcnt(0)
	v_lshl_add_u64 v[6:7], v[6:7], 0, v[8:9]
	v_mov_b32_e32 v8, s41
	v_mov_b32_e32 v9, s43
	v_cndmask_b32_e32 v9, v8, v9, vcc
	v_mov_b32_e32 v8, s40
	v_cndmask_b32_e32 v8, v8, v10, vcc
	v_lshl_add_u64 v[50:51], v[8:9], 0, v[4:5]
	v_lshlrev_b32_e32 v4, 2, v0
	v_and_b32_e32 v52, 0x7c0, v4
	v_lshlrev_b32_e32 v4, 7, v0
	v_lshlrev_b32_e32 v0, 8, v0
	v_and_b32_e32 v4, 0x700, v4
	v_cndmask_b32_e64 v5, 0, v102, s[6:7]
	v_and_b32_e32 v66, 0xf00, v0
	v_or3_b32 v54, v3, v5, v4
	v_and_or_b32 v4, v2, s77, v78
	v_lshl_add_u64 v[2:3], v[6:7], 0, v[66:67]
	v_lshl_add_u64 v[2:3], v[2:3], 0, v[70:71]
	v_lshlrev_b32_e32 v66, 14, v4
	v_lshl_add_u64 v[10:11], v[2:3], 0, v[66:67]
	v_add_co_u32_e64 v2, s[6:7], s4, v10
	global_load_dwordx4 v[56:59], v[10:11], off nt
	s_nop 0
	v_addc_co_u32_e64 v3, s[6:7], 0, v11, s[6:7]
	global_load_dwordx4 v[60:63], v[2:3], off offset:-4096 nt
	global_load_dwordx4 v[72:75], v[2:3], off nt
	v_add_co_u32_e64 v2, s[6:7], s78, v10
	s_nop 1
	v_addc_co_u32_e64 v3, s[6:7], 0, v11, s[6:7]
	global_load_dwordx4 v[108:111], v[2:3], off nt
	v_add_co_u32_e64 v2, s[6:7], s79, v10
	s_nop 1
	v_addc_co_u32_e64 v3, s[6:7], 0, v11, s[6:7]
	global_load_dwordx4 v[34:37], v[2:3], off offset:-4096 nt
	global_load_dwordx4 v[38:41], v[2:3], off nt
	v_add_co_u32_e64 v2, s[6:7], s80, v10
	s_nop 0
	s_nop 0
	v_addc_co_u32_e64 v3, s[6:7], 0, v11, s[6:7]
	global_load_dwordx4 v[42:45], v[2:3], off offset:-4096 nt
	global_load_dwordx4 v[46:49], v[2:3], off nt
	v_add_co_u32_e64 v2, s[6:7], s81, v10
	s_nop 0
	s_nop 0
	v_addc_co_u32_e64 v3, s[6:7], 0, v11, s[6:7]
	global_load_dwordx4 v[18:21], v[2:3], off offset:-4096 nt
	global_load_dwordx4 v[22:25], v[2:3], off nt
	v_add_co_u32_e64 v2, s[6:7], s82, v10
	s_nop 0
	s_nop 0
	v_addc_co_u32_e64 v3, s[6:7], 0, v11, s[6:7]
	global_load_dwordx4 v[26:29], v[2:3], off offset:-4096 nt
	global_load_dwordx4 v[30:33], v[2:3], off nt
	v_add_co_u32_e64 v6, s[6:7], s83, v10
	s_nop 0
	s_nop 0
	v_addc_co_u32_e64 v7, s[6:7], 0, v11, s[6:7]
	v_add_co_u32_e64 v14, s[6:7], s84, v10
	global_load_dwordx4 v[2:5], v[6:7], off offset:-4096 nt
	s_nop 0
	global_load_dwordx4 v[6:9], v[6:7], off nt
	v_addc_co_u32_e64 v15, s[6:7], 0, v11, s[6:7]
	global_load_dwordx4 v[10:13], v[14:15], off offset:-4096 nt
	s_nop 0
	global_load_dwordx4 v[14:17], v[14:15], off nt
	s_waitcnt vmcnt(15)
; #define LAS __attribute__((address_space(3)))
; __device__ __forceinline__ unsigned pk4_fp8(float a, float b, float c, float d) { unsigned w = 0u; w = __builtin_amdgcn_cvt_pk_fp8_f32(a, b, w, false); w = __builtin_amdgcn_cvt_pk_fp8_f32(c, d, w, true); return w; }
; __device__ __forceinline__ void conv_item8(const float* W, int K, int N, unsigned char* WT, int k0, int n0, int drow0, LAS unsigned* scr, int lane, float sc, bool rperm = false) {
;     ...
;     for (int i = 0; i < 4; ++i) { const int rp = 4 * i + q; LAS unsigned* sp = scr + (4 * n4) * 17 + rp;
;         sp[0]  = pk4_fp8(v[i][0].x * sc, v[i][1].x * sc, v[i][2].x * sc, v[i][3].x * sc);
;         sp[17] = pk4_fp8(v[i][0].y * sc, v[i][1].y * sc, v[i][2].y * sc, v[i][3].y * sc);
;         sp[34] = pk4_fp8(v[i][0].z * sc, v[i][1].z * sc, v[i][2].z * sc, v[i][3].z * sc);
;         sp[51] = pk4_fp8(v[i][0].w * sc, v[i][1].w * sc, v[i][2].w * sc, v[i][3].w * sc); }
;     asm volatile("s_waitcnt lgkmcnt(0)" ::: "memory");
;     const int c = lane & 3;
; #pragma unroll
;     for (int j = 0; j < 4; ++j) {
;         const int n = (lane >> 2) + 16 * j; const LAS unsigned* sp = scr + n * 17 + 4 * c;
;         u32x4 o; o.x = sp[0]; o.y = sp[1]; o.z = sp[2]; o.w = sp[3];
;         const int nr = (rperm && n < 32) ? ((n < 16) ? 2 * n : 2 * (n - 16) + 1) : n;
;         *(u32x4*)(WT + (size_t)(drow0 + nr) * K + k0 + 16 * c) = o;
;     }
	v_mul_f32_e32 v0, 0x43800000, v56
	s_waitcnt vmcnt(14)
	v_mul_f32_e32 v53, 0x43800000, v60
	v_mov_b32_e32 v60, v67
	v_cvt_pk_fp8_f32 v60, v0, v53
	v_mul_f32_e32 v0, 0x43800000, v57
	v_mul_f32_e32 v53, 0x43800000, v61
	v_mov_b32_e32 v57, v67
	v_cvt_pk_fp8_f32 v57, v0, v53
	v_mul_f32_e32 v0, 0x43800000, v58
	v_mul_f32_e32 v53, 0x43800000, v62
	v_mov_b32_e32 v58, v67
	v_cvt_pk_fp8_f32 v58, v0, v53
	v_mul_f32_e32 v0, 0x43800000, v59
	v_mul_f32_e32 v53, 0x43800000, v63
	v_mov_b32_e32 v59, v67
	v_cvt_pk_fp8_f32 v59, v0, v53
	s_waitcnt vmcnt(13)
	v_mul_f32_e32 v55, 0x43800000, v72
	v_mov_b32_e32 v53, v67
	s_waitcnt vmcnt(12)
	v_mul_f32_e32 v56, 0x43800000, v108
	v_cvt_pk_fp8_f32 v60, v55, v56 op_sel:[0,0,1]
	v_mul_f32_e32 v55, 0x43800000, v73
	v_mul_f32_e32 v56, 0x43800000, v109
	v_cvt_pk_fp8_f32 v57, v55, v56 op_sel:[0,0,1]
	s_waitcnt vmcnt(11)
	v_mul_f32_e32 v0, 0x43800000, v34
	s_waitcnt vmcnt(10)
	v_mul_f32_e32 v34, 0x43800000, v38
	v_mul_f32_e32 v55, 0x43800000, v74
	v_mul_f32_e32 v56, 0x43800000, v110
	v_cvt_pk_fp8_f32 v58, v55, v56 op_sel:[0,0,1]
	v_mul_f32_e32 v55, 0x43800000, v75
	s_waitcnt vmcnt(9)
	v_mul_f32_e32 v38, 0x43800000, v42
	s_waitcnt vmcnt(8)
	v_mul_f32_e32 v42, 0x43800000, v46
	v_mov_b32_e32 v46, v67
	v_cvt_pk_fp8_f32 v46, v0, v34
	v_mul_f32_e32 v0, 0x43800000, v35
	v_mul_f32_e32 v34, 0x43800000, v39
	v_mov_b32_e32 v39, v67
	v_cvt_pk_fp8_f32 v39, v0, v34
	v_cvt_pk_fp8_f32 v46, v38, v42 op_sel:[0,0,1]
	v_mul_f32_e32 v35, 0x43800000, v43
	v_mul_f32_e32 v38, 0x43800000, v47
	v_cvt_pk_fp8_f32 v39, v35, v38 op_sel:[0,0,1]
	v_mul_f32_e32 v0, 0x43800000, v36
	v_mul_f32_e32 v34, 0x43800000, v40
	v_mov_b32_e32 v38, v67
	v_cvt_pk_fp8_f32 v38, v0, v34
	v_mul_f32_e32 v0, 0x43800000, v37
	v_mul_f32_e32 v34, 0x43800000, v41
	v_mov_b32_e32 v37, v67
	v_cvt_pk_fp8_f32 v37, v0, v34
	s_waitcnt vmcnt(7)
	v_mul_f32_e32 v0, 0x43800000, v18
	s_waitcnt vmcnt(6)
	v_mul_f32_e32 v18, 0x43800000, v22
	s_waitcnt vmcnt(5)
	v_mul_f32_e32 v22, 0x43800000, v26
	s_waitcnt vmcnt(4)
	v_mul_f32_e32 v26, 0x43800000, v30
	v_mov_b32_e32 v30, v67
	v_cvt_pk_fp8_f32 v30, v0, v18
	v_mul_f32_e32 v0, 0x43800000, v19
	v_mul_f32_e32 v18, 0x43800000, v23
	v_mov_b32_e32 v23, v67
	v_cvt_pk_fp8_f32 v23, v0, v18
	v_cvt_pk_fp8_f32 v30, v22, v26 op_sel:[0,0,1]
	v_mul_f32_e32 v19, 0x43800000, v27
	v_mul_f32_e32 v22, 0x43800000, v31
	v_cvt_pk_fp8_f32 v23, v19, v22 op_sel:[0,0,1]
	v_mul_f32_e32 v0, 0x43800000, v20
	v_mul_f32_e32 v18, 0x43800000, v24
	v_mov_b32_e32 v22, v67
	v_cvt_pk_fp8_f32 v22, v0, v18
	v_mul_f32_e32 v0, 0x43800000, v21
	v_mul_f32_e32 v18, 0x43800000, v25
	v_mov_b32_e32 v21, v67
	v_cvt_pk_fp8_f32 v21, v0, v18
	s_waitcnt vmcnt(3)
	v_mul_f32_e32 v0, 0x43800000, v2
	s_waitcnt vmcnt(2)
	v_mul_f32_e32 v2, 0x43800000, v6
	s_waitcnt vmcnt(1)
	v_mul_f32_e32 v6, 0x43800000, v10
	s_waitcnt vmcnt(0)
	v_mul_f32_e32 v10, 0x43800000, v14
	v_mov_b32_e32 v14, v67
	v_cvt_pk_fp8_f32 v14, v0, v2
	v_mul_f32_e32 v0, 0x43800000, v3
	v_mul_f32_e32 v2, 0x43800000, v7
	v_mov_b32_e32 v7, v67
	v_cvt_pk_fp8_f32 v7, v0, v2
	v_cvt_pk_fp8_f32 v14, v6, v10 op_sel:[0,0,1]
	v_mul_f32_e32 v3, 0x43800000, v11
	v_mul_f32_e32 v6, 0x43800000, v15
	v_cvt_pk_fp8_f32 v7, v3, v6 op_sel:[0,0,1]
	v_mul_f32_e32 v0, 0x43800000, v4
	v_mul_f32_e32 v2, 0x43800000, v8
	v_mov_b32_e32 v6, v67
	v_cvt_pk_fp8_f32 v6, v0, v2
	v_mul_f32_e32 v0, 0x43800000, v5
	v_mul_f32_e32 v2, 0x43800000, v9
	v_mov_b32_e32 v5, v67
	v_cvt_pk_fp8_f32 v5, v0, v2
	v_mul_f32_e32 v35, 0x43800000, v44
	v_mul_f32_e32 v36, 0x43800000, v48
	v_mul_f32_e32 v19, 0x43800000, v28
	v_mul_f32_e32 v20, 0x43800000, v32
	v_mul_f32_e32 v3, 0x43800000, v12
	v_mul_f32_e32 v4, 0x43800000, v16
	v_mul_f32_e32 v56, 0x43800000, v111
	v_cvt_pk_fp8_f32 v38, v35, v36 op_sel:[0,0,1]
	v_mul_f32_e32 v35, 0x43800000, v45
	v_mul_f32_e32 v36, 0x43800000, v49
	v_cvt_pk_fp8_f32 v22, v19, v20 op_sel:[0,0,1]
	v_mul_f32_e32 v19, 0x43800000, v29
	v_mul_f32_e32 v20, 0x43800000, v33
	v_cvt_pk_fp8_f32 v6, v3, v4 op_sel:[0,0,1]
	v_mul_f32_e32 v3, 0x43800000, v13
	v_mul_f32_e32 v4, 0x43800000, v17
	v_cvt_pk_fp8_f32 v59, v55, v56 op_sel:[0,0,1]
	v_cvt_pk_fp8_f32 v37, v35, v36 op_sel:[0,0,1]
	v_cvt_pk_fp8_f32 v21, v19, v20 op_sel:[0,0,1]
	v_cvt_pk_fp8_f32 v5, v3, v4 op_sel:[0,0,1]
	ds_write2_b32 v80, v60, v46 offset1:4
	ds_write2_b32 v80, v57, v39 offset0:17 offset1:21
	ds_write2_b32 v80, v58, v38 offset0:34 offset1:38
	ds_write2_b32 v80, v59, v37 offset0:51 offset1:55
	ds_write2_b32 v80, v30, v14 offset0:8 offset1:12
	ds_write2_b32 v80, v23, v7 offset0:25 offset1:29
	ds_write2_b32 v80, v22, v6 offset0:42 offset1:46
	ds_write2_b32 v80, v21, v5 offset0:59 offset1:63
	s_waitcnt lgkmcnt(0)
	v_lshl_add_u64 v[2:3], v[50:51], 0, v[52:53]
	v_lshl_add_u64 v[6:7], v[2:3], 0, v[68:69]
	ds_read2_b32 v[2:3], v89 offset1:1
	ds_read2_b32 v[4:5], v89 offset0:2 offset1:3
	v_or_b32_e32 v0, v54, v81
	v_lshlrev_b32_e32 v66, 11, v0
	v_lshl_add_u64 v[8:9], v[6:7], 0, v[66:67]
	v_or_b32_e32 v0, v54, v82
	s_waitcnt lgkmcnt(0)
	global_store_dwordx4 v[8:9], v[2:5], off
	ds_read2_b32 v[2:3], v90 offset1:1
	ds_read2_b32 v[4:5], v91 offset1:1
	v_lshlrev_b32_e32 v66, 11, v0
	v_lshl_add_u64 v[8:9], v[6:7], 0, v[66:67]
	v_or_b32_e32 v0, v54, v83
	v_lshlrev_b32_e32 v66, 11, v0
	s_waitcnt lgkmcnt(0)
	global_store_dwordx4 v[8:9], v[2:5], off
	ds_read2_b32 v[2:3], v92 offset1:1
	ds_read2_b32 v[4:5], v93 offset1:1
	v_lshl_add_u64 v[8:9], v[6:7], 0, v[66:67]
	v_or_b32_e32 v0, v54, v84
	v_lshlrev_b32_e32 v66, 11, v0
	v_lshl_add_u64 v[6:7], v[6:7], 0, v[66:67]
	s_waitcnt lgkmcnt(0)
	global_store_dwordx4 v[8:9], v[2:5], off
	ds_read2_b32 v[2:3], v94 offset1:1
	ds_read2_b32 v[4:5], v95 offset1:1
	s_waitcnt lgkmcnt(0)
	global_store_dwordx4 v[6:7], v[2:5], off
	s_waitcnt lgkmcnt(0)

; __device__ __forceinline__ void conv_item8(const float* W, int K, int N, unsigned char* WT, int k0, int n0, int drow0, LAS unsigned* scr, int lane, float sc, bool rperm = false) {
;     const int q = lane >> 4, n4 = lane & 15;
;     f32x4 v[4][4];
; #pragma unroll
;     for (int i = 0; i < 4; ++i)
; #pragma unroll
;         for (int t = 0; t < 4; ++t) v[i][t] = __builtin_nontemporal_load((const f32x4*)(W + (size_t)(k0 + 4 * (4 * i + q) + t) * N + n0 + 4 * n4));
; __device__ __forceinline__ void conv_dispatch(const Params& p, int it, LAS unsigned* scr, int lane) {
;     ...
;     int r = it; const int l = (r >= I_L0) ? 1 : 0; if (l) r -= I_L0;
;     const int i_in = l ? I_IN1 : I_IN0;
;     if (r < i_in) { const int N = l ? ODW : EVW, nb = N / 64;
;         conv_item8(p.in[l ? 16 : 5], D, N, l ? p.wp[IX_WIN1] : p.wp[IX_WIN0], (r / nb) * 64, (r % nb) * 64, (r % nb) * 64, scr, lane, F8_SW, l == 1 && (r % nb) < 64 && ((r % nb) & 1) == 0);
.LBB0_963:
	s_andn2_saveexec_b64 s[22:23], s[8:9]
	s_cbranch_execz .LBB0_952
	v_cndmask_b32_e32 v66, 40, v102, vcc
	v_lshl_add_u64 v[4:5], s[0:1], 0, v[66:67]
	global_load_dwordx2 v[4:5], v[4:5], off
	v_cndmask_b32_e32 v16, v105, v106, vcc
	v_lshrrev_b32_e32 v0, 6, v16
	s_waitcnt vmcnt(3)
	v_sub_u32_e32 v7, 0, v0
	v_max_i32_e32 v7, v0, v7
	v_cvt_f32_u32_e32 v8, v7
	v_mov_b32_e32 v3, s45
	v_mov_b32_e32 v6, s47
	v_sub_u32_e32 v9, 0, v7
	v_rcp_iflag_f32_e32 v8, v8
	v_cndmask_b32_e32 v73, v3, v6, vcc
	v_mov_b32_e32 v3, s44
	v_mov_b32_e32 v6, s46
	v_mul_f32_e32 v8, 0x4f7ffffe, v8
	v_cvt_u32_f32_e32 v8, v8
	v_cndmask_b32_e32 v72, v3, v6, vcc
	v_sub_u32_e32 v6, 0, v2
	v_max_i32_e32 v6, v2, v6
	v_mul_lo_u32 v9, v9, v8
	v_mul_hi_u32 v9, v8, v9
	v_add_u32_e32 v8, v8, v9
	v_mul_hi_u32 v8, v6, v8
	v_mul_lo_u32 v9, v8, v7
	v_sub_u32_e32 v6, v6, v9
	v_cmp_ge_u32_e64 s[6:7], v6, v7
	v_add_u32_e32 v9, 1, v8
	v_xor_b32_e32 v3, v2, v0
	v_cndmask_b32_e64 v8, v8, v9, s[6:7]
	v_sub_u32_e32 v9, v6, v7
	v_cndmask_b32_e64 v6, v6, v9, s[6:7]
	v_cmp_ge_u32_e64 s[6:7], v6, v7
	v_add_u32_e32 v6, 1, v8
	v_ashrrev_i32_e32 v3, 31, v3
	v_cndmask_b32_e64 v6, v8, v6, s[6:7]
	v_xor_b32_e32 v6, v6, v3
	v_sub_u32_e32 v3, v6, v3
	v_mul_lo_u32 v0, v3, v0
	v_sub_u32_e32 v0, v2, v0
	v_lshlrev_b32_e32 v76, 6, v3
	v_lshlrev_b32_e32 v74, 6, v0
	v_cmp_gt_i32_e64 s[6:7], 64, v0
	v_and_b32_e32 v0, 1, v0
	v_cmp_eq_u32_e64 s[8:9], 0, v0
	v_or_b32_e32 v0, v76, v79
	v_ashrrev_i32_e32 v75, 31, v74
	s_and_b64 s[6:7], s[6:7], s[8:9]
	v_mov_b32_e32 v71, v67
	v_or_b32_e32 v6, 49, v0
	s_and_b64 vcc, vcc, s[6:7]
	v_mad_i64_i32 v[6:7], s[6:7], v6, v16, 0
	v_or_b32_e32 v10, 50, v0
	v_mad_i64_i32 v[10:11], s[6:7], v10, v16, 0
	v_ashrrev_i32_e32 v77, 31, v76
	s_waitcnt vmcnt(0)
	v_lshl_add_u64 v[2:3], v[74:75], 2, v[4:5]
	v_lshl_add_u64 v[14:15], v[2:3], 0, v[70:71]
	v_mad_i64_i32 v[2:3], s[6:7], v0, v16, 0
	v_lshl_add_u64 v[2:3], v[2:3], 2, v[14:15]
	v_lshl_add_u64 v[6:7], v[6:7], 2, v[14:15]
	global_load_dwordx4 v[50:53], v[2:3], off nt
	v_lshl_add_u64 v[10:11], v[10:11], 2, v[14:15]
	global_load_dwordx4 v[6:9], v[6:7], off nt
	v_or_b32_e32 v2, 1, v0
	v_mad_i64_i32 v[2:3], s[6:7], v2, v16, 0
	v_lshl_add_u64 v[2:3], v[2:3], 2, v[14:15]
	global_load_dwordx4 v[54:57], v[2:3], off nt
	s_nop 0
	global_load_dwordx4 v[10:13], v[10:11], off nt
	v_or_b32_e32 v2, 2, v0
	v_mad_i64_i32 v[2:3], s[6:7], v2, v16, 0
	v_lshl_add_u64 v[2:3], v[2:3], 2, v[14:15]
	global_load_dwordx4 v[58:61], v[2:3], off nt
	v_or_b32_e32 v2, 3, v0
	v_mad_i64_i32 v[2:3], s[6:7], v2, v16, 0
	v_lshl_add_u64 v[2:3], v[2:3], 2, v[14:15]
	global_load_dwordx4 v[62:65], v[2:3], off nt
	v_or_b32_e32 v2, 16, v0
	v_mad_i64_i32 v[2:3], s[6:7], v2, v16, 0
	v_lshl_add_u64 v[2:3], v[2:3], 2, v[14:15]
	global_load_dwordx4 v[18:21], v[2:3], off nt
	v_or_b32_e32 v2, 17, v0
	v_mad_i64_i32 v[2:3], s[6:7], v2, v16, 0
	v_lshl_add_u64 v[2:3], v[2:3], 2, v[14:15]
	global_load_dwordx4 v[22:25], v[2:3], off nt
	v_or_b32_e32 v2, 18, v0
	v_mad_i64_i32 v[2:3], s[6:7], v2, v16, 0
	v_lshl_add_u64 v[2:3], v[2:3], 2, v[14:15]
	global_load_dwordx4 v[26:29], v[2:3], off nt
	v_or_b32_e32 v2, 19, v0
	v_mad_i64_i32 v[2:3], s[6:7], v2, v16, 0
	v_lshl_add_u64 v[2:3], v[2:3], 2, v[14:15]
	global_load_dwordx4 v[46:49], v[2:3], off nt
	v_or_b32_e32 v2, 32, v0
	v_mad_i64_i32 v[2:3], s[6:7], v2, v16, 0
	v_lshl_add_u64 v[2:3], v[2:3], 2, v[14:15]
	global_load_dwordx4 v[30:33], v[2:3], off nt
	v_or_b32_e32 v2, 33, v0
	v_mad_i64_i32 v[2:3], s[6:7], v2, v16, 0
	v_lshl_add_u64 v[2:3], v[2:3], 2, v[14:15]
	global_load_dwordx4 v[34:37], v[2:3], off nt
	v_or_b32_e32 v2, 34, v0
	v_mad_i64_i32 v[2:3], s[6:7], v2, v16, 0
	v_lshl_add_u64 v[2:3], v[2:3], 2, v[14:15]
	global_load_dwordx4 v[38:41], v[2:3], off nt
	v_or_b32_e32 v2, 35, v0
	v_mad_i64_i32 v[2:3], s[6:7], v2, v16, 0
	v_lshl_add_u64 v[2:3], v[2:3], 2, v[14:15]
	global_load_dwordx4 v[42:45], v[2:3], off nt
	v_or_b32_e32 v2, 48, v0
	v_or_b32_e32 v0, 51, v0
	v_mad_i64_i32 v[2:3], s[6:7], v2, v16, 0
	v_mad_i64_i32 v[16:17], s[6:7], v0, v16, 0
	v_lshl_add_u64 v[2:3], v[2:3], 2, v[14:15]
	v_lshl_add_u64 v[14:15], v[16:17], 2, v[14:15]
	global_load_dwordx4 v[2:5], v[2:3], off nt
	global_load_dwordx4 v[14:17], v[14:15], off nt
	s_waitcnt vmcnt(15)
	v_mul_f32_e32 v0, 0x43800000, v50
	s_waitcnt vmcnt(13)
	v_mul_f32_e32 v50, 0x43800000, v54
	s_waitcnt vmcnt(11)
	v_mul_f32_e32 v54, 0x43800000, v58
	s_waitcnt vmcnt(10)
	v_mul_f32_e32 v58, 0x43800000, v62
	v_mov_b32_e32 v62, v67
	v_cvt_pk_fp8_f32 v62, v0, v50
	v_mul_f32_e32 v0, 0x43800000, v51
	v_mul_f32_e32 v50, 0x43800000, v55
	v_mov_b32_e32 v55, v67
	v_cvt_pk_fp8_f32 v55, v0, v50
	v_cvt_pk_fp8_f32 v62, v54, v58 op_sel:[0,0,1]
	v_mul_f32_e32 v51, 0x43800000, v59
	v_mul_f32_e32 v54, 0x43800000, v63
	v_cvt_pk_fp8_f32 v55, v51, v54 op_sel:[0,0,1]
	v_mul_f32_e32 v0, 0x43800000, v52
	v_mul_f32_e32 v50, 0x43800000, v56
	v_mov_b32_e32 v54, v67
	v_cvt_pk_fp8_f32 v54, v0, v50
	v_mul_f32_e32 v0, 0x43800000, v53
	v_mul_f32_e32 v50, 0x43800000, v57
	v_mov_b32_e32 v53, v67
	v_cvt_pk_fp8_f32 v53, v0, v50
	s_waitcnt vmcnt(9)
; #define LAS __attribute__((address_space(3)))
; __device__ __forceinline__ unsigned pk4_fp8(float a, float b, float c, float d) { unsigned w = 0u; w = __builtin_amdgcn_cvt_pk_fp8_f32(a, b, w, false); w = __builtin_amdgcn_cvt_pk_fp8_f32(c, d, w, true); return w; }
; __device__ __forceinline__ void conv_item8(const float* W, int K, int N, unsigned char* WT, int k0, int n0, int drow0, LAS unsigned* scr, int lane, float sc, bool rperm = false) {
;     ...
;     for (int i = 0; i < 4; ++i) { const int rp = 4 * i + q; LAS unsigned* sp = scr + (4 * n4) * 17 + rp;
;         sp[0]  = pk4_fp8(v[i][0].x * sc, v[i][1].x * sc, v[i][2].x * sc, v[i][3].x * sc);
;         sp[17] = pk4_fp8(v[i][0].y * sc, v[i][1].y * sc, v[i][2].y * sc, v[i][3].y * sc);
;         sp[34] = pk4_fp8(v[i][0].z * sc, v[i][1].z * sc, v[i][2].z * sc, v[i][3].z * sc);
;         sp[51] = pk4_fp8(v[i][0].w * sc, v[i][1].w * sc, v[i][2].w * sc, v[i][3].w * sc); }
;     asm volatile("s_waitcnt lgkmcnt(0)" ::: "memory");
;     const int c = lane & 3;
; #pragma unroll
;     for (int j = 0; j < 4; ++j) {
;         const int n = (lane >> 2) + 16 * j; const LAS unsigned* sp = scr + n * 17 + 4 * c;
;         u32x4 o; o.x = sp[0]; o.y = sp[1]; o.z = sp[2]; o.w = sp[3];
;         const int nr = (rperm && n < 32) ? ((n < 16) ? 2 * n : 2 * (n - 16) + 1) : n;
;         *(u32x4*)(WT + (size_t)(drow0 + nr) * K + k0 + 16 * c) = o;
;     }
	v_mul_f32_e32 v0, 0x43800000, v18
	s_waitcnt vmcnt(8)
	v_mul_f32_e32 v18, 0x43800000, v22
	s_waitcnt vmcnt(7)
	v_mul_f32_e32 v22, 0x43800000, v26
	s_waitcnt vmcnt(6)
	v_mul_f32_e32 v26, 0x43800000, v46
	v_mov_b32_e32 v46, v67
	v_cvt_pk_fp8_f32 v46, v0, v18
	v_mul_f32_e32 v0, 0x43800000, v19
	v_mul_f32_e32 v18, 0x43800000, v23
	v_mov_b32_e32 v23, v67
	v_cvt_pk_fp8_f32 v23, v0, v18
	v_cvt_pk_fp8_f32 v46, v22, v26 op_sel:[0,0,1]
	v_mul_f32_e32 v19, 0x43800000, v27
	v_mul_f32_e32 v22, 0x43800000, v47
	v_cvt_pk_fp8_f32 v23, v19, v22 op_sel:[0,0,1]
	v_mul_f32_e32 v0, 0x43800000, v20
	v_mul_f32_e32 v18, 0x43800000, v24
	v_mov_b32_e32 v22, v67
	v_cvt_pk_fp8_f32 v22, v0, v18
	v_mul_f32_e32 v0, 0x43800000, v21
	v_mul_f32_e32 v18, 0x43800000, v25
	v_mov_b32_e32 v21, v67
	v_cvt_pk_fp8_f32 v21, v0, v18
	v_mul_f32_e32 v51, 0x43800000, v60
	v_mul_f32_e32 v52, 0x43800000, v64
	v_mul_f32_e32 v19, 0x43800000, v28
	v_mul_f32_e32 v20, 0x43800000, v48
	v_cvt_pk_fp8_f32 v54, v51, v52 op_sel:[0,0,1]
	v_mul_f32_e32 v51, 0x43800000, v61
	v_mul_f32_e32 v52, 0x43800000, v65
	v_cvt_pk_fp8_f32 v22, v19, v20 op_sel:[0,0,1]
	v_mul_f32_e32 v19, 0x43800000, v29
	v_mul_f32_e32 v20, 0x43800000, v49
	v_cvt_pk_fp8_f32 v53, v51, v52 op_sel:[0,0,1]
	v_cvt_pk_fp8_f32 v21, v19, v20 op_sel:[0,0,1]
	s_waitcnt vmcnt(5)
	v_mul_f32_e32 v0, 0x43800000, v30
	s_waitcnt vmcnt(4)
	v_mul_f32_e32 v18, 0x43800000, v34
	ds_write2_b32 v80, v54, v22 offset0:34 offset1:38
	ds_write2_b32 v80, v53, v21 offset0:51 offset1:55
	v_mov_b32_e32 v21, v67
	v_cvt_pk_fp8_f32 v21, v0, v18
	v_mul_f32_e32 v0, 0x43800000, v31
	v_mul_f32_e32 v18, 0x43800000, v35
	v_mov_b32_e32 v22, v67
	ds_write2_b32 v80, v55, v23 offset0:17 offset1:21
	v_cvt_pk_fp8_f32 v22, v0, v18
	v_mul_f32_e32 v0, 0x43800000, v32
	v_mul_f32_e32 v18, 0x43800000, v36
	v_mov_b32_e32 v23, v67
	v_cvt_pk_fp8_f32 v23, v0, v18
	v_mul_f32_e32 v0, 0x43800000, v33
	v_mul_f32_e32 v18, 0x43800000, v37
	v_mov_b32_e32 v24, v67
	v_cvt_pk_fp8_f32 v24, v0, v18
	s_waitcnt vmcnt(1)
	v_mul_f32_e32 v0, 0x43800000, v2
	v_mul_f32_e32 v2, 0x43800000, v6
	v_mul_f32_e32 v6, 0x43800000, v10
	s_waitcnt vmcnt(0)
	v_mul_f32_e32 v10, 0x43800000, v14
	v_mov_b32_e32 v14, v67
	v_cvt_pk_fp8_f32 v14, v0, v2
	v_mul_f32_e32 v0, 0x43800000, v3
	v_mul_f32_e32 v2, 0x43800000, v7
	v_mov_b32_e32 v7, v67
	v_cvt_pk_fp8_f32 v7, v0, v2
	v_cvt_pk_fp8_f32 v14, v6, v10 op_sel:[0,0,1]
	v_mul_f32_e32 v3, 0x43800000, v11
	v_mul_f32_e32 v6, 0x43800000, v15
	v_cvt_pk_fp8_f32 v7, v3, v6 op_sel:[0,0,1]
	v_mul_f32_e32 v0, 0x43800000, v4
	v_mul_f32_e32 v2, 0x43800000, v8
	v_mov_b32_e32 v6, v67
	v_cvt_pk_fp8_f32 v6, v0, v2
	v_mul_f32_e32 v0, 0x43800000, v5
	v_mul_f32_e32 v2, 0x43800000, v9
	v_mov_b32_e32 v5, v67
	v_mul_f32_e32 v19, 0x43800000, v38
	v_mul_f32_e32 v20, 0x43800000, v42
	v_cvt_pk_fp8_f32 v5, v0, v2
	v_cvt_pk_fp8_f32 v21, v19, v20 op_sel:[0,0,1]
	v_mul_f32_e32 v19, 0x43800000, v39
	v_mul_f32_e32 v20, 0x43800000, v43
	v_cvt_pk_fp8_f32 v22, v19, v20 op_sel:[0,0,1]
	v_mul_f32_e32 v19, 0x43800000, v40
	v_mul_f32_e32 v20, 0x43800000, v44
	v_mul_f32_e32 v3, 0x43800000, v12
	v_mul_f32_e32 v4, 0x43800000, v16
	v_cvt_pk_fp8_f32 v23, v19, v20 op_sel:[0,0,1]
	v_mul_f32_e32 v19, 0x43800000, v41
	v_mul_f32_e32 v20, 0x43800000, v45
	v_cvt_pk_fp8_f32 v6, v3, v4 op_sel:[0,0,1]
	v_mul_f32_e32 v3, 0x43800000, v13
	v_mul_f32_e32 v4, 0x43800000, v17
	v_cvt_pk_fp8_f32 v24, v19, v20 op_sel:[0,0,1]
	v_cvt_pk_fp8_f32 v5, v3, v4 op_sel:[0,0,1]
	ds_write2_b32 v80, v62, v46 offset1:4
	ds_write2_b32 v80, v21, v14 offset0:8 offset1:12
	ds_write2_b32 v80, v22, v7 offset0:25 offset1:29
	ds_write2_b32 v80, v23, v6 offset0:42 offset1:46
	ds_write2_b32 v80, v24, v5 offset0:59 offset1:63
	s_waitcnt lgkmcnt(0)
	v_lshl_add_u64 v[2:3], v[72:73], 0, v[76:77]
	v_lshl_add_u64 v[6:7], v[2:3], 0, v[68:69]
	ds_read2_b32 v[2:3], v89 offset1:1
	ds_read2_b32 v[4:5], v89 offset0:2 offset1:3
	v_cndmask_b32_e64 v0, 0, 1, vcc
	v_lshl_or_b32 v8, v81, v0, v74
	v_ashrrev_i32_e32 v9, 31, v8
	v_lshlrev_b64 v[8:9], 11, v[8:9]
	v_lshl_add_u64 v[8:9], v[6:7], 0, v[8:9]
	s_waitcnt lgkmcnt(0)
	global_store_dwordx4 v[8:9], v[2:5], off
	ds_read2_b32 v[2:3], v90 offset1:1
	ds_read2_b32 v[4:5], v91 offset1:1
	v_cndmask_b32_e32 v0, v82, v85, vcc
	v_or_b32_e32 v8, v0, v74
	v_ashrrev_i32_e32 v9, 31, v8
	v_lshlrev_b64 v[8:9], 11, v[8:9]
	v_lshl_add_u64 v[8:9], v[6:7], 0, v[8:9]
	s_waitcnt lgkmcnt(0)
	global_store_dwordx4 v[8:9], v[2:5], off
	ds_read2_b32 v[2:3], v92 offset1:1
	ds_read2_b32 v[4:5], v93 offset1:1
	v_or_b32_e32 v8, v74, v83
	v_ashrrev_i32_e32 v9, 31, v8
	v_lshlrev_b64 v[8:9], 11, v[8:9]
	v_lshl_add_u64 v[8:9], v[6:7], 0, v[8:9]
	s_waitcnt lgkmcnt(0)
	global_store_dwordx4 v[8:9], v[2:5], off
	ds_read2_b32 v[2:3], v94 offset1:1
	ds_read2_b32 v[4:5], v95 offset1:1
	v_or_b32_e32 v8, v74, v84
	v_ashrrev_i32_e32 v9, 31, v8
	v_lshlrev_b64 v[8:9], 11, v[8:9]
	v_lshl_add_u64 v[6:7], v[6:7], 0, v[8:9]
	s_waitcnt lgkmcnt(0)
	global_store_dwordx4 v[6:7], v[2:5], off
	s_waitcnt lgkmcnt(0)
	s_branch .LBB0_952
